# xor-16 butterfly sum steps via v_permlane16_swap instead of ds_bpermute: layer-1 QKV epilogue row-norm and the routing wave sums
# baseline (speedup 1.0000x reference)
; #define LAS __attribute__((address_space(3)))
; __device__ __forceinline__ void phase_nrr(const Frame& F, const Args& a, int l, const bf16_t* XA, const float* g, const float* modl, unsigned char* XN8) {
;     ...
; #pragma unroll
;         for (int rb = 0; rb < 4; ++rb) *(LAS f32x4*)(Pl + (size_t)((kq * 64 + 16 * rb + fr) * NE + 16 * eb + 4 * fq)) = acc[rb];
;         __syncthreads();
;         const float bias = rbias[lane];
; #pragma unroll
;         for (int i = 0; i < 8; ++i) { const int t = tb + i;
;             const float lg = Pl[(w * 8 + i) * NE + lane] + Pl[(64 + w * 8 + i) * NE + lane]; const float sc = 1.f / (1.f + __expf(-lg)); const float bb = sc + bias;
;             float m1 = bb; m1 = fmaxf(m1, __shfl_xor(m1, 1)); m1 = fmaxf(m1, __shfl_xor(m1, 2)); m1 = fmaxf(m1, __shfl_xor(m1, 4));
;             const unsigned long long eq = __ballot(bb == m1); const int gbase = lane & ~7; const unsigned grpmask = (unsigned)((eq >> gbase) & 0xffull);
;             const int first = gbase + __builtin_ctz(grpmask);
;             float m2 = (lane == first) ? -INFINITY : bb; m2 = fmaxf(m2, __shfl_xor(m2, 1)); m2 = fmaxf(m2, __shfl_xor(m2, 2)); m2 = fmaxf(m2, __shfl_xor(m2, 4));
;             const float gsum = m1 + m2; const int gq = lane >> 3;
;             int grank = 0;
; #pragma unroll
;             for (int g2 = 0; g2 < 8; ++g2) { const float v = __int_as_float(__builtin_amdgcn_readlane(__float_as_int(gsum), g2 * 8)); grank += (v > gsum || (v == gsum && g2 < gq)) ? 1 : 0; }
;             const bool keep = grank < 4; const float val = keep ? bb : -INFINITY;
;             int rank = 0;
; #pragma unroll 8
;             for (int e2 = 0; e2 < 64; ++e2) { const float v = __int_as_float(__builtin_amdgcn_readlane(__float_as_int(val), e2)); rank += (v > val || (v == val && e2 < lane)) ? 1 : 0; }
.LBB0_535:
	s_barrier
	ds_write_b128 v242, v[110:113]
	ds_write_b128 v242, v[118:121] offset:4096
	s_nop 0
	ds_write_b128 v242, v[126:129] offset:8192
	s_nop 1
	ds_write_b128 v242, v[130:133] offset:12288
	s_waitcnt lgkmcnt(0)
	s_barrier
	global_load_dword v3, v[198:199], off
	s_waitcnt vmcnt(15)
	v_add_u32_e32 v4, s76, v226
	ds_read2st64_b32 v[6:7], v4 offset1:64
	s_mov_b32 s3, 0
	s_waitcnt lgkmcnt(0)
	v_add_f32_e32 v2, v6, v7
	v_mul_f32_e32 v2, 0xbfb8aa3b, v2
	v_exp_f32_e32 v2, v2
	s_nop 0
	v_add_f32_e32 v2, 1.0, v2
	v_div_scale_f32 v5, s[22:23], v2, v2, 1.0
	v_rcp_f32_e32 v6, v5
	s_nop 0
	v_fma_f32 v7, -v5, v6, 1.0
	v_fmac_f32_e32 v6, v7, v6
	v_div_scale_f32 v7, vcc, 1.0, v2, 1.0
	v_mul_f32_e32 v8, v7, v6
	v_fma_f32 v9, -v5, v8, v7
	v_fmac_f32_e32 v8, v9, v6
	v_fma_f32 v5, -v5, v8, v7
	v_div_fmas_f32 v5, v5, v6, v8
	v_div_fixup_f32 v2, v5, v2, 1.0
	s_waitcnt vmcnt(0)
	v_add_f32_e32 v5, v3, v2
	s_nop 1
	s_waitcnt lgkmcnt(0)
	v_max_f32_dpp v6, v5, v5 quad_perm:[1,0,3,2] row_mask:0xf bank_mask:0xf
	s_nop 1
	s_waitcnt lgkmcnt(0)
	v_max_f32_dpp v6, v6, v6 quad_perm:[2,3,0,1] row_mask:0xf bank_mask:0xf
	s_nop 1
	s_waitcnt lgkmcnt(0)
	v_max_f32_dpp v8, v6, v6 row_half_mirror row_mask:0xf bank_mask:0xf
	v_cmp_eq_f32_e32 vcc, v5, v8
	s_nop 1
	v_lshrrev_b64 v[6:7], v200, vcc
	v_ffbl_b32_sdwa v6, v6 dst_sel:DWORD dst_unused:UNUSED_PAD src0_sel:BYTE_0
	v_add_u32_e32 v6, v6, v200
	v_cmp_ne_u32_e32 vcc, v230, v6
	s_nop 1
	v_cndmask_b32_e32 v6, v245, v5, vcc
	s_nop 1
	s_waitcnt lgkmcnt(0)
	v_max_f32_dpp v6, v6, v6 quad_perm:[1,0,3,2] row_mask:0xf bank_mask:0xf
	s_nop 1
	s_waitcnt lgkmcnt(0)
	v_max_f32_dpp v6, v6, v6 quad_perm:[2,3,0,1] row_mask:0xf bank_mask:0xf
	s_nop 1
	s_waitcnt lgkmcnt(0)
	v_max_f32_dpp v6, v6, v6 row_half_mirror row_mask:0xf bank_mask:0xf
	v_add_f32_e32 v6, v8, v6
	s_nop 0
	v_readlane_b32 s5, v6, 0
	s_nop 1
	v_cmp_eq_f32_e64 s[22:23], s5, v6
	v_cmp_gt_f32_e32 vcc, s5, v6
	s_and_b64 s[22:23], s[6:7], s[22:23]
	s_or_b64 s[22:23], vcc, s[22:23]
	v_readlane_b32 s5, v6, 8
	v_cndmask_b32_e64 v7, 0, 1, s[22:23]
	s_nop 0
	v_cmp_eq_f32_e64 s[22:23], s5, v6
	v_cmp_gt_f32_e32 vcc, s5, v6
	s_and_b64 s[22:23], s[8:9], s[22:23]
	s_or_b64 s[22:23], vcc, s[22:23]
	v_readlane_b32 s5, v6, 16
	v_cndmask_b32_e64 v8, 0, 1, s[22:23]
	s_nop 0
	v_cmp_eq_f32_e64 s[22:23], s5, v6
	v_cmp_gt_f32_e32 vcc, s5, v6
	s_and_b64 s[22:23], s[10:11], s[22:23]
	s_or_b64 s[22:23], vcc, s[22:23]
	v_readlane_b32 s5, v6, 24
	v_cndmask_b32_e64 v9, 0, 1, s[22:23]
	s_nop 0
	v_cmp_eq_f32_e64 s[22:23], s5, v6
	v_cmp_gt_f32_e32 vcc, s5, v6
	s_and_b64 s[22:23], s[12:13], s[22:23]
	s_or_b64 s[22:23], vcc, s[22:23]
	v_readlane_b32 s5, v6, 32
	v_cndmask_b32_e64 v10, 0, 1, s[22:23]
	s_nop 0
	v_cmp_eq_f32_e64 s[22:23], s5, v6
	v_cmp_gt_f32_e32 vcc, s5, v6
	s_and_b64 s[22:23], s[14:15], s[22:23]
	s_or_b64 s[22:23], vcc, s[22:23]
	v_readlane_b32 s5, v6, 40
	v_cndmask_b32_e64 v11, 0, 1, s[22:23]
	s_nop 0
	v_cmp_eq_f32_e64 s[22:23], s5, v6
	v_cmp_gt_f32_e32 vcc, s5, v6
	s_and_b64 s[22:23], s[16:17], s[22:23]
	s_or_b64 s[22:23], vcc, s[22:23]
	v_readlane_b32 s5, v6, 48
	v_cndmask_b32_e64 v12, 0, 1, s[22:23]
	s_nop 0
	v_cmp_eq_f32_e64 s[22:23], s5, v6
	v_cmp_gt_f32_e32 vcc, s5, v6
	s_and_b64 s[22:23], s[18:19], s[22:23]
	v_readlane_b32 s5, v6, 56
	s_or_b64 s[22:23], vcc, s[22:23]
	v_cndmask_b32_e64 v13, 0, 1, s[22:23]
	v_cmp_gt_f32_e32 vcc, s5, v6
	s_nop 1
	v_cndmask_b32_e64 v6, 0, 1, vcc
	v_add_u32_e32 v6, v8, v6
	v_add3_u32 v6, v6, v7, v9
	v_add3_u32 v6, v6, v10, v11
	v_add3_u32 v6, v6, v12, v13
	v_cmp_eq_u32_e32 vcc, 0, v6
	s_ff1_i32_b64 s98, vcc
	v_cmp_eq_u32_e32 vcc, 1, v6
	s_ff1_i32_b64 s99, vcc
	v_cmp_eq_u32_e32 vcc, 2, v6
	s_ff1_i32_b64 s100, vcc
	v_cmp_eq_u32_e32 vcc, 3, v6
	s_ff1_i32_b64 s101, vcc
	v_cmp_gt_u32_e32 vcc, 4, v6
	v_mov_b32_e32 v6, 0
	s_nop 0
	v_cndmask_b32_e32 v5, v245, v5, vcc
	v_ashrrev_i32_e32 v9, 31, v5
	v_sub_u32_e32 v8, 63, v230
	v_and_b32_e32 v9, 0x7fffffff, v9
	v_xor_b32_e32 v9, v5, v9
	s_nop 0
	v_readlane_b32 s25, v9, s98
	s_sub_i32 s24, 63, s98
	s_add_i32 s98, s98, 1
	v_readlane_b32 s23, v9, s98
	s_sub_i32 s22, 63, s98
	s_add_i32 s98, s98, 1
	v_cmp_gt_i64_e32 vcc, s[24:25], v[8:9]
	v_readlane_b32 s25, v9, s98
	s_sub_i32 s24, 63, s98
	s_add_i32 s98, s98, 1
	v_addc_co_u32_e32 v6, vcc, 0, v6, vcc
	v_cmp_gt_i64_e32 vcc, s[22:23], v[8:9]
	v_readlane_b32 s23, v9, s98
	s_sub_i32 s22, 63, s98
	s_add_i32 s98, s98, 1
	v_addc_co_u32_e32 v6, vcc, 0, v6, vcc
	v_cmp_gt_i64_e32 vcc, s[24:25], v[8:9]
	v_readlane_b32 s25, v9, s98
	s_sub_i32 s24, 63, s98
	s_add_i32 s98, s98, 1
	v_addc_co_u32_e32 v6, vcc, 0, v6, vcc
	v_cmp_gt_i64_e32 vcc, s[22:23], v[8:9]
	v_readlane_b32 s23, v9, s98
	s_sub_i32 s22, 63, s98
	s_add_i32 s98, s98, 1
	v_addc_co_u32_e32 v6, vcc, 0, v6, vcc
	v_cmp_gt_i64_e32 vcc, s[24:25], v[8:9]
	v_readlane_b32 s25, v9, s98
	s_sub_i32 s24, 63, s98
	s_add_i32 s98, s98, 1
	v_addc_co_u32_e32 v6, vcc, 0, v6, vcc
	v_cmp_gt_i64_e32 vcc, s[22:23], v[8:9]
	v_readlane_b32 s23, v9, s98
	s_sub_i32 s22, 63, s98
	s_nop 0
	v_addc_co_u32_e32 v6, vcc, 0, v6, vcc
	v_cmp_gt_i64_e32 vcc, s[24:25], v[8:9]
	v_readlane_b32 s25, v9, s99
	s_sub_i32 s24, 63, s99
	s_add_i32 s99, s99, 1
	v_addc_co_u32_e32 v6, vcc, 0, v6, vcc
	v_cmp_gt_i64_e32 vcc, s[22:23], v[8:9]
	v_readlane_b32 s23, v9, s99
	s_sub_i32 s22, 63, s99
	s_add_i32 s99, s99, 1
	v_addc_co_u32_e32 v6, vcc, 0, v6, vcc
	v_cmp_gt_i64_e32 vcc, s[24:25], v[8:9]
	v_readlane_b32 s25, v9, s99
	s_sub_i32 s24, 63, s99
	s_add_i32 s99, s99, 1
	v_addc_co_u32_e32 v6, vcc, 0, v6, vcc
	v_cmp_gt_i64_e32 vcc, s[22:23], v[8:9]
	v_readlane_b32 s23, v9, s99
	s_sub_i32 s22, 63, s99
	s_add_i32 s99, s99, 1
	v_addc_co_u32_e32 v6, vcc, 0, v6, vcc
; __device__ __forceinline__ void phase_nrr(const Frame& F, const Args& a, int l, const bf16_t* XA, const float* g, const float* modl, unsigned char* XN8) {
;     ...
;             const bool keep = grank < 4; const float val = keep ? bb : -INFINITY;
;             int rank = 0;
; #pragma unroll 8
;             for (int e2 = 0; e2 < 64; ++e2) { const float v = __int_as_float(__builtin_amdgcn_readlane(__float_as_int(val), e2)); rank += (v > val || (v == val && e2 < lane)) ? 1 : 0; }
;             const bool sel = rank < TOPK;
;             const float ssum = wave_sum(sel ? sc : 0.f);
;             if (sel) { const int p = atomicAdd((int*)(hist + lane), 1); top_e[t * TOPK + rank] = lane; gate[t * TOPK + rank] = sc / ssum * 2.5f; lpos[t * TOPK + rank] = p; }
	v_cmp_gt_i64_e32 vcc, s[24:25], v[8:9]
	v_readlane_b32 s25, v9, s99
	s_sub_i32 s24, 63, s99
	s_add_i32 s99, s99, 1
	v_addc_co_u32_e32 v6, vcc, 0, v6, vcc
	v_cmp_gt_i64_e32 vcc, s[22:23], v[8:9]
	v_readlane_b32 s23, v9, s99
	s_sub_i32 s22, 63, s99
	s_add_i32 s99, s99, 1
	v_addc_co_u32_e32 v6, vcc, 0, v6, vcc
	v_cmp_gt_i64_e32 vcc, s[24:25], v[8:9]
	v_readlane_b32 s25, v9, s99
	s_sub_i32 s24, 63, s99
	s_add_i32 s99, s99, 1
	v_addc_co_u32_e32 v6, vcc, 0, v6, vcc
	v_cmp_gt_i64_e32 vcc, s[22:23], v[8:9]
	v_readlane_b32 s23, v9, s99
	s_sub_i32 s22, 63, s99
	s_nop 0
	v_addc_co_u32_e32 v6, vcc, 0, v6, vcc
	v_cmp_gt_i64_e32 vcc, s[24:25], v[8:9]
	v_readlane_b32 s25, v9, s100
	s_sub_i32 s24, 63, s100
	s_add_i32 s100, s100, 1
	v_addc_co_u32_e32 v6, vcc, 0, v6, vcc
	v_cmp_gt_i64_e32 vcc, s[22:23], v[8:9]
	v_readlane_b32 s23, v9, s100
	s_sub_i32 s22, 63, s100
	s_add_i32 s100, s100, 1
	v_addc_co_u32_e32 v6, vcc, 0, v6, vcc
	v_cmp_gt_i64_e32 vcc, s[24:25], v[8:9]
	v_readlane_b32 s25, v9, s100
	s_sub_i32 s24, 63, s100
	s_add_i32 s100, s100, 1
	v_addc_co_u32_e32 v6, vcc, 0, v6, vcc
	v_cmp_gt_i64_e32 vcc, s[22:23], v[8:9]
	v_readlane_b32 s23, v9, s100
	s_sub_i32 s22, 63, s100
	s_add_i32 s100, s100, 1
	v_addc_co_u32_e32 v6, vcc, 0, v6, vcc
	v_cmp_gt_i64_e32 vcc, s[24:25], v[8:9]
	v_readlane_b32 s25, v9, s100
	s_sub_i32 s24, 63, s100
	s_add_i32 s100, s100, 1
	v_addc_co_u32_e32 v6, vcc, 0, v6, vcc
	v_cmp_gt_i64_e32 vcc, s[22:23], v[8:9]
	v_readlane_b32 s23, v9, s100
	s_sub_i32 s22, 63, s100
	s_add_i32 s100, s100, 1
	v_addc_co_u32_e32 v6, vcc, 0, v6, vcc
	v_cmp_gt_i64_e32 vcc, s[24:25], v[8:9]
	v_readlane_b32 s25, v9, s100
	s_sub_i32 s24, 63, s100
	s_add_i32 s100, s100, 1
	v_addc_co_u32_e32 v6, vcc, 0, v6, vcc
	v_cmp_gt_i64_e32 vcc, s[22:23], v[8:9]
	v_readlane_b32 s23, v9, s100
	s_sub_i32 s22, 63, s100
	s_nop 0
	v_addc_co_u32_e32 v6, vcc, 0, v6, vcc
	v_cmp_gt_i64_e32 vcc, s[24:25], v[8:9]
	v_readlane_b32 s25, v9, s101
	s_sub_i32 s24, 63, s101
	s_add_i32 s101, s101, 1
	v_addc_co_u32_e32 v6, vcc, 0, v6, vcc
	v_cmp_gt_i64_e32 vcc, s[22:23], v[8:9]
	v_readlane_b32 s23, v9, s101
	s_sub_i32 s22, 63, s101
	s_add_i32 s101, s101, 1
	v_addc_co_u32_e32 v6, vcc, 0, v6, vcc
	v_cmp_gt_i64_e32 vcc, s[24:25], v[8:9]
	v_readlane_b32 s25, v9, s101
	s_sub_i32 s24, 63, s101
	s_add_i32 s101, s101, 1
	v_addc_co_u32_e32 v6, vcc, 0, v6, vcc
	v_cmp_gt_i64_e32 vcc, s[22:23], v[8:9]
	v_readlane_b32 s23, v9, s101
	s_sub_i32 s22, 63, s101
	s_add_i32 s101, s101, 1
	v_addc_co_u32_e32 v6, vcc, 0, v6, vcc
	v_cmp_gt_i64_e32 vcc, s[24:25], v[8:9]
	v_readlane_b32 s25, v9, s101
	s_sub_i32 s24, 63, s101
	s_add_i32 s101, s101, 1
	v_addc_co_u32_e32 v6, vcc, 0, v6, vcc
	v_cmp_gt_i64_e32 vcc, s[22:23], v[8:9]
	v_readlane_b32 s23, v9, s101
	s_sub_i32 s22, 63, s101
	s_add_i32 s101, s101, 1
	v_addc_co_u32_e32 v6, vcc, 0, v6, vcc
	v_cmp_gt_i64_e32 vcc, s[24:25], v[8:9]
	v_readlane_b32 s25, v9, s101
	s_sub_i32 s24, 63, s101
	s_add_i32 s101, s101, 1
	v_addc_co_u32_e32 v6, vcc, 0, v6, vcc
	v_cmp_gt_i64_e32 vcc, s[22:23], v[8:9]
	v_readlane_b32 s23, v9, s101
	s_sub_i32 s22, 63, s101
	s_nop 0
	v_addc_co_u32_e32 v6, vcc, 0, v6, vcc
	v_cmp_gt_i64_e32 vcc, s[24:25], v[8:9]
	s_nop 1
	v_addc_co_u32_e32 v6, vcc, 0, v6, vcc
	v_cmp_gt_i64_e32 vcc, s[22:23], v[8:9]
	s_nop 1
	v_addc_co_u32_e32 v6, vcc, 0, v6, vcc
	v_cmp_gt_u32_e32 vcc, 6, v6
	s_mul_i32 s36, s44, 6
	s_nop 0
	v_cndmask_b32_e32 v5, 0, v2, vcc
	s_nop 1
	v_add_f32_dpp v5, v5, v5 quad_perm:[1,0,3,2] row_mask:0xf bank_mask:0xf
	s_nop 1
	v_add_f32_dpp v5, v5, v5 quad_perm:[2,3,0,1] row_mask:0xf bank_mask:0xf
	s_nop 1
	v_add_f32_dpp v5, v5, v5 row_half_mirror row_mask:0xf bank_mask:0xf
	s_nop 1
	v_add_f32_dpp v5, v5, v5 row_mirror row_mask:0xf bank_mask:0xf
	v_mov_b32_e32 v7, v5
	s_nop 1
	v_permlane16_swap_b32_e32 v7, v5
	s_waitcnt lgkmcnt(0)
	v_add_f32_e32 v5, v5, v7
	v_mov_b32_e32 v7, v5
	s_nop 1
	v_permlane32_swap_b32_e32 v7, v5
	s_and_saveexec_b64 s[22:23], vcc
	s_cbranch_execz .LBB0_539
	s_waitcnt lgkmcnt(0)
	v_add_f32_e32 v5, v5, v7
	v_div_scale_f32 v11, s[24:25], v5, v5, v2
	v_or_b32_e32 v6, s36, v6
	v_rcp_f32_e32 v12, v11
	v_ashrrev_i32_e32 v7, 31, v6
	v_lshlrev_b64 v[6:7], 2, v[6:7]
	v_lshl_add_u64 v[8:9], s[26:27], 0, v[6:7]
	ds_add_rtn_u32 v10, v227, v243
	global_store_dword v[8:9], v230, off
	v_fma_f32 v8, -v11, v12, 1.0
	v_fmac_f32_e32 v12, v8, v12
	v_div_scale_f32 v8, vcc, v2, v5, v2
	v_mul_f32_e32 v9, v8, v12
	v_fma_f32 v13, -v11, v9, v8
	v_fmac_f32_e32 v9, v13, v12
	v_fma_f32 v8, -v11, v9, v8
	v_div_fmas_f32 v8, v8, v12, v9
	v_div_fixup_f32 v2, v8, v5, v2
	v_mul_f32_e32 v2, 0x40200000, v2
	v_lshl_add_u64 v[8:9], s[28:29], 0, v[6:7]
	v_lshl_add_u64 v[6:7], s[30:31], 0, v[6:7]
	global_store_dword v[8:9], v2, off
	s_waitcnt lgkmcnt(0)
	global_store_dword v[6:7], v10, off
; __device__ __forceinline__ void phase_nrr(const Frame& F, const Args& a, int l, const bf16_t* XA, const float* g, const float* modl, unsigned char* XN8) {
;     ...
;         for (int i = 0; i < 8; ++i) { const int t = tb + i;
;             const float lg = Pl[(w * 8 + i) * NE + lane] + Pl[(64 + w * 8 + i) * NE + lane]; const float sc = 1.f / (1.f + __expf(-lg)); const float bb = sc + bias;
;             float m1 = bb; m1 = fmaxf(m1, __shfl_xor(m1, 1)); m1 = fmaxf(m1, __shfl_xor(m1, 2)); m1 = fmaxf(m1, __shfl_xor(m1, 4));
;             const unsigned long long eq = __ballot(bb == m1); const int gbase = lane & ~7; const unsigned grpmask = (unsigned)((eq >> gbase) & 0xffull);
;             const int first = gbase + __builtin_ctz(grpmask);
;             float m2 = (lane == first) ? -INFINITY : bb; m2 = fmaxf(m2, __shfl_xor(m2, 1)); m2 = fmaxf(m2, __shfl_xor(m2, 2)); m2 = fmaxf(m2, __shfl_xor(m2, 4));
;             const float gsum = m1 + m2; const int gq = lane >> 3;
;             int grank = 0;
; #pragma unroll
;             for (int g2 = 0; g2 < 8; ++g2) { const float v = __int_as_float(__builtin_amdgcn_readlane(__float_as_int(gsum), g2 * 8)); grank += (v > gsum || (v == gsum && g2 < gq)) ? 1 : 0; }
;             const bool keep = grank < 4; const float val = keep ? bb : -INFINITY;
;             int rank = 0;
; #pragma unroll 8
;             for (int e2 = 0; e2 < 64; ++e2) { const float v = __int_as_float(__builtin_amdgcn_readlane(__float_as_int(val), e2)); rank += (v > val || (v == val && e2 < lane)) ? 1 : 0; }
.LBB0_539:
	s_or_b64 exec, exec, s[22:23]
	v_add_u32_e32 v2, s77, v226
	ds_read_b32 v2, v2
	ds_read_b32 v5, v4 offset:16640
	s_mov_b32 s3, 0
	s_waitcnt lgkmcnt(0)
	v_add_f32_e32 v2, v2, v5
	v_mul_f32_e32 v2, 0xbfb8aa3b, v2
	v_exp_f32_e32 v2, v2
	s_nop 0
	v_add_f32_e32 v2, 1.0, v2
	v_div_scale_f32 v5, s[22:23], v2, v2, 1.0
	v_rcp_f32_e32 v6, v5
	s_nop 0
	v_fma_f32 v7, -v5, v6, 1.0
	v_fmac_f32_e32 v6, v7, v6
	v_div_scale_f32 v7, vcc, 1.0, v2, 1.0
	v_mul_f32_e32 v8, v7, v6
	v_fma_f32 v9, -v5, v8, v7
	v_fmac_f32_e32 v8, v9, v6
	v_fma_f32 v5, -v5, v8, v7
	v_div_fmas_f32 v5, v5, v6, v8
	v_div_fixup_f32 v5, v5, v2, 1.0
	v_add_f32_e32 v2, v3, v5
	s_nop 1
	s_waitcnt lgkmcnt(0)
	v_max_f32_dpp v6, v2, v2 quad_perm:[1,0,3,2] row_mask:0xf bank_mask:0xf
	s_nop 1
	s_waitcnt lgkmcnt(0)
	v_max_f32_dpp v6, v6, v6 quad_perm:[2,3,0,1] row_mask:0xf bank_mask:0xf
	s_nop 1
	s_waitcnt lgkmcnt(0)
	v_max_f32_dpp v8, v6, v6 row_half_mirror row_mask:0xf bank_mask:0xf
	v_cmp_eq_f32_e32 vcc, v2, v8
	s_nop 1
	v_lshrrev_b64 v[6:7], v200, vcc
	v_ffbl_b32_sdwa v6, v6 dst_sel:DWORD dst_unused:UNUSED_PAD src0_sel:BYTE_0
	v_add_u32_e32 v6, v6, v200
	v_cmp_ne_u32_e32 vcc, v230, v6
	s_nop 1
	v_cndmask_b32_e32 v6, v245, v2, vcc
	s_nop 1
	s_waitcnt lgkmcnt(0)
	v_max_f32_dpp v6, v6, v6 quad_perm:[1,0,3,2] row_mask:0xf bank_mask:0xf
	s_nop 1
	s_waitcnt lgkmcnt(0)
	v_max_f32_dpp v6, v6, v6 quad_perm:[2,3,0,1] row_mask:0xf bank_mask:0xf
	s_nop 1
	s_waitcnt lgkmcnt(0)
	v_max_f32_dpp v6, v6, v6 row_half_mirror row_mask:0xf bank_mask:0xf
	v_add_f32_e32 v6, v8, v6
	s_nop 0
	v_readlane_b32 s5, v6, 0
	s_nop 1
	v_cmp_eq_f32_e64 s[22:23], s5, v6
	v_cmp_gt_f32_e32 vcc, s5, v6
	s_and_b64 s[22:23], s[6:7], s[22:23]
	s_or_b64 s[22:23], vcc, s[22:23]
	v_readlane_b32 s5, v6, 8
	v_cndmask_b32_e64 v7, 0, 1, s[22:23]
	s_nop 0
	v_cmp_eq_f32_e64 s[22:23], s5, v6
	v_cmp_gt_f32_e32 vcc, s5, v6
	s_and_b64 s[22:23], s[8:9], s[22:23]
	s_or_b64 s[22:23], vcc, s[22:23]
	v_readlane_b32 s5, v6, 16
	v_cndmask_b32_e64 v8, 0, 1, s[22:23]
	s_nop 0
	v_cmp_eq_f32_e64 s[22:23], s5, v6
	v_cmp_gt_f32_e32 vcc, s5, v6
	s_and_b64 s[22:23], s[10:11], s[22:23]
	s_or_b64 s[22:23], vcc, s[22:23]
	v_readlane_b32 s5, v6, 24
	v_cndmask_b32_e64 v9, 0, 1, s[22:23]
	s_nop 0
	v_cmp_eq_f32_e64 s[22:23], s5, v6
	v_cmp_gt_f32_e32 vcc, s5, v6
	s_and_b64 s[22:23], s[12:13], s[22:23]
	s_or_b64 s[22:23], vcc, s[22:23]
	v_readlane_b32 s5, v6, 32
	v_cndmask_b32_e64 v10, 0, 1, s[22:23]
	s_nop 0
	v_cmp_eq_f32_e64 s[22:23], s5, v6
	v_cmp_gt_f32_e32 vcc, s5, v6
	s_and_b64 s[22:23], s[14:15], s[22:23]
	s_or_b64 s[22:23], vcc, s[22:23]
	v_readlane_b32 s5, v6, 40
	v_cndmask_b32_e64 v11, 0, 1, s[22:23]
	s_nop 0
	v_cmp_eq_f32_e64 s[22:23], s5, v6
	v_cmp_gt_f32_e32 vcc, s5, v6
	s_and_b64 s[22:23], s[16:17], s[22:23]
	s_or_b64 s[22:23], vcc, s[22:23]
	v_readlane_b32 s5, v6, 48
	v_cndmask_b32_e64 v12, 0, 1, s[22:23]
	s_nop 0
	v_cmp_eq_f32_e64 s[22:23], s5, v6
	v_cmp_gt_f32_e32 vcc, s5, v6
	s_and_b64 s[22:23], s[18:19], s[22:23]
	v_readlane_b32 s5, v6, 56
	s_or_b64 s[22:23], vcc, s[22:23]
	v_cndmask_b32_e64 v13, 0, 1, s[22:23]
	v_cmp_gt_f32_e32 vcc, s5, v6
	s_nop 1
	v_cndmask_b32_e64 v6, 0, 1, vcc
	v_add_u32_e32 v6, v8, v6
	v_add3_u32 v6, v6, v7, v9
	v_add3_u32 v6, v6, v10, v11
	v_add3_u32 v6, v6, v12, v13
	v_cmp_eq_u32_e32 vcc, 0, v6
	s_ff1_i32_b64 s98, vcc
	v_cmp_eq_u32_e32 vcc, 1, v6
	s_ff1_i32_b64 s99, vcc
	v_cmp_eq_u32_e32 vcc, 2, v6
	s_ff1_i32_b64 s100, vcc
	v_cmp_eq_u32_e32 vcc, 3, v6
	s_ff1_i32_b64 s101, vcc
	v_cmp_gt_u32_e32 vcc, 4, v6
	s_nop 1
	v_cndmask_b32_e32 v6, v245, v2, vcc
	v_mov_b32_e32 v2, 0
	v_ashrrev_i32_e32 v9, 31, v6
	v_sub_u32_e32 v8, 63, v230
	v_and_b32_e32 v9, 0x7fffffff, v9
	v_xor_b32_e32 v9, v6, v9
	s_nop 0
	v_readlane_b32 s25, v9, s98
	s_sub_i32 s24, 63, s98
	s_add_i32 s98, s98, 1
	v_readlane_b32 s23, v9, s98
	s_sub_i32 s22, 63, s98
	s_add_i32 s98, s98, 1
	v_cmp_gt_i64_e32 vcc, s[24:25], v[8:9]
	v_readlane_b32 s25, v9, s98
	s_sub_i32 s24, 63, s98
	s_add_i32 s98, s98, 1
	v_addc_co_u32_e32 v2, vcc, 0, v2, vcc
	v_cmp_gt_i64_e32 vcc, s[22:23], v[8:9]
	v_readlane_b32 s23, v9, s98
	s_sub_i32 s22, 63, s98
	s_add_i32 s98, s98, 1
	v_addc_co_u32_e32 v2, vcc, 0, v2, vcc
	v_cmp_gt_i64_e32 vcc, s[24:25], v[8:9]
	v_readlane_b32 s25, v9, s98
	s_sub_i32 s24, 63, s98
	s_add_i32 s98, s98, 1
	v_addc_co_u32_e32 v2, vcc, 0, v2, vcc
	v_cmp_gt_i64_e32 vcc, s[22:23], v[8:9]
	v_readlane_b32 s23, v9, s98
	s_sub_i32 s22, 63, s98
	s_add_i32 s98, s98, 1
	v_addc_co_u32_e32 v2, vcc, 0, v2, vcc
	v_cmp_gt_i64_e32 vcc, s[24:25], v[8:9]
	v_readlane_b32 s25, v9, s98
	s_sub_i32 s24, 63, s98
	s_add_i32 s98, s98, 1
	v_addc_co_u32_e32 v2, vcc, 0, v2, vcc
	v_cmp_gt_i64_e32 vcc, s[22:23], v[8:9]
	v_readlane_b32 s23, v9, s98
	s_sub_i32 s22, 63, s98
	s_nop 0
	v_addc_co_u32_e32 v2, vcc, 0, v2, vcc
	v_cmp_gt_i64_e32 vcc, s[24:25], v[8:9]
	v_readlane_b32 s25, v9, s99
	s_sub_i32 s24, 63, s99
	s_add_i32 s99, s99, 1
	v_addc_co_u32_e32 v2, vcc, 0, v2, vcc
	v_cmp_gt_i64_e32 vcc, s[22:23], v[8:9]
	v_readlane_b32 s23, v9, s99
	s_sub_i32 s22, 63, s99
	s_add_i32 s99, s99, 1
	v_addc_co_u32_e32 v2, vcc, 0, v2, vcc
	v_cmp_gt_i64_e32 vcc, s[24:25], v[8:9]
	v_readlane_b32 s25, v9, s99
	s_sub_i32 s24, 63, s99
	s_add_i32 s99, s99, 1
	v_addc_co_u32_e32 v2, vcc, 0, v2, vcc
	v_cmp_gt_i64_e32 vcc, s[22:23], v[8:9]
	v_readlane_b32 s23, v9, s99
	s_sub_i32 s22, 63, s99
	s_add_i32 s99, s99, 1
	v_addc_co_u32_e32 v2, vcc, 0, v2, vcc
	v_cmp_gt_i64_e32 vcc, s[24:25], v[8:9]
	v_readlane_b32 s25, v9, s99
	s_sub_i32 s24, 63, s99
	s_add_i32 s99, s99, 1
	v_addc_co_u32_e32 v2, vcc, 0, v2, vcc
	v_cmp_gt_i64_e32 vcc, s[22:23], v[8:9]
	v_readlane_b32 s23, v9, s99
	s_sub_i32 s22, 63, s99
	s_add_i32 s99, s99, 1
; __device__ __forceinline__ void phase_nrr(const Frame& F, const Args& a, int l, const bf16_t* XA, const float* g, const float* modl, unsigned char* XN8) {
;     ...
;             const bool keep = grank < 4; const float val = keep ? bb : -INFINITY;
;             int rank = 0;
; #pragma unroll 8
;             for (int e2 = 0; e2 < 64; ++e2) { const float v = __int_as_float(__builtin_amdgcn_readlane(__float_as_int(val), e2)); rank += (v > val || (v == val && e2 < lane)) ? 1 : 0; }
;             const bool sel = rank < TOPK;
;             const float ssum = wave_sum(sel ? sc : 0.f);
;             if (sel) { const int p = atomicAdd((int*)(hist + lane), 1); top_e[t * TOPK + rank] = lane; gate[t * TOPK + rank] = sc / ssum * 2.5f; lpos[t * TOPK + rank] = p; }
	v_addc_co_u32_e32 v2, vcc, 0, v2, vcc
	v_cmp_gt_i64_e32 vcc, s[24:25], v[8:9]
	v_readlane_b32 s25, v9, s99
	s_sub_i32 s24, 63, s99
	s_add_i32 s99, s99, 1
	v_addc_co_u32_e32 v2, vcc, 0, v2, vcc
	v_cmp_gt_i64_e32 vcc, s[22:23], v[8:9]
	v_readlane_b32 s23, v9, s99
	s_sub_i32 s22, 63, s99
	s_nop 0
	v_addc_co_u32_e32 v2, vcc, 0, v2, vcc
	v_cmp_gt_i64_e32 vcc, s[24:25], v[8:9]
	v_readlane_b32 s25, v9, s100
	s_sub_i32 s24, 63, s100
	s_add_i32 s100, s100, 1
	v_addc_co_u32_e32 v2, vcc, 0, v2, vcc
	v_cmp_gt_i64_e32 vcc, s[22:23], v[8:9]
	v_readlane_b32 s23, v9, s100
	s_sub_i32 s22, 63, s100
	s_add_i32 s100, s100, 1
	v_addc_co_u32_e32 v2, vcc, 0, v2, vcc
	v_cmp_gt_i64_e32 vcc, s[24:25], v[8:9]
	v_readlane_b32 s25, v9, s100
	s_sub_i32 s24, 63, s100
	s_add_i32 s100, s100, 1
	v_addc_co_u32_e32 v2, vcc, 0, v2, vcc
	v_cmp_gt_i64_e32 vcc, s[22:23], v[8:9]
	v_readlane_b32 s23, v9, s100
	s_sub_i32 s22, 63, s100
	s_add_i32 s100, s100, 1
	v_addc_co_u32_e32 v2, vcc, 0, v2, vcc
	v_cmp_gt_i64_e32 vcc, s[24:25], v[8:9]
	v_readlane_b32 s25, v9, s100
	s_sub_i32 s24, 63, s100
	s_add_i32 s100, s100, 1
	v_addc_co_u32_e32 v2, vcc, 0, v2, vcc
	v_cmp_gt_i64_e32 vcc, s[22:23], v[8:9]
	v_readlane_b32 s23, v9, s100
	s_sub_i32 s22, 63, s100
	s_add_i32 s100, s100, 1
	v_addc_co_u32_e32 v2, vcc, 0, v2, vcc
	v_cmp_gt_i64_e32 vcc, s[24:25], v[8:9]
	v_readlane_b32 s25, v9, s100
	s_sub_i32 s24, 63, s100
	s_add_i32 s100, s100, 1
	v_addc_co_u32_e32 v2, vcc, 0, v2, vcc
	v_cmp_gt_i64_e32 vcc, s[22:23], v[8:9]
	v_readlane_b32 s23, v9, s100
	s_sub_i32 s22, 63, s100
	s_nop 0
	v_addc_co_u32_e32 v2, vcc, 0, v2, vcc
	v_cmp_gt_i64_e32 vcc, s[24:25], v[8:9]
	v_readlane_b32 s25, v9, s101
	s_sub_i32 s24, 63, s101
	s_add_i32 s101, s101, 1
	v_addc_co_u32_e32 v2, vcc, 0, v2, vcc
	v_cmp_gt_i64_e32 vcc, s[22:23], v[8:9]
	v_readlane_b32 s23, v9, s101
	s_sub_i32 s22, 63, s101
	s_add_i32 s101, s101, 1
	v_addc_co_u32_e32 v2, vcc, 0, v2, vcc
	v_cmp_gt_i64_e32 vcc, s[24:25], v[8:9]
	v_readlane_b32 s25, v9, s101
	s_sub_i32 s24, 63, s101
	s_add_i32 s101, s101, 1
	v_addc_co_u32_e32 v2, vcc, 0, v2, vcc
	v_cmp_gt_i64_e32 vcc, s[22:23], v[8:9]
	v_readlane_b32 s23, v9, s101
	s_sub_i32 s22, 63, s101
	s_add_i32 s101, s101, 1
	v_addc_co_u32_e32 v2, vcc, 0, v2, vcc
	v_cmp_gt_i64_e32 vcc, s[24:25], v[8:9]
	v_readlane_b32 s25, v9, s101
	s_sub_i32 s24, 63, s101
	s_add_i32 s101, s101, 1
	v_addc_co_u32_e32 v2, vcc, 0, v2, vcc
	v_cmp_gt_i64_e32 vcc, s[22:23], v[8:9]
	v_readlane_b32 s23, v9, s101
	s_sub_i32 s22, 63, s101
	s_add_i32 s101, s101, 1
	v_addc_co_u32_e32 v2, vcc, 0, v2, vcc
	v_cmp_gt_i64_e32 vcc, s[24:25], v[8:9]
	v_readlane_b32 s25, v9, s101
	s_sub_i32 s24, 63, s101
	s_add_i32 s101, s101, 1
	v_addc_co_u32_e32 v2, vcc, 0, v2, vcc
	v_cmp_gt_i64_e32 vcc, s[22:23], v[8:9]
	v_readlane_b32 s23, v9, s101
	s_sub_i32 s22, 63, s101
	s_nop 0
	v_addc_co_u32_e32 v2, vcc, 0, v2, vcc
	v_cmp_gt_i64_e32 vcc, s[24:25], v[8:9]
	s_nop 1
	v_addc_co_u32_e32 v2, vcc, 0, v2, vcc
	v_cmp_gt_i64_e32 vcc, s[22:23], v[8:9]
	s_nop 1
	v_addc_co_u32_e32 v2, vcc, 0, v2, vcc
	v_cmp_gt_u32_e32 vcc, 6, v2
	s_nop 1
	v_cndmask_b32_e32 v6, 0, v5, vcc
	s_nop 1
	v_add_f32_dpp v6, v6, v6 quad_perm:[1,0,3,2] row_mask:0xf bank_mask:0xf
	s_nop 1
	v_add_f32_dpp v6, v6, v6 quad_perm:[2,3,0,1] row_mask:0xf bank_mask:0xf
	s_nop 1
	v_add_f32_dpp v6, v6, v6 row_half_mirror row_mask:0xf bank_mask:0xf
	s_nop 1
	v_add_f32_dpp v6, v6, v6 row_mirror row_mask:0xf bank_mask:0xf
	v_mov_b32_e32 v7, v6
	s_nop 1
	v_permlane16_swap_b32_e32 v7, v6
	s_waitcnt lgkmcnt(0)
	v_add_f32_e32 v6, v6, v7
	v_mov_b32_e32 v7, v6
	s_nop 1
	v_permlane32_swap_b32_e32 v7, v6
	s_and_saveexec_b64 s[22:23], vcc
	s_cbranch_execz .LBB0_543
	s_waitcnt lgkmcnt(0)
	v_add_f32_e32 v10, v6, v7
	v_mad_u64_u32 v[6:7], s[24:25], s42, 6, v[2:3]
	v_div_scale_f32 v2, s[24:25], v10, v10, v5
	v_rcp_f32_e32 v12, v2
	v_ashrrev_i32_e32 v7, 31, v6
	v_lshlrev_b64 v[6:7], 2, v[6:7]
	v_lshl_add_u64 v[8:9], s[26:27], 0, v[6:7]
	ds_add_rtn_u32 v11, v227, v243
	global_store_dword v[8:9], v230, off
	v_fma_f32 v8, -v2, v12, 1.0
	v_fmac_f32_e32 v12, v8, v12
	v_div_scale_f32 v8, vcc, v5, v10, v5
	v_mul_f32_e32 v9, v8, v12
	v_fma_f32 v13, -v2, v9, v8
	v_fmac_f32_e32 v9, v13, v12
	v_fma_f32 v2, -v2, v9, v8
	v_div_fmas_f32 v2, v2, v12, v9
	v_div_fixup_f32 v2, v2, v10, v5
	v_mul_f32_e32 v2, 0x40200000, v2
	v_lshl_add_u64 v[8:9], s[28:29], 0, v[6:7]
	v_lshl_add_u64 v[6:7], s[30:31], 0, v[6:7]
	global_store_dword v[8:9], v2, off
	s_waitcnt lgkmcnt(0)
	global_store_dword v[6:7], v11, off
; __device__ __forceinline__ void phase_nrr(const Frame& F, const Args& a, int l, const bf16_t* XA, const float* g, const float* modl, unsigned char* XN8) {
;     ...
;         for (int i = 0; i < 8; ++i) { const int t = tb + i;
;             const float lg = Pl[(w * 8 + i) * NE + lane] + Pl[(64 + w * 8 + i) * NE + lane]; const float sc = 1.f / (1.f + __expf(-lg)); const float bb = sc + bias;
;             float m1 = bb; m1 = fmaxf(m1, __shfl_xor(m1, 1)); m1 = fmaxf(m1, __shfl_xor(m1, 2)); m1 = fmaxf(m1, __shfl_xor(m1, 4));
;             const unsigned long long eq = __ballot(bb == m1); const int gbase = lane & ~7; const unsigned grpmask = (unsigned)((eq >> gbase) & 0xffull);
;             const int first = gbase + __builtin_ctz(grpmask);
;             float m2 = (lane == first) ? -INFINITY : bb; m2 = fmaxf(m2, __shfl_xor(m2, 1)); m2 = fmaxf(m2, __shfl_xor(m2, 2)); m2 = fmaxf(m2, __shfl_xor(m2, 4));
;             const float gsum = m1 + m2; const int gq = lane >> 3;
;             int grank = 0;
; #pragma unroll
;             for (int g2 = 0; g2 < 8; ++g2) { const float v = __int_as_float(__builtin_amdgcn_readlane(__float_as_int(gsum), g2 * 8)); grank += (v > gsum || (v == gsum && g2 < gq)) ? 1 : 0; }
;             const bool keep = grank < 4; const float val = keep ? bb : -INFINITY;
;             int rank = 0;
; #pragma unroll 8
;             for (int e2 = 0; e2 < 64; ++e2) { const float v = __int_as_float(__builtin_amdgcn_readlane(__float_as_int(val), e2)); rank += (v > val || (v == val && e2 < lane)) ? 1 : 0; }
.LBB0_543:
	s_or_b64 exec, exec, s[22:23]
	v_add_u32_e32 v2, s78, v226
	ds_read_b32 v2, v2
	ds_read_b32 v5, v4 offset:16896
	s_mov_b32 s3, 0
	s_waitcnt lgkmcnt(0)
	v_add_f32_e32 v2, v2, v5
	v_mul_f32_e32 v2, 0xbfb8aa3b, v2
	v_exp_f32_e32 v2, v2
	s_nop 0
	v_add_f32_e32 v2, 1.0, v2
	v_div_scale_f32 v5, s[22:23], v2, v2, 1.0
	v_rcp_f32_e32 v6, v5
	s_nop 0
	v_fma_f32 v7, -v5, v6, 1.0
	v_fmac_f32_e32 v6, v7, v6
	v_div_scale_f32 v7, vcc, 1.0, v2, 1.0
	v_mul_f32_e32 v8, v7, v6
	v_fma_f32 v9, -v5, v8, v7
	v_fmac_f32_e32 v8, v9, v6
	v_fma_f32 v5, -v5, v8, v7
	v_div_fmas_f32 v5, v5, v6, v8
	v_div_fixup_f32 v5, v5, v2, 1.0
	v_add_f32_e32 v2, v3, v5
	s_nop 1
	s_waitcnt lgkmcnt(0)
	v_max_f32_dpp v6, v2, v2 quad_perm:[1,0,3,2] row_mask:0xf bank_mask:0xf
	s_nop 1
	s_waitcnt lgkmcnt(0)
	v_max_f32_dpp v6, v6, v6 quad_perm:[2,3,0,1] row_mask:0xf bank_mask:0xf
	s_nop 1
	s_waitcnt lgkmcnt(0)
	v_max_f32_dpp v8, v6, v6 row_half_mirror row_mask:0xf bank_mask:0xf
	v_cmp_eq_f32_e32 vcc, v2, v8
	s_nop 1
	v_lshrrev_b64 v[6:7], v200, vcc
	v_ffbl_b32_sdwa v6, v6 dst_sel:DWORD dst_unused:UNUSED_PAD src0_sel:BYTE_0
	v_add_u32_e32 v6, v6, v200
	v_cmp_ne_u32_e32 vcc, v230, v6
	s_nop 1
	v_cndmask_b32_e32 v6, v245, v2, vcc
	s_nop 1
	s_waitcnt lgkmcnt(0)
	v_max_f32_dpp v6, v6, v6 quad_perm:[1,0,3,2] row_mask:0xf bank_mask:0xf
	s_nop 1
	s_waitcnt lgkmcnt(0)
	v_max_f32_dpp v6, v6, v6 quad_perm:[2,3,0,1] row_mask:0xf bank_mask:0xf
	s_nop 1
	s_waitcnt lgkmcnt(0)
	v_max_f32_dpp v6, v6, v6 row_half_mirror row_mask:0xf bank_mask:0xf
	v_add_f32_e32 v6, v8, v6
	s_nop 0
	v_readlane_b32 s5, v6, 0
	s_nop 1
	v_cmp_eq_f32_e64 s[22:23], s5, v6
	v_cmp_gt_f32_e32 vcc, s5, v6
	s_and_b64 s[22:23], s[6:7], s[22:23]
	s_or_b64 s[22:23], vcc, s[22:23]
	v_readlane_b32 s5, v6, 8
	v_cndmask_b32_e64 v7, 0, 1, s[22:23]
	s_nop 0
	v_cmp_eq_f32_e64 s[22:23], s5, v6
	v_cmp_gt_f32_e32 vcc, s5, v6
	s_and_b64 s[22:23], s[8:9], s[22:23]
	s_or_b64 s[22:23], vcc, s[22:23]
	v_readlane_b32 s5, v6, 16
	v_cndmask_b32_e64 v8, 0, 1, s[22:23]
	s_nop 0
	v_cmp_eq_f32_e64 s[22:23], s5, v6
	v_cmp_gt_f32_e32 vcc, s5, v6
	s_and_b64 s[22:23], s[10:11], s[22:23]
	s_or_b64 s[22:23], vcc, s[22:23]
	v_readlane_b32 s5, v6, 24
	v_cndmask_b32_e64 v9, 0, 1, s[22:23]
	s_nop 0
	v_cmp_eq_f32_e64 s[22:23], s5, v6
	v_cmp_gt_f32_e32 vcc, s5, v6
	s_and_b64 s[22:23], s[12:13], s[22:23]
	s_or_b64 s[22:23], vcc, s[22:23]
	v_readlane_b32 s5, v6, 32
	v_cndmask_b32_e64 v10, 0, 1, s[22:23]
	s_nop 0
	v_cmp_eq_f32_e64 s[22:23], s5, v6
	v_cmp_gt_f32_e32 vcc, s5, v6
	s_and_b64 s[22:23], s[14:15], s[22:23]
	s_or_b64 s[22:23], vcc, s[22:23]
	v_readlane_b32 s5, v6, 40
	v_cndmask_b32_e64 v11, 0, 1, s[22:23]
	s_nop 0
	v_cmp_eq_f32_e64 s[22:23], s5, v6
	v_cmp_gt_f32_e32 vcc, s5, v6
	s_and_b64 s[22:23], s[16:17], s[22:23]
	s_or_b64 s[22:23], vcc, s[22:23]
	v_readlane_b32 s5, v6, 48
	v_cndmask_b32_e64 v12, 0, 1, s[22:23]
	s_nop 0
	v_cmp_eq_f32_e64 s[22:23], s5, v6
	v_cmp_gt_f32_e32 vcc, s5, v6
	s_and_b64 s[22:23], s[18:19], s[22:23]
	v_readlane_b32 s5, v6, 56
	s_or_b64 s[22:23], vcc, s[22:23]
	v_cndmask_b32_e64 v13, 0, 1, s[22:23]
	v_cmp_gt_f32_e32 vcc, s5, v6
	s_nop 1
	v_cndmask_b32_e64 v6, 0, 1, vcc
	v_add_u32_e32 v6, v8, v6
	v_add3_u32 v6, v6, v7, v9
	v_add3_u32 v6, v6, v10, v11
	v_add3_u32 v6, v6, v12, v13
	v_cmp_eq_u32_e32 vcc, 0, v6
	s_ff1_i32_b64 s98, vcc
	v_cmp_eq_u32_e32 vcc, 1, v6
	s_ff1_i32_b64 s99, vcc
	v_cmp_eq_u32_e32 vcc, 2, v6
	s_ff1_i32_b64 s100, vcc
	v_cmp_eq_u32_e32 vcc, 3, v6
	s_ff1_i32_b64 s101, vcc
	v_cmp_gt_u32_e32 vcc, 4, v6
	s_nop 1
	v_cndmask_b32_e32 v6, v245, v2, vcc
	v_mov_b32_e32 v2, 0
	v_ashrrev_i32_e32 v9, 31, v6
	v_sub_u32_e32 v8, 63, v230
	v_and_b32_e32 v9, 0x7fffffff, v9
	v_xor_b32_e32 v9, v6, v9
	s_nop 0
	v_readlane_b32 s25, v9, s98
	s_sub_i32 s24, 63, s98
	s_add_i32 s98, s98, 1
	v_readlane_b32 s23, v9, s98
	s_sub_i32 s22, 63, s98
	s_add_i32 s98, s98, 1
	v_cmp_gt_i64_e32 vcc, s[24:25], v[8:9]
	v_readlane_b32 s25, v9, s98
	s_sub_i32 s24, 63, s98
	s_add_i32 s98, s98, 1
	v_addc_co_u32_e32 v2, vcc, 0, v2, vcc
	v_cmp_gt_i64_e32 vcc, s[22:23], v[8:9]
	v_readlane_b32 s23, v9, s98
	s_sub_i32 s22, 63, s98
	s_add_i32 s98, s98, 1
	v_addc_co_u32_e32 v2, vcc, 0, v2, vcc
	v_cmp_gt_i64_e32 vcc, s[24:25], v[8:9]
	v_readlane_b32 s25, v9, s98
	s_sub_i32 s24, 63, s98
	s_add_i32 s98, s98, 1
	v_addc_co_u32_e32 v2, vcc, 0, v2, vcc
	v_cmp_gt_i64_e32 vcc, s[22:23], v[8:9]
	v_readlane_b32 s23, v9, s98
	s_sub_i32 s22, 63, s98
	s_add_i32 s98, s98, 1
	v_addc_co_u32_e32 v2, vcc, 0, v2, vcc
	v_cmp_gt_i64_e32 vcc, s[24:25], v[8:9]
	v_readlane_b32 s25, v9, s98
	s_sub_i32 s24, 63, s98
	s_add_i32 s98, s98, 1
	v_addc_co_u32_e32 v2, vcc, 0, v2, vcc
	v_cmp_gt_i64_e32 vcc, s[22:23], v[8:9]
	v_readlane_b32 s23, v9, s98
	s_sub_i32 s22, 63, s98
	s_nop 0
	v_addc_co_u32_e32 v2, vcc, 0, v2, vcc
	v_cmp_gt_i64_e32 vcc, s[24:25], v[8:9]
	v_readlane_b32 s25, v9, s99
	s_sub_i32 s24, 63, s99
	s_add_i32 s99, s99, 1
	v_addc_co_u32_e32 v2, vcc, 0, v2, vcc
	v_cmp_gt_i64_e32 vcc, s[22:23], v[8:9]
	v_readlane_b32 s23, v9, s99
	s_sub_i32 s22, 63, s99
	s_add_i32 s99, s99, 1
	v_addc_co_u32_e32 v2, vcc, 0, v2, vcc
	v_cmp_gt_i64_e32 vcc, s[24:25], v[8:9]
	v_readlane_b32 s25, v9, s99
	s_sub_i32 s24, 63, s99
	s_add_i32 s99, s99, 1
	v_addc_co_u32_e32 v2, vcc, 0, v2, vcc
	v_cmp_gt_i64_e32 vcc, s[22:23], v[8:9]
	v_readlane_b32 s23, v9, s99
	s_sub_i32 s22, 63, s99
	s_add_i32 s99, s99, 1
	v_addc_co_u32_e32 v2, vcc, 0, v2, vcc
	v_cmp_gt_i64_e32 vcc, s[24:25], v[8:9]
	v_readlane_b32 s25, v9, s99
	s_sub_i32 s24, 63, s99
	s_add_i32 s99, s99, 1
	v_addc_co_u32_e32 v2, vcc, 0, v2, vcc
	v_cmp_gt_i64_e32 vcc, s[22:23], v[8:9]
	v_readlane_b32 s23, v9, s99
	s_sub_i32 s22, 63, s99
	s_add_i32 s99, s99, 1
; __device__ __forceinline__ void phase_nrr(const Frame& F, const Args& a, int l, const bf16_t* XA, const float* g, const float* modl, unsigned char* XN8) {
;     ...
;             const bool keep = grank < 4; const float val = keep ? bb : -INFINITY;
;             int rank = 0;
; #pragma unroll 8
;             for (int e2 = 0; e2 < 64; ++e2) { const float v = __int_as_float(__builtin_amdgcn_readlane(__float_as_int(val), e2)); rank += (v > val || (v == val && e2 < lane)) ? 1 : 0; }
;             const bool sel = rank < TOPK;
;             const float ssum = wave_sum(sel ? sc : 0.f);
;             if (sel) { const int p = atomicAdd((int*)(hist + lane), 1); top_e[t * TOPK + rank] = lane; gate[t * TOPK + rank] = sc / ssum * 2.5f; lpos[t * TOPK + rank] = p; }
	v_addc_co_u32_e32 v2, vcc, 0, v2, vcc
	v_cmp_gt_i64_e32 vcc, s[24:25], v[8:9]
	v_readlane_b32 s25, v9, s99
	s_sub_i32 s24, 63, s99
	s_add_i32 s99, s99, 1
	v_addc_co_u32_e32 v2, vcc, 0, v2, vcc
	v_cmp_gt_i64_e32 vcc, s[22:23], v[8:9]
	v_readlane_b32 s23, v9, s99
	s_sub_i32 s22, 63, s99
	s_nop 0
	v_addc_co_u32_e32 v2, vcc, 0, v2, vcc
	v_cmp_gt_i64_e32 vcc, s[24:25], v[8:9]
	v_readlane_b32 s25, v9, s100
	s_sub_i32 s24, 63, s100
	s_add_i32 s100, s100, 1
	v_addc_co_u32_e32 v2, vcc, 0, v2, vcc
	v_cmp_gt_i64_e32 vcc, s[22:23], v[8:9]
	v_readlane_b32 s23, v9, s100
	s_sub_i32 s22, 63, s100
	s_add_i32 s100, s100, 1
	v_addc_co_u32_e32 v2, vcc, 0, v2, vcc
	v_cmp_gt_i64_e32 vcc, s[24:25], v[8:9]
	v_readlane_b32 s25, v9, s100
	s_sub_i32 s24, 63, s100
	s_add_i32 s100, s100, 1
	v_addc_co_u32_e32 v2, vcc, 0, v2, vcc
	v_cmp_gt_i64_e32 vcc, s[22:23], v[8:9]
	v_readlane_b32 s23, v9, s100
	s_sub_i32 s22, 63, s100
	s_add_i32 s100, s100, 1
	v_addc_co_u32_e32 v2, vcc, 0, v2, vcc
	v_cmp_gt_i64_e32 vcc, s[24:25], v[8:9]
	v_readlane_b32 s25, v9, s100
	s_sub_i32 s24, 63, s100
	s_add_i32 s100, s100, 1
	v_addc_co_u32_e32 v2, vcc, 0, v2, vcc
	v_cmp_gt_i64_e32 vcc, s[22:23], v[8:9]
	v_readlane_b32 s23, v9, s100
	s_sub_i32 s22, 63, s100
	s_add_i32 s100, s100, 1
	v_addc_co_u32_e32 v2, vcc, 0, v2, vcc
	v_cmp_gt_i64_e32 vcc, s[24:25], v[8:9]
	v_readlane_b32 s25, v9, s100
	s_sub_i32 s24, 63, s100
	s_add_i32 s100, s100, 1
	v_addc_co_u32_e32 v2, vcc, 0, v2, vcc
	v_cmp_gt_i64_e32 vcc, s[22:23], v[8:9]
	v_readlane_b32 s23, v9, s100
	s_sub_i32 s22, 63, s100
	s_nop 0
	v_addc_co_u32_e32 v2, vcc, 0, v2, vcc
	v_cmp_gt_i64_e32 vcc, s[24:25], v[8:9]
	v_readlane_b32 s25, v9, s101
	s_sub_i32 s24, 63, s101
	s_add_i32 s101, s101, 1
	v_addc_co_u32_e32 v2, vcc, 0, v2, vcc
	v_cmp_gt_i64_e32 vcc, s[22:23], v[8:9]
	v_readlane_b32 s23, v9, s101
	s_sub_i32 s22, 63, s101
	s_add_i32 s101, s101, 1
	v_addc_co_u32_e32 v2, vcc, 0, v2, vcc
	v_cmp_gt_i64_e32 vcc, s[24:25], v[8:9]
	v_readlane_b32 s25, v9, s101
	s_sub_i32 s24, 63, s101
	s_add_i32 s101, s101, 1
	v_addc_co_u32_e32 v2, vcc, 0, v2, vcc
	v_cmp_gt_i64_e32 vcc, s[22:23], v[8:9]
	v_readlane_b32 s23, v9, s101
	s_sub_i32 s22, 63, s101
	s_add_i32 s101, s101, 1
	v_addc_co_u32_e32 v2, vcc, 0, v2, vcc
	v_cmp_gt_i64_e32 vcc, s[24:25], v[8:9]
	v_readlane_b32 s25, v9, s101
	s_sub_i32 s24, 63, s101
	s_add_i32 s101, s101, 1
	v_addc_co_u32_e32 v2, vcc, 0, v2, vcc
	v_cmp_gt_i64_e32 vcc, s[22:23], v[8:9]
	v_readlane_b32 s23, v9, s101
	s_sub_i32 s22, 63, s101
	s_add_i32 s101, s101, 1
	v_addc_co_u32_e32 v2, vcc, 0, v2, vcc
	v_cmp_gt_i64_e32 vcc, s[24:25], v[8:9]
	v_readlane_b32 s25, v9, s101
	s_sub_i32 s24, 63, s101
	s_add_i32 s101, s101, 1
	v_addc_co_u32_e32 v2, vcc, 0, v2, vcc
	v_cmp_gt_i64_e32 vcc, s[22:23], v[8:9]
	v_readlane_b32 s23, v9, s101
	s_sub_i32 s22, 63, s101
	s_nop 0
	v_addc_co_u32_e32 v2, vcc, 0, v2, vcc
	v_cmp_gt_i64_e32 vcc, s[24:25], v[8:9]
	s_nop 1
	v_addc_co_u32_e32 v2, vcc, 0, v2, vcc
	v_cmp_gt_i64_e32 vcc, s[22:23], v[8:9]
	s_nop 1
	v_addc_co_u32_e32 v2, vcc, 0, v2, vcc
	v_cmp_gt_u32_e32 vcc, 6, v2
	s_nop 1
	v_cndmask_b32_e32 v6, 0, v5, vcc
	s_nop 1
	v_add_f32_dpp v6, v6, v6 quad_perm:[1,0,3,2] row_mask:0xf bank_mask:0xf
	s_nop 1
	v_add_f32_dpp v6, v6, v6 quad_perm:[2,3,0,1] row_mask:0xf bank_mask:0xf
	s_nop 1
	v_add_f32_dpp v6, v6, v6 row_half_mirror row_mask:0xf bank_mask:0xf
	s_nop 1
	v_add_f32_dpp v6, v6, v6 row_mirror row_mask:0xf bank_mask:0xf
	v_mov_b32_e32 v7, v6
	s_nop 1
	v_permlane16_swap_b32_e32 v7, v6
	s_waitcnt lgkmcnt(0)
	v_add_f32_e32 v6, v6, v7
	v_mov_b32_e32 v7, v6
	s_nop 1
	v_permlane32_swap_b32_e32 v7, v6
	s_and_saveexec_b64 s[22:23], vcc
	s_cbranch_execz .LBB0_547
	s_waitcnt lgkmcnt(0)
	v_add_f32_e32 v10, v6, v7
	v_mad_u64_u32 v[6:7], s[24:25], s40, 6, v[2:3]
	v_div_scale_f32 v2, s[24:25], v10, v10, v5
	v_rcp_f32_e32 v12, v2
	v_ashrrev_i32_e32 v7, 31, v6
	v_lshlrev_b64 v[6:7], 2, v[6:7]
	v_lshl_add_u64 v[8:9], s[26:27], 0, v[6:7]
	ds_add_rtn_u32 v11, v227, v243
	global_store_dword v[8:9], v230, off
	v_fma_f32 v8, -v2, v12, 1.0
	v_fmac_f32_e32 v12, v8, v12
	v_div_scale_f32 v8, vcc, v5, v10, v5
	v_mul_f32_e32 v9, v8, v12
	v_fma_f32 v13, -v2, v9, v8
	v_fmac_f32_e32 v9, v13, v12
	v_fma_f32 v2, -v2, v9, v8
	v_div_fmas_f32 v2, v2, v12, v9
	v_div_fixup_f32 v2, v2, v10, v5
	v_mul_f32_e32 v2, 0x40200000, v2
	v_lshl_add_u64 v[8:9], s[28:29], 0, v[6:7]
	v_lshl_add_u64 v[6:7], s[30:31], 0, v[6:7]
	global_store_dword v[8:9], v2, off
	s_waitcnt lgkmcnt(0)
	global_store_dword v[6:7], v11, off
; __device__ __forceinline__ void phase_nrr(const Frame& F, const Args& a, int l, const bf16_t* XA, const float* g, const float* modl, unsigned char* XN8) {
;     ...
;         for (int i = 0; i < 8; ++i) { const int t = tb + i;
;             const float lg = Pl[(w * 8 + i) * NE + lane] + Pl[(64 + w * 8 + i) * NE + lane]; const float sc = 1.f / (1.f + __expf(-lg)); const float bb = sc + bias;
;             float m1 = bb; m1 = fmaxf(m1, __shfl_xor(m1, 1)); m1 = fmaxf(m1, __shfl_xor(m1, 2)); m1 = fmaxf(m1, __shfl_xor(m1, 4));
;             const unsigned long long eq = __ballot(bb == m1); const int gbase = lane & ~7; const unsigned grpmask = (unsigned)((eq >> gbase) & 0xffull);
;             const int first = gbase + __builtin_ctz(grpmask);
;             float m2 = (lane == first) ? -INFINITY : bb; m2 = fmaxf(m2, __shfl_xor(m2, 1)); m2 = fmaxf(m2, __shfl_xor(m2, 2)); m2 = fmaxf(m2, __shfl_xor(m2, 4));
;             const float gsum = m1 + m2; const int gq = lane >> 3;
;             int grank = 0;
; #pragma unroll
;             for (int g2 = 0; g2 < 8; ++g2) { const float v = __int_as_float(__builtin_amdgcn_readlane(__float_as_int(gsum), g2 * 8)); grank += (v > gsum || (v == gsum && g2 < gq)) ? 1 : 0; }
;             const bool keep = grank < 4; const float val = keep ? bb : -INFINITY;
;             int rank = 0;
; #pragma unroll 8
;             for (int e2 = 0; e2 < 64; ++e2) { const float v = __int_as_float(__builtin_amdgcn_readlane(__float_as_int(val), e2)); rank += (v > val || (v == val && e2 < lane)) ? 1 : 0; }
.LBB0_547:
	s_or_b64 exec, exec, s[22:23]
	v_add_u32_e32 v2, s79, v226
	ds_read_b32 v2, v2
	ds_read_b32 v5, v4 offset:17152
	s_mov_b32 s3, 0
	s_waitcnt lgkmcnt(0)
	v_add_f32_e32 v2, v2, v5
	v_mul_f32_e32 v2, 0xbfb8aa3b, v2
	v_exp_f32_e32 v2, v2
	s_nop 0
	v_add_f32_e32 v2, 1.0, v2
	v_div_scale_f32 v5, s[22:23], v2, v2, 1.0
	v_rcp_f32_e32 v6, v5
	s_nop 0
	v_fma_f32 v7, -v5, v6, 1.0
	v_fmac_f32_e32 v6, v7, v6
	v_div_scale_f32 v7, vcc, 1.0, v2, 1.0
	v_mul_f32_e32 v8, v7, v6
	v_fma_f32 v9, -v5, v8, v7
	v_fmac_f32_e32 v8, v9, v6
	v_fma_f32 v5, -v5, v8, v7
	v_div_fmas_f32 v5, v5, v6, v8
	v_div_fixup_f32 v5, v5, v2, 1.0
	v_add_f32_e32 v2, v3, v5
	s_nop 1
	s_waitcnt lgkmcnt(0)
	v_max_f32_dpp v6, v2, v2 quad_perm:[1,0,3,2] row_mask:0xf bank_mask:0xf
	s_nop 1
	s_waitcnt lgkmcnt(0)
	v_max_f32_dpp v6, v6, v6 quad_perm:[2,3,0,1] row_mask:0xf bank_mask:0xf
	s_nop 1
	s_waitcnt lgkmcnt(0)
	v_max_f32_dpp v8, v6, v6 row_half_mirror row_mask:0xf bank_mask:0xf
	v_cmp_eq_f32_e32 vcc, v2, v8
	s_nop 1
	v_lshrrev_b64 v[6:7], v200, vcc
	v_ffbl_b32_sdwa v6, v6 dst_sel:DWORD dst_unused:UNUSED_PAD src0_sel:BYTE_0
	v_add_u32_e32 v6, v6, v200
	v_cmp_ne_u32_e32 vcc, v230, v6
	s_nop 1
	v_cndmask_b32_e32 v6, v245, v2, vcc
	s_nop 1
	s_waitcnt lgkmcnt(0)
	v_max_f32_dpp v6, v6, v6 quad_perm:[1,0,3,2] row_mask:0xf bank_mask:0xf
	s_nop 1
	s_waitcnt lgkmcnt(0)
	v_max_f32_dpp v6, v6, v6 quad_perm:[2,3,0,1] row_mask:0xf bank_mask:0xf
	s_nop 1
	s_waitcnt lgkmcnt(0)
	v_max_f32_dpp v6, v6, v6 row_half_mirror row_mask:0xf bank_mask:0xf
	v_add_f32_e32 v6, v8, v6
	s_nop 0
	v_readlane_b32 s5, v6, 0
	s_nop 1
	v_cmp_eq_f32_e64 s[22:23], s5, v6
	v_cmp_gt_f32_e32 vcc, s5, v6
	s_and_b64 s[22:23], s[6:7], s[22:23]
	s_or_b64 s[22:23], vcc, s[22:23]
	v_readlane_b32 s5, v6, 8
	v_cndmask_b32_e64 v7, 0, 1, s[22:23]
	s_nop 0
	v_cmp_eq_f32_e64 s[22:23], s5, v6
	v_cmp_gt_f32_e32 vcc, s5, v6
	s_and_b64 s[22:23], s[8:9], s[22:23]
	s_or_b64 s[22:23], vcc, s[22:23]
	v_readlane_b32 s5, v6, 16
	v_cndmask_b32_e64 v8, 0, 1, s[22:23]
	s_nop 0
	v_cmp_eq_f32_e64 s[22:23], s5, v6
	v_cmp_gt_f32_e32 vcc, s5, v6
	s_and_b64 s[22:23], s[10:11], s[22:23]
	s_or_b64 s[22:23], vcc, s[22:23]
	v_readlane_b32 s5, v6, 24
	v_cndmask_b32_e64 v9, 0, 1, s[22:23]
	s_nop 0
	v_cmp_eq_f32_e64 s[22:23], s5, v6
	v_cmp_gt_f32_e32 vcc, s5, v6
	s_and_b64 s[22:23], s[12:13], s[22:23]
	s_or_b64 s[22:23], vcc, s[22:23]
	v_readlane_b32 s5, v6, 32
	v_cndmask_b32_e64 v10, 0, 1, s[22:23]
	s_nop 0
	v_cmp_eq_f32_e64 s[22:23], s5, v6
	v_cmp_gt_f32_e32 vcc, s5, v6
	s_and_b64 s[22:23], s[14:15], s[22:23]
	s_or_b64 s[22:23], vcc, s[22:23]
	v_readlane_b32 s5, v6, 40
	v_cndmask_b32_e64 v11, 0, 1, s[22:23]
	s_nop 0
	v_cmp_eq_f32_e64 s[22:23], s5, v6
	v_cmp_gt_f32_e32 vcc, s5, v6
	s_and_b64 s[22:23], s[16:17], s[22:23]
	s_or_b64 s[22:23], vcc, s[22:23]
	v_readlane_b32 s5, v6, 48
	v_cndmask_b32_e64 v12, 0, 1, s[22:23]
	s_nop 0
	v_cmp_eq_f32_e64 s[22:23], s5, v6
	v_cmp_gt_f32_e32 vcc, s5, v6
	s_and_b64 s[22:23], s[18:19], s[22:23]
	v_readlane_b32 s5, v6, 56
	s_or_b64 s[22:23], vcc, s[22:23]
	v_cndmask_b32_e64 v13, 0, 1, s[22:23]
	v_cmp_gt_f32_e32 vcc, s5, v6
	s_nop 1
	v_cndmask_b32_e64 v6, 0, 1, vcc
	v_add_u32_e32 v6, v8, v6
	v_add3_u32 v6, v6, v7, v9
	v_add3_u32 v6, v6, v10, v11
	v_add3_u32 v6, v6, v12, v13
	v_cmp_eq_u32_e32 vcc, 0, v6
	s_ff1_i32_b64 s98, vcc
	v_cmp_eq_u32_e32 vcc, 1, v6
	s_ff1_i32_b64 s99, vcc
	v_cmp_eq_u32_e32 vcc, 2, v6
	s_ff1_i32_b64 s100, vcc
	v_cmp_eq_u32_e32 vcc, 3, v6
	s_ff1_i32_b64 s101, vcc
	v_cmp_gt_u32_e32 vcc, 4, v6
	s_nop 1
	v_cndmask_b32_e32 v6, v245, v2, vcc
	v_mov_b32_e32 v2, 0
	v_ashrrev_i32_e32 v9, 31, v6
	v_sub_u32_e32 v8, 63, v230
	v_and_b32_e32 v9, 0x7fffffff, v9
	v_xor_b32_e32 v9, v6, v9
	s_nop 0
	v_readlane_b32 s25, v9, s98
	s_sub_i32 s24, 63, s98
	s_add_i32 s98, s98, 1
	v_readlane_b32 s23, v9, s98
	s_sub_i32 s22, 63, s98
	s_add_i32 s98, s98, 1
	v_cmp_gt_i64_e32 vcc, s[24:25], v[8:9]
	v_readlane_b32 s25, v9, s98
	s_sub_i32 s24, 63, s98
	s_add_i32 s98, s98, 1
	v_addc_co_u32_e32 v2, vcc, 0, v2, vcc
	v_cmp_gt_i64_e32 vcc, s[22:23], v[8:9]
	v_readlane_b32 s23, v9, s98
	s_sub_i32 s22, 63, s98
	s_add_i32 s98, s98, 1
	v_addc_co_u32_e32 v2, vcc, 0, v2, vcc
	v_cmp_gt_i64_e32 vcc, s[24:25], v[8:9]
	v_readlane_b32 s25, v9, s98
	s_sub_i32 s24, 63, s98
	s_add_i32 s98, s98, 1
	v_addc_co_u32_e32 v2, vcc, 0, v2, vcc
	v_cmp_gt_i64_e32 vcc, s[22:23], v[8:9]
	v_readlane_b32 s23, v9, s98
	s_sub_i32 s22, 63, s98
	s_add_i32 s98, s98, 1
	v_addc_co_u32_e32 v2, vcc, 0, v2, vcc
	v_cmp_gt_i64_e32 vcc, s[24:25], v[8:9]
	v_readlane_b32 s25, v9, s98
	s_sub_i32 s24, 63, s98
	s_add_i32 s98, s98, 1
	v_addc_co_u32_e32 v2, vcc, 0, v2, vcc
	v_cmp_gt_i64_e32 vcc, s[22:23], v[8:9]
	v_readlane_b32 s23, v9, s98
	s_sub_i32 s22, 63, s98
	s_nop 0
	v_addc_co_u32_e32 v2, vcc, 0, v2, vcc
	v_cmp_gt_i64_e32 vcc, s[24:25], v[8:9]
	v_readlane_b32 s25, v9, s99
	s_sub_i32 s24, 63, s99
	s_add_i32 s99, s99, 1
	v_addc_co_u32_e32 v2, vcc, 0, v2, vcc
	v_cmp_gt_i64_e32 vcc, s[22:23], v[8:9]
	v_readlane_b32 s23, v9, s99
	s_sub_i32 s22, 63, s99
	s_add_i32 s99, s99, 1
	v_addc_co_u32_e32 v2, vcc, 0, v2, vcc
	v_cmp_gt_i64_e32 vcc, s[24:25], v[8:9]
	v_readlane_b32 s25, v9, s99
	s_sub_i32 s24, 63, s99
	s_add_i32 s99, s99, 1
	v_addc_co_u32_e32 v2, vcc, 0, v2, vcc
	v_cmp_gt_i64_e32 vcc, s[22:23], v[8:9]
	v_readlane_b32 s23, v9, s99
	s_sub_i32 s22, 63, s99
	s_add_i32 s99, s99, 1
	v_addc_co_u32_e32 v2, vcc, 0, v2, vcc
	v_cmp_gt_i64_e32 vcc, s[24:25], v[8:9]
	v_readlane_b32 s25, v9, s99
	s_sub_i32 s24, 63, s99
	s_add_i32 s99, s99, 1
	v_addc_co_u32_e32 v2, vcc, 0, v2, vcc
	v_cmp_gt_i64_e32 vcc, s[22:23], v[8:9]
	v_readlane_b32 s23, v9, s99
	s_sub_i32 s22, 63, s99
	s_add_i32 s99, s99, 1
; __device__ __forceinline__ void phase_nrr(const Frame& F, const Args& a, int l, const bf16_t* XA, const float* g, const float* modl, unsigned char* XN8) {
;     ...
;             const bool keep = grank < 4; const float val = keep ? bb : -INFINITY;
;             int rank = 0;
; #pragma unroll 8
;             for (int e2 = 0; e2 < 64; ++e2) { const float v = __int_as_float(__builtin_amdgcn_readlane(__float_as_int(val), e2)); rank += (v > val || (v == val && e2 < lane)) ? 1 : 0; }
;             const bool sel = rank < TOPK;
;             const float ssum = wave_sum(sel ? sc : 0.f);
;             if (sel) { const int p = atomicAdd((int*)(hist + lane), 1); top_e[t * TOPK + rank] = lane; gate[t * TOPK + rank] = sc / ssum * 2.5f; lpos[t * TOPK + rank] = p; }
	v_addc_co_u32_e32 v2, vcc, 0, v2, vcc
	v_cmp_gt_i64_e32 vcc, s[24:25], v[8:9]
	v_readlane_b32 s25, v9, s99
	s_sub_i32 s24, 63, s99
	s_add_i32 s99, s99, 1
	v_addc_co_u32_e32 v2, vcc, 0, v2, vcc
	v_cmp_gt_i64_e32 vcc, s[22:23], v[8:9]
	v_readlane_b32 s23, v9, s99
	s_sub_i32 s22, 63, s99
	s_nop 0
	v_addc_co_u32_e32 v2, vcc, 0, v2, vcc
	v_cmp_gt_i64_e32 vcc, s[24:25], v[8:9]
	v_readlane_b32 s25, v9, s100
	s_sub_i32 s24, 63, s100
	s_add_i32 s100, s100, 1
	v_addc_co_u32_e32 v2, vcc, 0, v2, vcc
	v_cmp_gt_i64_e32 vcc, s[22:23], v[8:9]
	v_readlane_b32 s23, v9, s100
	s_sub_i32 s22, 63, s100
	s_add_i32 s100, s100, 1
	v_addc_co_u32_e32 v2, vcc, 0, v2, vcc
	v_cmp_gt_i64_e32 vcc, s[24:25], v[8:9]
	v_readlane_b32 s25, v9, s100
	s_sub_i32 s24, 63, s100
	s_add_i32 s100, s100, 1
	v_addc_co_u32_e32 v2, vcc, 0, v2, vcc
	v_cmp_gt_i64_e32 vcc, s[22:23], v[8:9]
	v_readlane_b32 s23, v9, s100
	s_sub_i32 s22, 63, s100
	s_add_i32 s100, s100, 1
	v_addc_co_u32_e32 v2, vcc, 0, v2, vcc
	v_cmp_gt_i64_e32 vcc, s[24:25], v[8:9]
	v_readlane_b32 s25, v9, s100
	s_sub_i32 s24, 63, s100
	s_add_i32 s100, s100, 1
	v_addc_co_u32_e32 v2, vcc, 0, v2, vcc
	v_cmp_gt_i64_e32 vcc, s[22:23], v[8:9]
	v_readlane_b32 s23, v9, s100
	s_sub_i32 s22, 63, s100
	s_add_i32 s100, s100, 1
	v_addc_co_u32_e32 v2, vcc, 0, v2, vcc
	v_cmp_gt_i64_e32 vcc, s[24:25], v[8:9]
	v_readlane_b32 s25, v9, s100
	s_sub_i32 s24, 63, s100
	s_add_i32 s100, s100, 1
	v_addc_co_u32_e32 v2, vcc, 0, v2, vcc
	v_cmp_gt_i64_e32 vcc, s[22:23], v[8:9]
	v_readlane_b32 s23, v9, s100
	s_sub_i32 s22, 63, s100
	s_nop 0
	v_addc_co_u32_e32 v2, vcc, 0, v2, vcc
	v_cmp_gt_i64_e32 vcc, s[24:25], v[8:9]
	v_readlane_b32 s25, v9, s101
	s_sub_i32 s24, 63, s101
	s_add_i32 s101, s101, 1
	v_addc_co_u32_e32 v2, vcc, 0, v2, vcc
	v_cmp_gt_i64_e32 vcc, s[22:23], v[8:9]
	v_readlane_b32 s23, v9, s101
	s_sub_i32 s22, 63, s101
	s_add_i32 s101, s101, 1
	v_addc_co_u32_e32 v2, vcc, 0, v2, vcc
	v_cmp_gt_i64_e32 vcc, s[24:25], v[8:9]
	v_readlane_b32 s25, v9, s101
	s_sub_i32 s24, 63, s101
	s_add_i32 s101, s101, 1
	v_addc_co_u32_e32 v2, vcc, 0, v2, vcc
	v_cmp_gt_i64_e32 vcc, s[22:23], v[8:9]
	v_readlane_b32 s23, v9, s101
	s_sub_i32 s22, 63, s101
	s_add_i32 s101, s101, 1
	v_addc_co_u32_e32 v2, vcc, 0, v2, vcc
	v_cmp_gt_i64_e32 vcc, s[24:25], v[8:9]
	v_readlane_b32 s25, v9, s101
	s_sub_i32 s24, 63, s101
	s_add_i32 s101, s101, 1
	v_addc_co_u32_e32 v2, vcc, 0, v2, vcc
	v_cmp_gt_i64_e32 vcc, s[22:23], v[8:9]
	v_readlane_b32 s23, v9, s101
	s_sub_i32 s22, 63, s101
	s_add_i32 s101, s101, 1
	v_addc_co_u32_e32 v2, vcc, 0, v2, vcc
	v_cmp_gt_i64_e32 vcc, s[24:25], v[8:9]
	v_readlane_b32 s25, v9, s101
	s_sub_i32 s24, 63, s101
	s_add_i32 s101, s101, 1
	v_addc_co_u32_e32 v2, vcc, 0, v2, vcc
	v_cmp_gt_i64_e32 vcc, s[22:23], v[8:9]
	v_readlane_b32 s23, v9, s101
	s_sub_i32 s22, 63, s101
	s_nop 0
	v_addc_co_u32_e32 v2, vcc, 0, v2, vcc
	v_cmp_gt_i64_e32 vcc, s[24:25], v[8:9]
	s_nop 1
	v_addc_co_u32_e32 v2, vcc, 0, v2, vcc
	v_cmp_gt_i64_e32 vcc, s[22:23], v[8:9]
	s_nop 1
	v_addc_co_u32_e32 v2, vcc, 0, v2, vcc
	v_cmp_gt_u32_e32 vcc, 6, v2
	s_nop 1
	v_cndmask_b32_e32 v6, 0, v5, vcc
	s_nop 1
	v_add_f32_dpp v6, v6, v6 quad_perm:[1,0,3,2] row_mask:0xf bank_mask:0xf
	s_nop 1
	v_add_f32_dpp v6, v6, v6 quad_perm:[2,3,0,1] row_mask:0xf bank_mask:0xf
	s_nop 1
	v_add_f32_dpp v6, v6, v6 row_half_mirror row_mask:0xf bank_mask:0xf
	s_nop 1
	v_add_f32_dpp v6, v6, v6 row_mirror row_mask:0xf bank_mask:0xf
	v_mov_b32_e32 v7, v6
	s_nop 1
	v_permlane16_swap_b32_e32 v7, v6
	s_waitcnt lgkmcnt(0)
	v_add_f32_e32 v6, v6, v7
	v_mov_b32_e32 v7, v6
	s_nop 1
	v_permlane32_swap_b32_e32 v7, v6
	s_and_saveexec_b64 s[22:23], vcc
	s_cbranch_execz .LBB0_551
	s_waitcnt lgkmcnt(0)
	v_add_f32_e32 v10, v6, v7
	v_mad_u64_u32 v[6:7], s[4:5], s4, 6, v[2:3]
	v_div_scale_f32 v2, s[4:5], v10, v10, v5
	v_rcp_f32_e32 v12, v2
	v_ashrrev_i32_e32 v7, 31, v6
	v_lshlrev_b64 v[6:7], 2, v[6:7]
	v_lshl_add_u64 v[8:9], s[26:27], 0, v[6:7]
	ds_add_rtn_u32 v11, v227, v243
	global_store_dword v[8:9], v230, off
	v_fma_f32 v8, -v2, v12, 1.0
	v_fmac_f32_e32 v12, v8, v12
	v_div_scale_f32 v8, vcc, v5, v10, v5
	v_mul_f32_e32 v9, v8, v12
	v_fma_f32 v13, -v2, v9, v8
	v_fmac_f32_e32 v9, v13, v12
	v_fma_f32 v2, -v2, v9, v8
	v_div_fmas_f32 v2, v2, v12, v9
	v_div_fixup_f32 v2, v2, v10, v5
	v_mul_f32_e32 v2, 0x40200000, v2
	v_lshl_add_u64 v[8:9], s[28:29], 0, v[6:7]
	v_lshl_add_u64 v[6:7], s[30:31], 0, v[6:7]
	global_store_dword v[8:9], v2, off
	s_waitcnt lgkmcnt(0)
	global_store_dword v[6:7], v11, off
; __device__ __forceinline__ void phase_nrr(const Frame& F, const Args& a, int l, const bf16_t* XA, const float* g, const float* modl, unsigned char* XN8) {
;     ...
;         for (int i = 0; i < 8; ++i) { const int t = tb + i;
;             const float lg = Pl[(w * 8 + i) * NE + lane] + Pl[(64 + w * 8 + i) * NE + lane]; const float sc = 1.f / (1.f + __expf(-lg)); const float bb = sc + bias;
;             float m1 = bb; m1 = fmaxf(m1, __shfl_xor(m1, 1)); m1 = fmaxf(m1, __shfl_xor(m1, 2)); m1 = fmaxf(m1, __shfl_xor(m1, 4));
;             const unsigned long long eq = __ballot(bb == m1); const int gbase = lane & ~7; const unsigned grpmask = (unsigned)((eq >> gbase) & 0xffull);
;             const int first = gbase + __builtin_ctz(grpmask);
;             float m2 = (lane == first) ? -INFINITY : bb; m2 = fmaxf(m2, __shfl_xor(m2, 1)); m2 = fmaxf(m2, __shfl_xor(m2, 2)); m2 = fmaxf(m2, __shfl_xor(m2, 4));
;             const float gsum = m1 + m2; const int gq = lane >> 3;
;             int grank = 0;
; #pragma unroll
;             for (int g2 = 0; g2 < 8; ++g2) { const float v = __int_as_float(__builtin_amdgcn_readlane(__float_as_int(gsum), g2 * 8)); grank += (v > gsum || (v == gsum && g2 < gq)) ? 1 : 0; }
;             const bool keep = grank < 4; const float val = keep ? bb : -INFINITY;
;             int rank = 0;
; #pragma unroll 8
;             for (int e2 = 0; e2 < 64; ++e2) { const float v = __int_as_float(__builtin_amdgcn_readlane(__float_as_int(val), e2)); rank += (v > val || (v == val && e2 < lane)) ? 1 : 0; }
.LBB0_551:
	s_or_b64 exec, exec, s[22:23]
	v_add_u32_e32 v2, s84, v226
	ds_read_b32 v2, v2
	ds_read_b32 v5, v4 offset:17408
	s_mov_b32 s3, 0
	s_waitcnt lgkmcnt(0)
	v_add_f32_e32 v2, v2, v5
	v_mul_f32_e32 v2, 0xbfb8aa3b, v2
	v_exp_f32_e32 v2, v2
	s_nop 0
	v_add_f32_e32 v2, 1.0, v2
	v_div_scale_f32 v5, s[4:5], v2, v2, 1.0
	v_rcp_f32_e32 v6, v5
	s_nop 0
	v_fma_f32 v7, -v5, v6, 1.0
	v_fmac_f32_e32 v6, v7, v6
	v_div_scale_f32 v7, vcc, 1.0, v2, 1.0
	v_mul_f32_e32 v8, v7, v6
	v_fma_f32 v9, -v5, v8, v7
	v_fmac_f32_e32 v8, v9, v6
	v_fma_f32 v5, -v5, v8, v7
	v_div_fmas_f32 v5, v5, v6, v8
	v_div_fixup_f32 v2, v5, v2, 1.0
	v_add_f32_e32 v5, v3, v2
	s_nop 1
	s_waitcnt lgkmcnt(0)
	v_max_f32_dpp v6, v5, v5 quad_perm:[1,0,3,2] row_mask:0xf bank_mask:0xf
	s_nop 1
	s_waitcnt lgkmcnt(0)
	v_max_f32_dpp v6, v6, v6 quad_perm:[2,3,0,1] row_mask:0xf bank_mask:0xf
	s_nop 1
	s_waitcnt lgkmcnt(0)
	v_max_f32_dpp v8, v6, v6 row_half_mirror row_mask:0xf bank_mask:0xf
	v_cmp_eq_f32_e32 vcc, v5, v8
	s_nop 1
	v_lshrrev_b64 v[6:7], v200, vcc
	v_ffbl_b32_sdwa v6, v6 dst_sel:DWORD dst_unused:UNUSED_PAD src0_sel:BYTE_0
	v_add_u32_e32 v6, v6, v200
	v_cmp_ne_u32_e32 vcc, v230, v6
	s_nop 1
	v_cndmask_b32_e32 v6, v245, v5, vcc
	s_nop 1
	s_waitcnt lgkmcnt(0)
	v_max_f32_dpp v6, v6, v6 quad_perm:[1,0,3,2] row_mask:0xf bank_mask:0xf
	s_nop 1
	s_waitcnt lgkmcnt(0)
	v_max_f32_dpp v6, v6, v6 quad_perm:[2,3,0,1] row_mask:0xf bank_mask:0xf
	s_nop 1
	s_waitcnt lgkmcnt(0)
	v_max_f32_dpp v6, v6, v6 row_half_mirror row_mask:0xf bank_mask:0xf
	v_add_f32_e32 v6, v8, v6
	s_nop 0
	v_readlane_b32 s4, v6, 0
	s_nop 1
	v_cmp_eq_f32_e64 s[22:23], s4, v6
	v_cmp_gt_f32_e32 vcc, s4, v6
	s_and_b64 s[4:5], s[6:7], s[22:23]
	s_or_b64 s[4:5], vcc, s[4:5]
	v_cndmask_b32_e64 v7, 0, 1, s[4:5]
	v_readlane_b32 s4, v6, 8
	s_nop 1
	v_cmp_eq_f32_e64 s[22:23], s4, v6
	v_cmp_gt_f32_e32 vcc, s4, v6
	s_and_b64 s[4:5], s[8:9], s[22:23]
	s_or_b64 s[4:5], vcc, s[4:5]
	v_cndmask_b32_e64 v8, 0, 1, s[4:5]
	v_readlane_b32 s4, v6, 16
	s_nop 1
	v_cmp_eq_f32_e64 s[22:23], s4, v6
	v_cmp_gt_f32_e32 vcc, s4, v6
	s_and_b64 s[4:5], s[10:11], s[22:23]
	s_or_b64 s[4:5], vcc, s[4:5]
	v_cndmask_b32_e64 v9, 0, 1, s[4:5]
	v_readlane_b32 s4, v6, 24
	s_nop 1
	v_cmp_eq_f32_e64 s[22:23], s4, v6
	v_cmp_gt_f32_e32 vcc, s4, v6
	s_and_b64 s[4:5], s[12:13], s[22:23]
	s_or_b64 s[4:5], vcc, s[4:5]
	v_cndmask_b32_e64 v10, 0, 1, s[4:5]
	v_readlane_b32 s4, v6, 32
	s_nop 1
	v_cmp_eq_f32_e64 s[22:23], s4, v6
	v_cmp_gt_f32_e32 vcc, s4, v6
	s_and_b64 s[4:5], s[14:15], s[22:23]
	s_or_b64 s[4:5], vcc, s[4:5]
	v_cndmask_b32_e64 v11, 0, 1, s[4:5]
	v_readlane_b32 s4, v6, 40
	s_nop 1
	v_cmp_eq_f32_e64 s[22:23], s4, v6
	v_cmp_gt_f32_e32 vcc, s4, v6
	s_and_b64 s[4:5], s[16:17], s[22:23]
	s_or_b64 s[4:5], vcc, s[4:5]
	v_cndmask_b32_e64 v12, 0, 1, s[4:5]
	v_readlane_b32 s4, v6, 48
	s_nop 1
	v_cmp_eq_f32_e64 s[22:23], s4, v6
	v_cmp_gt_f32_e32 vcc, s4, v6
	s_and_b64 s[4:5], s[18:19], s[22:23]
	s_or_b64 s[4:5], vcc, s[4:5]
	v_cndmask_b32_e64 v13, 0, 1, s[4:5]
	v_readlane_b32 s4, v6, 56
	s_nop 1
	v_cmp_gt_f32_e32 vcc, s4, v6
	s_nop 1
	v_cndmask_b32_e64 v6, 0, 1, vcc
	v_add_u32_e32 v6, v8, v6
	v_add3_u32 v6, v6, v7, v9
	v_add3_u32 v6, v6, v10, v11
	v_add3_u32 v6, v6, v12, v13
	v_cmp_eq_u32_e32 vcc, 0, v6
	s_ff1_i32_b64 s98, vcc
	v_cmp_eq_u32_e32 vcc, 1, v6
	s_ff1_i32_b64 s99, vcc
	v_cmp_eq_u32_e32 vcc, 2, v6
	s_ff1_i32_b64 s100, vcc
	v_cmp_eq_u32_e32 vcc, 3, v6
	s_ff1_i32_b64 s101, vcc
	v_cmp_gt_u32_e32 vcc, 4, v6
	v_mov_b32_e32 v6, 0
	s_nop 0
	v_cndmask_b32_e32 v5, v245, v5, vcc
	v_ashrrev_i32_e32 v9, 31, v5
	v_sub_u32_e32 v8, 63, v230
	v_and_b32_e32 v9, 0x7fffffff, v9
	v_xor_b32_e32 v9, v5, v9
	s_nop 0
	v_readlane_b32 s25, v9, s98
	s_sub_i32 s24, 63, s98
	s_add_i32 s98, s98, 1
	v_readlane_b32 s23, v9, s98
	s_sub_i32 s22, 63, s98
	s_add_i32 s98, s98, 1
	v_cmp_gt_i64_e32 vcc, s[24:25], v[8:9]
	v_readlane_b32 s25, v9, s98
	s_sub_i32 s24, 63, s98
	s_add_i32 s98, s98, 1
	v_addc_co_u32_e32 v6, vcc, 0, v6, vcc
	v_cmp_gt_i64_e32 vcc, s[22:23], v[8:9]
	v_readlane_b32 s23, v9, s98
	s_sub_i32 s22, 63, s98
	s_add_i32 s98, s98, 1
	v_addc_co_u32_e32 v6, vcc, 0, v6, vcc
	v_cmp_gt_i64_e32 vcc, s[24:25], v[8:9]
	v_readlane_b32 s25, v9, s98
	s_sub_i32 s24, 63, s98
	s_add_i32 s98, s98, 1
	v_addc_co_u32_e32 v6, vcc, 0, v6, vcc
	v_cmp_gt_i64_e32 vcc, s[22:23], v[8:9]
	v_readlane_b32 s23, v9, s98
	s_sub_i32 s22, 63, s98
	s_add_i32 s98, s98, 1
	v_addc_co_u32_e32 v6, vcc, 0, v6, vcc
	v_cmp_gt_i64_e32 vcc, s[24:25], v[8:9]
	v_readlane_b32 s25, v9, s98
	s_sub_i32 s24, 63, s98
	s_add_i32 s98, s98, 1
	v_addc_co_u32_e32 v6, vcc, 0, v6, vcc
	v_cmp_gt_i64_e32 vcc, s[22:23], v[8:9]
	v_readlane_b32 s23, v9, s98
	s_sub_i32 s22, 63, s98
	s_nop 0
	v_addc_co_u32_e32 v6, vcc, 0, v6, vcc
	v_cmp_gt_i64_e32 vcc, s[24:25], v[8:9]
	v_readlane_b32 s25, v9, s99
	s_sub_i32 s24, 63, s99
	s_add_i32 s99, s99, 1
	v_addc_co_u32_e32 v6, vcc, 0, v6, vcc
	v_cmp_gt_i64_e32 vcc, s[22:23], v[8:9]
	v_readlane_b32 s23, v9, s99
	s_sub_i32 s22, 63, s99
	s_add_i32 s99, s99, 1
	v_addc_co_u32_e32 v6, vcc, 0, v6, vcc
	v_cmp_gt_i64_e32 vcc, s[24:25], v[8:9]
	v_readlane_b32 s25, v9, s99
	s_sub_i32 s24, 63, s99
	s_add_i32 s99, s99, 1
	v_addc_co_u32_e32 v6, vcc, 0, v6, vcc
	v_cmp_gt_i64_e32 vcc, s[22:23], v[8:9]
	v_readlane_b32 s23, v9, s99
	s_sub_i32 s22, 63, s99
	s_add_i32 s99, s99, 1
	v_addc_co_u32_e32 v6, vcc, 0, v6, vcc
	v_cmp_gt_i64_e32 vcc, s[24:25], v[8:9]
	v_readlane_b32 s25, v9, s99
	s_sub_i32 s24, 63, s99
	s_add_i32 s99, s99, 1
	v_addc_co_u32_e32 v6, vcc, 0, v6, vcc
	v_cmp_gt_i64_e32 vcc, s[22:23], v[8:9]
	v_readlane_b32 s23, v9, s99
	s_sub_i32 s22, 63, s99
	s_add_i32 s99, s99, 1
	v_addc_co_u32_e32 v6, vcc, 0, v6, vcc
; __device__ __forceinline__ void phase_nrr(const Frame& F, const Args& a, int l, const bf16_t* XA, const float* g, const float* modl, unsigned char* XN8) {
;     ...
;             const bool keep = grank < 4; const float val = keep ? bb : -INFINITY;
;             int rank = 0;
; #pragma unroll 8
;             for (int e2 = 0; e2 < 64; ++e2) { const float v = __int_as_float(__builtin_amdgcn_readlane(__float_as_int(val), e2)); rank += (v > val || (v == val && e2 < lane)) ? 1 : 0; }
;             const bool sel = rank < TOPK;
;             const float ssum = wave_sum(sel ? sc : 0.f);
;             if (sel) { const int p = atomicAdd((int*)(hist + lane), 1); top_e[t * TOPK + rank] = lane; gate[t * TOPK + rank] = sc / ssum * 2.5f; lpos[t * TOPK + rank] = p; }
	v_cmp_gt_i64_e32 vcc, s[24:25], v[8:9]
	v_readlane_b32 s25, v9, s99
	s_sub_i32 s24, 63, s99
	s_add_i32 s99, s99, 1
	v_addc_co_u32_e32 v6, vcc, 0, v6, vcc
	v_cmp_gt_i64_e32 vcc, s[22:23], v[8:9]
	v_readlane_b32 s23, v9, s99
	s_sub_i32 s22, 63, s99
	s_nop 0
	v_addc_co_u32_e32 v6, vcc, 0, v6, vcc
	v_cmp_gt_i64_e32 vcc, s[24:25], v[8:9]
	v_readlane_b32 s25, v9, s100
	s_sub_i32 s24, 63, s100
	s_add_i32 s100, s100, 1
	v_addc_co_u32_e32 v6, vcc, 0, v6, vcc
	v_cmp_gt_i64_e32 vcc, s[22:23], v[8:9]
	v_readlane_b32 s23, v9, s100
	s_sub_i32 s22, 63, s100
	s_add_i32 s100, s100, 1
	v_addc_co_u32_e32 v6, vcc, 0, v6, vcc
	v_cmp_gt_i64_e32 vcc, s[24:25], v[8:9]
	v_readlane_b32 s25, v9, s100
	s_sub_i32 s24, 63, s100
	s_add_i32 s100, s100, 1
	v_addc_co_u32_e32 v6, vcc, 0, v6, vcc
	v_cmp_gt_i64_e32 vcc, s[22:23], v[8:9]
	v_readlane_b32 s23, v9, s100
	s_sub_i32 s22, 63, s100
	s_add_i32 s100, s100, 1
	v_addc_co_u32_e32 v6, vcc, 0, v6, vcc
	v_cmp_gt_i64_e32 vcc, s[24:25], v[8:9]
	v_readlane_b32 s25, v9, s100
	s_sub_i32 s24, 63, s100
	s_add_i32 s100, s100, 1
	v_addc_co_u32_e32 v6, vcc, 0, v6, vcc
	v_cmp_gt_i64_e32 vcc, s[22:23], v[8:9]
	v_readlane_b32 s23, v9, s100
	s_sub_i32 s22, 63, s100
	s_add_i32 s100, s100, 1
	v_addc_co_u32_e32 v6, vcc, 0, v6, vcc
	v_cmp_gt_i64_e32 vcc, s[24:25], v[8:9]
	v_readlane_b32 s25, v9, s100
	s_sub_i32 s24, 63, s100
	s_add_i32 s100, s100, 1
	v_addc_co_u32_e32 v6, vcc, 0, v6, vcc
	v_cmp_gt_i64_e32 vcc, s[22:23], v[8:9]
	v_readlane_b32 s23, v9, s100
	s_sub_i32 s22, 63, s100
	s_nop 0
	v_addc_co_u32_e32 v6, vcc, 0, v6, vcc
	v_cmp_gt_i64_e32 vcc, s[24:25], v[8:9]
	v_readlane_b32 s25, v9, s101
	s_sub_i32 s24, 63, s101
	s_add_i32 s101, s101, 1
	v_addc_co_u32_e32 v6, vcc, 0, v6, vcc
	v_cmp_gt_i64_e32 vcc, s[22:23], v[8:9]
	v_readlane_b32 s23, v9, s101
	s_sub_i32 s22, 63, s101
	s_add_i32 s101, s101, 1
	v_addc_co_u32_e32 v6, vcc, 0, v6, vcc
	v_cmp_gt_i64_e32 vcc, s[24:25], v[8:9]
	v_readlane_b32 s25, v9, s101
	s_sub_i32 s24, 63, s101
	s_add_i32 s101, s101, 1
	v_addc_co_u32_e32 v6, vcc, 0, v6, vcc
	v_cmp_gt_i64_e32 vcc, s[22:23], v[8:9]
	v_readlane_b32 s23, v9, s101
	s_sub_i32 s22, 63, s101
	s_add_i32 s101, s101, 1
	v_addc_co_u32_e32 v6, vcc, 0, v6, vcc
	v_cmp_gt_i64_e32 vcc, s[24:25], v[8:9]
	v_readlane_b32 s25, v9, s101
	s_sub_i32 s24, 63, s101
	s_add_i32 s101, s101, 1
	v_addc_co_u32_e32 v6, vcc, 0, v6, vcc
	v_cmp_gt_i64_e32 vcc, s[22:23], v[8:9]
	v_readlane_b32 s23, v9, s101
	s_sub_i32 s22, 63, s101
	s_add_i32 s101, s101, 1
	v_addc_co_u32_e32 v6, vcc, 0, v6, vcc
	v_cmp_gt_i64_e32 vcc, s[24:25], v[8:9]
	v_readlane_b32 s25, v9, s101
	s_sub_i32 s24, 63, s101
	s_add_i32 s101, s101, 1
	v_addc_co_u32_e32 v6, vcc, 0, v6, vcc
	v_cmp_gt_i64_e32 vcc, s[22:23], v[8:9]
	v_readlane_b32 s23, v9, s101
	s_sub_i32 s22, 63, s101
	s_nop 0
	v_addc_co_u32_e32 v6, vcc, 0, v6, vcc
	v_cmp_gt_i64_e32 vcc, s[24:25], v[8:9]
	s_nop 1
	v_addc_co_u32_e32 v6, vcc, 0, v6, vcc
	v_cmp_gt_i64_e32 vcc, s[22:23], v[8:9]
	s_nop 1
	v_addc_co_u32_e32 v6, vcc, 0, v6, vcc
	v_cmp_gt_u32_e32 vcc, 6, v6
	s_nop 1
	v_cndmask_b32_e32 v5, 0, v2, vcc
	s_nop 1
	v_add_f32_dpp v5, v5, v5 quad_perm:[1,0,3,2] row_mask:0xf bank_mask:0xf
	s_nop 1
	v_add_f32_dpp v5, v5, v5 quad_perm:[2,3,0,1] row_mask:0xf bank_mask:0xf
	s_nop 1
	v_add_f32_dpp v5, v5, v5 row_half_mirror row_mask:0xf bank_mask:0xf
	s_nop 1
	v_add_f32_dpp v5, v5, v5 row_mirror row_mask:0xf bank_mask:0xf
	v_mov_b32_e32 v7, v5
	s_nop 1
	v_permlane16_swap_b32_e32 v7, v5
	s_waitcnt lgkmcnt(0)
	v_add_f32_e32 v5, v5, v7
	v_mov_b32_e32 v7, v5
	s_nop 1
	v_permlane32_swap_b32_e32 v7, v5
	s_and_saveexec_b64 s[4:5], vcc
	s_cbranch_execz .LBB0_555
	s_waitcnt lgkmcnt(0)
	v_add_f32_e32 v5, v5, v7
	s_mul_i32 s2, s2, 6
	v_or_b32_e32 v6, s2, v6
	v_div_scale_f32 v11, s[2:3], v5, v5, v2
	v_rcp_f32_e32 v12, v11
	v_ashrrev_i32_e32 v7, 31, v6
	v_lshlrev_b64 v[6:7], 2, v[6:7]
	v_lshl_add_u64 v[8:9], s[26:27], 0, v[6:7]
	ds_add_rtn_u32 v10, v227, v243
	global_store_dword v[8:9], v230, off
	v_fma_f32 v8, -v11, v12, 1.0
	v_fmac_f32_e32 v12, v8, v12
	v_div_scale_f32 v8, vcc, v2, v5, v2
	v_mul_f32_e32 v9, v8, v12
	v_fma_f32 v13, -v11, v9, v8
	v_fmac_f32_e32 v9, v13, v12
	v_fma_f32 v8, -v11, v9, v8
	v_div_fmas_f32 v8, v8, v12, v9
	v_div_fixup_f32 v2, v8, v5, v2
	v_mul_f32_e32 v2, 0x40200000, v2
	v_lshl_add_u64 v[8:9], s[28:29], 0, v[6:7]
	v_lshl_add_u64 v[6:7], s[30:31], 0, v[6:7]
	global_store_dword v[8:9], v2, off
	s_waitcnt lgkmcnt(0)
	global_store_dword v[6:7], v10, off
; __device__ __forceinline__ void phase_nrr(const Frame& F, const Args& a, int l, const bf16_t* XA, const float* g, const float* modl, unsigned char* XN8) {
;     ...
;         for (int i = 0; i < 8; ++i) { const int t = tb + i;
;             const float lg = Pl[(w * 8 + i) * NE + lane] + Pl[(64 + w * 8 + i) * NE + lane]; const float sc = 1.f / (1.f + __expf(-lg)); const float bb = sc + bias;
;             float m1 = bb; m1 = fmaxf(m1, __shfl_xor(m1, 1)); m1 = fmaxf(m1, __shfl_xor(m1, 2)); m1 = fmaxf(m1, __shfl_xor(m1, 4));
;             const unsigned long long eq = __ballot(bb == m1); const int gbase = lane & ~7; const unsigned grpmask = (unsigned)((eq >> gbase) & 0xffull);
;             const int first = gbase + __builtin_ctz(grpmask);
;             float m2 = (lane == first) ? -INFINITY : bb; m2 = fmaxf(m2, __shfl_xor(m2, 1)); m2 = fmaxf(m2, __shfl_xor(m2, 2)); m2 = fmaxf(m2, __shfl_xor(m2, 4));
;             const float gsum = m1 + m2; const int gq = lane >> 3;
;             int grank = 0;
; #pragma unroll
;             for (int g2 = 0; g2 < 8; ++g2) { const float v = __int_as_float(__builtin_amdgcn_readlane(__float_as_int(gsum), g2 * 8)); grank += (v > gsum || (v == gsum && g2 < gq)) ? 1 : 0; }
;             const bool keep = grank < 4; const float val = keep ? bb : -INFINITY;
;             int rank = 0;
; #pragma unroll 8
;             for (int e2 = 0; e2 < 64; ++e2) { const float v = __int_as_float(__builtin_amdgcn_readlane(__float_as_int(val), e2)); rank += (v > val || (v == val && e2 < lane)) ? 1 : 0; }
.LBB0_555:
	s_or_b64 exec, exec, s[4:5]
	v_add_u32_e32 v2, s85, v226
	ds_read_b32 v2, v2
	ds_read_b32 v5, v4 offset:17664
	s_waitcnt lgkmcnt(0)
	v_add_f32_e32 v2, v2, v5
	v_mul_f32_e32 v2, 0xbfb8aa3b, v2
	v_exp_f32_e32 v2, v2
	s_nop 0
	v_add_f32_e32 v2, 1.0, v2
	v_div_scale_f32 v5, s[2:3], v2, v2, 1.0
	v_rcp_f32_e32 v6, v5
	s_mov_b32 s2, 0
	v_fma_f32 v7, -v5, v6, 1.0
	v_fmac_f32_e32 v6, v7, v6
	v_div_scale_f32 v7, vcc, 1.0, v2, 1.0
	v_mul_f32_e32 v8, v7, v6
	v_fma_f32 v9, -v5, v8, v7
	v_fmac_f32_e32 v8, v9, v6
	v_fma_f32 v5, -v5, v8, v7
	v_div_fmas_f32 v5, v5, v6, v8
	v_div_fixup_f32 v2, v5, v2, 1.0
	v_add_f32_e32 v5, v3, v2
	s_nop 1
	s_waitcnt lgkmcnt(0)
	v_max_f32_dpp v6, v5, v5 quad_perm:[1,0,3,2] row_mask:0xf bank_mask:0xf
	s_nop 1
	s_waitcnt lgkmcnt(0)
	v_max_f32_dpp v6, v6, v6 quad_perm:[2,3,0,1] row_mask:0xf bank_mask:0xf
	s_nop 1
	s_waitcnt lgkmcnt(0)
	v_max_f32_dpp v8, v6, v6 row_half_mirror row_mask:0xf bank_mask:0xf
	v_cmp_eq_f32_e32 vcc, v5, v8
	s_nop 1
	v_lshrrev_b64 v[6:7], v200, vcc
	v_ffbl_b32_sdwa v6, v6 dst_sel:DWORD dst_unused:UNUSED_PAD src0_sel:BYTE_0
	v_add_u32_e32 v6, v6, v200
	v_cmp_ne_u32_e32 vcc, v230, v6
	s_nop 1
	v_cndmask_b32_e32 v6, v245, v5, vcc
	s_nop 1
	s_waitcnt lgkmcnt(0)
	v_max_f32_dpp v6, v6, v6 quad_perm:[1,0,3,2] row_mask:0xf bank_mask:0xf
	s_nop 1
	s_waitcnt lgkmcnt(0)
	v_max_f32_dpp v6, v6, v6 quad_perm:[2,3,0,1] row_mask:0xf bank_mask:0xf
	s_nop 1
	s_waitcnt lgkmcnt(0)
	v_max_f32_dpp v6, v6, v6 row_half_mirror row_mask:0xf bank_mask:0xf
	v_add_f32_e32 v6, v8, v6
	s_nop 0
	v_readlane_b32 s3, v6, 0
	s_nop 1
	v_cmp_eq_f32_e64 s[22:23], s3, v6
	v_cmp_gt_f32_e32 vcc, s3, v6
	s_and_b64 s[4:5], s[6:7], s[22:23]
	v_readlane_b32 s3, v6, 8
	s_or_b64 s[4:5], vcc, s[4:5]
	v_cndmask_b32_e64 v7, 0, 1, s[4:5]
	v_cmp_eq_f32_e64 s[22:23], s3, v6
	v_cmp_gt_f32_e32 vcc, s3, v6
	s_and_b64 s[4:5], s[8:9], s[22:23]
	v_readlane_b32 s3, v6, 16
	s_or_b64 s[4:5], vcc, s[4:5]
	v_cndmask_b32_e64 v8, 0, 1, s[4:5]
	v_cmp_eq_f32_e64 s[22:23], s3, v6
	v_cmp_gt_f32_e32 vcc, s3, v6
	s_and_b64 s[4:5], s[10:11], s[22:23]
	v_readlane_b32 s3, v6, 24
	s_or_b64 s[4:5], vcc, s[4:5]
	v_cndmask_b32_e64 v9, 0, 1, s[4:5]
	v_cmp_eq_f32_e64 s[22:23], s3, v6
	v_cmp_gt_f32_e32 vcc, s3, v6
	s_and_b64 s[4:5], s[12:13], s[22:23]
	v_readlane_b32 s3, v6, 32
	s_or_b64 s[4:5], vcc, s[4:5]
	v_cndmask_b32_e64 v10, 0, 1, s[4:5]
	v_cmp_eq_f32_e64 s[22:23], s3, v6
	v_cmp_gt_f32_e32 vcc, s3, v6
	s_and_b64 s[4:5], s[14:15], s[22:23]
	v_readlane_b32 s3, v6, 40
	s_or_b64 s[4:5], vcc, s[4:5]
	v_cndmask_b32_e64 v11, 0, 1, s[4:5]
	v_cmp_eq_f32_e64 s[22:23], s3, v6
	v_cmp_gt_f32_e32 vcc, s3, v6
	s_and_b64 s[4:5], s[16:17], s[22:23]
	v_readlane_b32 s3, v6, 48
	s_or_b64 s[4:5], vcc, s[4:5]
	v_cndmask_b32_e64 v12, 0, 1, s[4:5]
	v_cmp_eq_f32_e64 s[22:23], s3, v6
	v_cmp_gt_f32_e32 vcc, s3, v6
	s_and_b64 s[4:5], s[18:19], s[22:23]
	v_readlane_b32 s3, v6, 56
	s_or_b64 s[4:5], vcc, s[4:5]
	v_cndmask_b32_e64 v13, 0, 1, s[4:5]
	v_cmp_gt_f32_e32 vcc, s3, v6
	s_nop 1
	v_cndmask_b32_e64 v6, 0, 1, vcc
	v_add_u32_e32 v6, v8, v6
	v_add3_u32 v6, v6, v7, v9
	v_add3_u32 v6, v6, v10, v11
	v_add3_u32 v6, v6, v12, v13
	v_cmp_eq_u32_e32 vcc, 0, v6
	s_ff1_i32_b64 s98, vcc
	v_cmp_eq_u32_e32 vcc, 1, v6
	s_ff1_i32_b64 s99, vcc
	v_cmp_eq_u32_e32 vcc, 2, v6
	s_ff1_i32_b64 s100, vcc
	v_cmp_eq_u32_e32 vcc, 3, v6
	s_ff1_i32_b64 s101, vcc
	v_cmp_gt_u32_e32 vcc, 4, v6
	v_mov_b32_e32 v6, 0
	s_nop 0
	v_cndmask_b32_e32 v5, v245, v5, vcc
	v_ashrrev_i32_e32 v9, 31, v5
	v_sub_u32_e32 v8, 63, v230
	v_and_b32_e32 v9, 0x7fffffff, v9
	v_xor_b32_e32 v9, v5, v9
	s_nop 0
	v_readlane_b32 s25, v9, s98
	s_sub_i32 s24, 63, s98
	s_add_i32 s98, s98, 1
	v_readlane_b32 s23, v9, s98
	s_sub_i32 s22, 63, s98
	s_add_i32 s98, s98, 1
	v_cmp_gt_i64_e32 vcc, s[24:25], v[8:9]
	v_readlane_b32 s25, v9, s98
	s_sub_i32 s24, 63, s98
	s_add_i32 s98, s98, 1
	v_addc_co_u32_e32 v6, vcc, 0, v6, vcc
	v_cmp_gt_i64_e32 vcc, s[22:23], v[8:9]
	v_readlane_b32 s23, v9, s98
	s_sub_i32 s22, 63, s98
	s_add_i32 s98, s98, 1
	v_addc_co_u32_e32 v6, vcc, 0, v6, vcc
	v_cmp_gt_i64_e32 vcc, s[24:25], v[8:9]
	v_readlane_b32 s25, v9, s98
	s_sub_i32 s24, 63, s98
	s_add_i32 s98, s98, 1
	v_addc_co_u32_e32 v6, vcc, 0, v6, vcc
	v_cmp_gt_i64_e32 vcc, s[22:23], v[8:9]
	v_readlane_b32 s23, v9, s98
	s_sub_i32 s22, 63, s98
	s_add_i32 s98, s98, 1
	v_addc_co_u32_e32 v6, vcc, 0, v6, vcc
	v_cmp_gt_i64_e32 vcc, s[24:25], v[8:9]
	v_readlane_b32 s25, v9, s98
	s_sub_i32 s24, 63, s98
	s_add_i32 s98, s98, 1
	v_addc_co_u32_e32 v6, vcc, 0, v6, vcc
	v_cmp_gt_i64_e32 vcc, s[22:23], v[8:9]
	v_readlane_b32 s23, v9, s98
	s_sub_i32 s22, 63, s98
	s_nop 0
	v_addc_co_u32_e32 v6, vcc, 0, v6, vcc
	v_cmp_gt_i64_e32 vcc, s[24:25], v[8:9]
	v_readlane_b32 s25, v9, s99
	s_sub_i32 s24, 63, s99
	s_add_i32 s99, s99, 1
	v_addc_co_u32_e32 v6, vcc, 0, v6, vcc
	v_cmp_gt_i64_e32 vcc, s[22:23], v[8:9]
	v_readlane_b32 s23, v9, s99
	s_sub_i32 s22, 63, s99
	s_add_i32 s99, s99, 1
	v_addc_co_u32_e32 v6, vcc, 0, v6, vcc
	v_cmp_gt_i64_e32 vcc, s[24:25], v[8:9]
	v_readlane_b32 s25, v9, s99
	s_sub_i32 s24, 63, s99
	s_add_i32 s99, s99, 1
	v_addc_co_u32_e32 v6, vcc, 0, v6, vcc
	v_cmp_gt_i64_e32 vcc, s[22:23], v[8:9]
	v_readlane_b32 s23, v9, s99
	s_sub_i32 s22, 63, s99
	s_add_i32 s99, s99, 1
	v_addc_co_u32_e32 v6, vcc, 0, v6, vcc
	v_cmp_gt_i64_e32 vcc, s[24:25], v[8:9]
	v_readlane_b32 s25, v9, s99
	s_sub_i32 s24, 63, s99
	s_add_i32 s99, s99, 1
	v_addc_co_u32_e32 v6, vcc, 0, v6, vcc
	v_cmp_gt_i64_e32 vcc, s[22:23], v[8:9]
	v_readlane_b32 s23, v9, s99
	s_sub_i32 s22, 63, s99
	s_add_i32 s99, s99, 1
	v_addc_co_u32_e32 v6, vcc, 0, v6, vcc
	v_cmp_gt_i64_e32 vcc, s[24:25], v[8:9]
	v_readlane_b32 s25, v9, s99
; __device__ __forceinline__ void phase_nrr(const Frame& F, const Args& a, int l, const bf16_t* XA, const float* g, const float* modl, unsigned char* XN8) {
;     ...
;             const bool keep = grank < 4; const float val = keep ? bb : -INFINITY;
;             int rank = 0;
; #pragma unroll 8
;             for (int e2 = 0; e2 < 64; ++e2) { const float v = __int_as_float(__builtin_amdgcn_readlane(__float_as_int(val), e2)); rank += (v > val || (v == val && e2 < lane)) ? 1 : 0; }
;             const bool sel = rank < TOPK;
;             const float ssum = wave_sum(sel ? sc : 0.f);
;             if (sel) { const int p = atomicAdd((int*)(hist + lane), 1); top_e[t * TOPK + rank] = lane; gate[t * TOPK + rank] = sc / ssum * 2.5f; lpos[t * TOPK + rank] = p; }
	s_sub_i32 s24, 63, s99
	s_add_i32 s99, s99, 1
	v_addc_co_u32_e32 v6, vcc, 0, v6, vcc
	v_cmp_gt_i64_e32 vcc, s[22:23], v[8:9]
	v_readlane_b32 s23, v9, s99
	s_sub_i32 s22, 63, s99
	s_nop 0
	v_addc_co_u32_e32 v6, vcc, 0, v6, vcc
	v_cmp_gt_i64_e32 vcc, s[24:25], v[8:9]
	v_readlane_b32 s25, v9, s100
	s_sub_i32 s24, 63, s100
	s_add_i32 s100, s100, 1
	v_addc_co_u32_e32 v6, vcc, 0, v6, vcc
	v_cmp_gt_i64_e32 vcc, s[22:23], v[8:9]
	v_readlane_b32 s23, v9, s100
	s_sub_i32 s22, 63, s100
	s_add_i32 s100, s100, 1
	v_addc_co_u32_e32 v6, vcc, 0, v6, vcc
	v_cmp_gt_i64_e32 vcc, s[24:25], v[8:9]
	v_readlane_b32 s25, v9, s100
	s_sub_i32 s24, 63, s100
	s_add_i32 s100, s100, 1
	v_addc_co_u32_e32 v6, vcc, 0, v6, vcc
	v_cmp_gt_i64_e32 vcc, s[22:23], v[8:9]
	v_readlane_b32 s23, v9, s100
	s_sub_i32 s22, 63, s100
	s_add_i32 s100, s100, 1
	v_addc_co_u32_e32 v6, vcc, 0, v6, vcc
	v_cmp_gt_i64_e32 vcc, s[24:25], v[8:9]
	v_readlane_b32 s25, v9, s100
	s_sub_i32 s24, 63, s100
	s_add_i32 s100, s100, 1
	v_addc_co_u32_e32 v6, vcc, 0, v6, vcc
	v_cmp_gt_i64_e32 vcc, s[22:23], v[8:9]
	v_readlane_b32 s23, v9, s100
	s_sub_i32 s22, 63, s100
	s_add_i32 s100, s100, 1
	v_addc_co_u32_e32 v6, vcc, 0, v6, vcc
	v_cmp_gt_i64_e32 vcc, s[24:25], v[8:9]
	v_readlane_b32 s25, v9, s100
	s_sub_i32 s24, 63, s100
	s_add_i32 s100, s100, 1
	v_addc_co_u32_e32 v6, vcc, 0, v6, vcc
	v_cmp_gt_i64_e32 vcc, s[22:23], v[8:9]
	v_readlane_b32 s23, v9, s100
	s_sub_i32 s22, 63, s100
	s_nop 0
	v_addc_co_u32_e32 v6, vcc, 0, v6, vcc
	v_cmp_gt_i64_e32 vcc, s[24:25], v[8:9]
	v_readlane_b32 s25, v9, s101
	s_sub_i32 s24, 63, s101
	s_add_i32 s101, s101, 1
	v_addc_co_u32_e32 v6, vcc, 0, v6, vcc
	v_cmp_gt_i64_e32 vcc, s[22:23], v[8:9]
	v_readlane_b32 s23, v9, s101
	s_sub_i32 s22, 63, s101
	s_add_i32 s101, s101, 1
	v_addc_co_u32_e32 v6, vcc, 0, v6, vcc
	v_cmp_gt_i64_e32 vcc, s[24:25], v[8:9]
	v_readlane_b32 s25, v9, s101
	s_sub_i32 s24, 63, s101
	s_add_i32 s101, s101, 1
	v_addc_co_u32_e32 v6, vcc, 0, v6, vcc
	v_cmp_gt_i64_e32 vcc, s[22:23], v[8:9]
	v_readlane_b32 s23, v9, s101
	s_sub_i32 s22, 63, s101
	s_add_i32 s101, s101, 1
	v_addc_co_u32_e32 v6, vcc, 0, v6, vcc
	v_cmp_gt_i64_e32 vcc, s[24:25], v[8:9]
	v_readlane_b32 s25, v9, s101
	s_sub_i32 s24, 63, s101
	s_add_i32 s101, s101, 1
	v_addc_co_u32_e32 v6, vcc, 0, v6, vcc
	v_cmp_gt_i64_e32 vcc, s[22:23], v[8:9]
	v_readlane_b32 s23, v9, s101
	s_sub_i32 s22, 63, s101
	s_add_i32 s101, s101, 1
	v_addc_co_u32_e32 v6, vcc, 0, v6, vcc
	v_cmp_gt_i64_e32 vcc, s[24:25], v[8:9]
	v_readlane_b32 s25, v9, s101
	s_sub_i32 s24, 63, s101
	s_add_i32 s101, s101, 1
	v_addc_co_u32_e32 v6, vcc, 0, v6, vcc
	v_cmp_gt_i64_e32 vcc, s[22:23], v[8:9]
	v_readlane_b32 s23, v9, s101
	s_sub_i32 s22, 63, s101
	s_nop 0
	v_addc_co_u32_e32 v6, vcc, 0, v6, vcc
	v_cmp_gt_i64_e32 vcc, s[24:25], v[8:9]
	s_nop 1
	v_addc_co_u32_e32 v6, vcc, 0, v6, vcc
	v_cmp_gt_i64_e32 vcc, s[22:23], v[8:9]
	s_nop 1
	v_addc_co_u32_e32 v6, vcc, 0, v6, vcc
	v_cmp_gt_u32_e32 vcc, 6, v6
	s_nop 1
	v_cndmask_b32_e32 v5, 0, v2, vcc
	s_nop 1
	v_add_f32_dpp v5, v5, v5 quad_perm:[1,0,3,2] row_mask:0xf bank_mask:0xf
	s_nop 1
	v_add_f32_dpp v5, v5, v5 quad_perm:[2,3,0,1] row_mask:0xf bank_mask:0xf
	s_nop 1
	v_add_f32_dpp v5, v5, v5 row_half_mirror row_mask:0xf bank_mask:0xf
	s_nop 1
	v_add_f32_dpp v5, v5, v5 row_mirror row_mask:0xf bank_mask:0xf
	v_mov_b32_e32 v7, v5
	s_nop 1
	v_permlane16_swap_b32_e32 v7, v5
	s_waitcnt lgkmcnt(0)
	v_add_f32_e32 v5, v5, v7
	v_mov_b32_e32 v7, v5
	s_nop 1
	v_permlane32_swap_b32_e32 v7, v5
	s_and_saveexec_b64 s[2:3], vcc
	s_cbranch_execz .LBB0_559
	s_waitcnt lgkmcnt(0)
	v_add_f32_e32 v5, v5, v7
	v_div_scale_f32 v11, s[4:5], v5, v5, v2
	v_add3_u32 v6, s36, 30, v6
	v_rcp_f32_e32 v12, v11
	v_ashrrev_i32_e32 v7, 31, v6
	v_lshlrev_b64 v[6:7], 2, v[6:7]
	v_lshl_add_u64 v[8:9], s[26:27], 0, v[6:7]
	ds_add_rtn_u32 v10, v227, v243
	global_store_dword v[8:9], v230, off
	v_fma_f32 v8, -v11, v12, 1.0
	v_fmac_f32_e32 v12, v8, v12
	v_div_scale_f32 v8, vcc, v2, v5, v2
	v_mul_f32_e32 v9, v8, v12
	v_fma_f32 v13, -v11, v9, v8
	v_fmac_f32_e32 v9, v13, v12
	v_fma_f32 v8, -v11, v9, v8
	v_div_fmas_f32 v8, v8, v12, v9
	v_div_fixup_f32 v2, v8, v5, v2
	v_mul_f32_e32 v2, 0x40200000, v2
	v_lshl_add_u64 v[8:9], s[28:29], 0, v[6:7]
	v_lshl_add_u64 v[6:7], s[30:31], 0, v[6:7]
	global_store_dword v[8:9], v2, off
	s_waitcnt lgkmcnt(0)
	global_store_dword v[6:7], v10, off
; __device__ __forceinline__ void phase_nrr(const Frame& F, const Args& a, int l, const bf16_t* XA, const float* g, const float* modl, unsigned char* XN8) {
;     ...
;         for (int i = 0; i < 8; ++i) { const int t = tb + i;
;             const float lg = Pl[(w * 8 + i) * NE + lane] + Pl[(64 + w * 8 + i) * NE + lane]; const float sc = 1.f / (1.f + __expf(-lg)); const float bb = sc + bias;
;             float m1 = bb; m1 = fmaxf(m1, __shfl_xor(m1, 1)); m1 = fmaxf(m1, __shfl_xor(m1, 2)); m1 = fmaxf(m1, __shfl_xor(m1, 4));
;             const unsigned long long eq = __ballot(bb == m1); const int gbase = lane & ~7; const unsigned grpmask = (unsigned)((eq >> gbase) & 0xffull);
;             const int first = gbase + __builtin_ctz(grpmask);
;             float m2 = (lane == first) ? -INFINITY : bb; m2 = fmaxf(m2, __shfl_xor(m2, 1)); m2 = fmaxf(m2, __shfl_xor(m2, 2)); m2 = fmaxf(m2, __shfl_xor(m2, 4));
;             const float gsum = m1 + m2; const int gq = lane >> 3;
;             int grank = 0;
; #pragma unroll
;             for (int g2 = 0; g2 < 8; ++g2) { const float v = __int_as_float(__builtin_amdgcn_readlane(__float_as_int(gsum), g2 * 8)); grank += (v > gsum || (v == gsum && g2 < gq)) ? 1 : 0; }
;             const bool keep = grank < 4; const float val = keep ? bb : -INFINITY;
;             int rank = 0;
; #pragma unroll 8
;             for (int e2 = 0; e2 < 64; ++e2) { const float v = __int_as_float(__builtin_amdgcn_readlane(__float_as_int(val), e2)); rank += (v > val || (v == val && e2 < lane)) ? 1 : 0; }
.LBB0_559:
	s_or_b64 exec, exec, s[2:3]
	v_add_u32_e32 v2, s86, v226
	ds_read_b32 v2, v2
	ds_read_b32 v5, v4 offset:17920
	s_waitcnt lgkmcnt(0)
	v_add_f32_e32 v2, v2, v5
	v_mul_f32_e32 v2, 0xbfb8aa3b, v2
	v_exp_f32_e32 v2, v2
	s_nop 0
	v_add_f32_e32 v2, 1.0, v2
	v_div_scale_f32 v5, s[2:3], v2, v2, 1.0
	v_rcp_f32_e32 v6, v5
	s_mov_b32 s2, 0
	v_fma_f32 v7, -v5, v6, 1.0
	v_fmac_f32_e32 v6, v7, v6
	v_div_scale_f32 v7, vcc, 1.0, v2, 1.0
	v_mul_f32_e32 v8, v7, v6
	v_fma_f32 v9, -v5, v8, v7
	v_fmac_f32_e32 v8, v9, v6
	v_fma_f32 v5, -v5, v8, v7
	v_div_fmas_f32 v5, v5, v6, v8
	v_div_fixup_f32 v2, v5, v2, 1.0
	v_add_f32_e32 v5, v3, v2
	s_nop 1
	s_waitcnt lgkmcnt(0)
	v_max_f32_dpp v6, v5, v5 quad_perm:[1,0,3,2] row_mask:0xf bank_mask:0xf
	s_nop 1
	s_waitcnt lgkmcnt(0)
	v_max_f32_dpp v6, v6, v6 quad_perm:[2,3,0,1] row_mask:0xf bank_mask:0xf
	s_nop 1
	s_waitcnt lgkmcnt(0)
	v_max_f32_dpp v8, v6, v6 row_half_mirror row_mask:0xf bank_mask:0xf
	v_cmp_eq_f32_e32 vcc, v5, v8
	s_nop 1
	v_lshrrev_b64 v[6:7], v200, vcc
	v_ffbl_b32_sdwa v6, v6 dst_sel:DWORD dst_unused:UNUSED_PAD src0_sel:BYTE_0
	v_add_u32_e32 v6, v6, v200
	v_cmp_ne_u32_e32 vcc, v230, v6
	s_nop 1
	v_cndmask_b32_e32 v6, v245, v5, vcc
	s_nop 1
	s_waitcnt lgkmcnt(0)
	v_max_f32_dpp v6, v6, v6 quad_perm:[1,0,3,2] row_mask:0xf bank_mask:0xf
	s_nop 1
	s_waitcnt lgkmcnt(0)
	v_max_f32_dpp v6, v6, v6 quad_perm:[2,3,0,1] row_mask:0xf bank_mask:0xf
	s_nop 1
	s_waitcnt lgkmcnt(0)
	v_max_f32_dpp v6, v6, v6 row_half_mirror row_mask:0xf bank_mask:0xf
	v_add_f32_e32 v6, v8, v6
	s_nop 0
	v_readlane_b32 s3, v6, 0
	s_nop 1
	v_cmp_eq_f32_e64 s[22:23], s3, v6
	v_cmp_gt_f32_e32 vcc, s3, v6
	s_and_b64 s[4:5], s[6:7], s[22:23]
	v_readlane_b32 s3, v6, 8
	s_or_b64 s[4:5], vcc, s[4:5]
	v_cndmask_b32_e64 v7, 0, 1, s[4:5]
	v_cmp_eq_f32_e64 s[22:23], s3, v6
	v_cmp_gt_f32_e32 vcc, s3, v6
	s_and_b64 s[4:5], s[8:9], s[22:23]
	v_readlane_b32 s3, v6, 16
	s_or_b64 s[4:5], vcc, s[4:5]
	v_cndmask_b32_e64 v8, 0, 1, s[4:5]
	v_cmp_eq_f32_e64 s[22:23], s3, v6
	v_cmp_gt_f32_e32 vcc, s3, v6
	s_and_b64 s[4:5], s[10:11], s[22:23]
	v_readlane_b32 s3, v6, 24
	s_or_b64 s[4:5], vcc, s[4:5]
	v_cndmask_b32_e64 v9, 0, 1, s[4:5]
	v_cmp_eq_f32_e64 s[22:23], s3, v6
	v_cmp_gt_f32_e32 vcc, s3, v6
	s_and_b64 s[4:5], s[12:13], s[22:23]
	v_readlane_b32 s3, v6, 32
	s_or_b64 s[4:5], vcc, s[4:5]
	v_cndmask_b32_e64 v10, 0, 1, s[4:5]
	v_cmp_eq_f32_e64 s[22:23], s3, v6
	v_cmp_gt_f32_e32 vcc, s3, v6
	s_and_b64 s[4:5], s[14:15], s[22:23]
	v_readlane_b32 s3, v6, 40
	s_or_b64 s[4:5], vcc, s[4:5]
	v_cndmask_b32_e64 v11, 0, 1, s[4:5]
	v_cmp_eq_f32_e64 s[22:23], s3, v6
	v_cmp_gt_f32_e32 vcc, s3, v6
	s_and_b64 s[4:5], s[16:17], s[22:23]
	v_readlane_b32 s3, v6, 48
	s_or_b64 s[4:5], vcc, s[4:5]
	v_cndmask_b32_e64 v12, 0, 1, s[4:5]
	v_cmp_eq_f32_e64 s[22:23], s3, v6
	v_cmp_gt_f32_e32 vcc, s3, v6
	s_and_b64 s[4:5], s[18:19], s[22:23]
	v_readlane_b32 s3, v6, 56
	s_or_b64 s[4:5], vcc, s[4:5]
	v_cndmask_b32_e64 v13, 0, 1, s[4:5]
	v_cmp_gt_f32_e32 vcc, s3, v6
	s_nop 1
	v_cndmask_b32_e64 v6, 0, 1, vcc
	v_add_u32_e32 v6, v8, v6
	v_add3_u32 v6, v6, v7, v9
	v_add3_u32 v6, v6, v10, v11
	v_add3_u32 v6, v6, v12, v13
	v_cmp_eq_u32_e32 vcc, 0, v6
	s_ff1_i32_b64 s98, vcc
	v_cmp_eq_u32_e32 vcc, 1, v6
	s_ff1_i32_b64 s99, vcc
	v_cmp_eq_u32_e32 vcc, 2, v6
	s_ff1_i32_b64 s100, vcc
	v_cmp_eq_u32_e32 vcc, 3, v6
	s_ff1_i32_b64 s101, vcc
	v_cmp_gt_u32_e32 vcc, 4, v6
	v_mov_b32_e32 v6, 0
	s_nop 0
	v_cndmask_b32_e32 v5, v245, v5, vcc
	v_ashrrev_i32_e32 v9, 31, v5
	v_sub_u32_e32 v8, 63, v230
	v_and_b32_e32 v9, 0x7fffffff, v9
	v_xor_b32_e32 v9, v5, v9
	s_nop 0
	v_readlane_b32 s25, v9, s98
	s_sub_i32 s24, 63, s98
	s_add_i32 s98, s98, 1
	v_readlane_b32 s23, v9, s98
	s_sub_i32 s22, 63, s98
	s_add_i32 s98, s98, 1
	v_cmp_gt_i64_e32 vcc, s[24:25], v[8:9]
	v_readlane_b32 s25, v9, s98
	s_sub_i32 s24, 63, s98
	s_add_i32 s98, s98, 1
	v_addc_co_u32_e32 v6, vcc, 0, v6, vcc
	v_cmp_gt_i64_e32 vcc, s[22:23], v[8:9]
	v_readlane_b32 s23, v9, s98
	s_sub_i32 s22, 63, s98
	s_add_i32 s98, s98, 1
	v_addc_co_u32_e32 v6, vcc, 0, v6, vcc
	v_cmp_gt_i64_e32 vcc, s[24:25], v[8:9]
	v_readlane_b32 s25, v9, s98
	s_sub_i32 s24, 63, s98
	s_add_i32 s98, s98, 1
	v_addc_co_u32_e32 v6, vcc, 0, v6, vcc
	v_cmp_gt_i64_e32 vcc, s[22:23], v[8:9]
	v_readlane_b32 s23, v9, s98
	s_sub_i32 s22, 63, s98
	s_add_i32 s98, s98, 1
	v_addc_co_u32_e32 v6, vcc, 0, v6, vcc
	v_cmp_gt_i64_e32 vcc, s[24:25], v[8:9]
	v_readlane_b32 s25, v9, s98
	s_sub_i32 s24, 63, s98
	s_add_i32 s98, s98, 1
	v_addc_co_u32_e32 v6, vcc, 0, v6, vcc
	v_cmp_gt_i64_e32 vcc, s[22:23], v[8:9]
	v_readlane_b32 s23, v9, s98
	s_sub_i32 s22, 63, s98
	s_nop 0
	v_addc_co_u32_e32 v6, vcc, 0, v6, vcc
	v_cmp_gt_i64_e32 vcc, s[24:25], v[8:9]
	v_readlane_b32 s25, v9, s99
	s_sub_i32 s24, 63, s99
	s_add_i32 s99, s99, 1
	v_addc_co_u32_e32 v6, vcc, 0, v6, vcc
	v_cmp_gt_i64_e32 vcc, s[22:23], v[8:9]
	v_readlane_b32 s23, v9, s99
	s_sub_i32 s22, 63, s99
	s_add_i32 s99, s99, 1
	v_addc_co_u32_e32 v6, vcc, 0, v6, vcc
	v_cmp_gt_i64_e32 vcc, s[24:25], v[8:9]
	v_readlane_b32 s25, v9, s99
	s_sub_i32 s24, 63, s99
	s_add_i32 s99, s99, 1
	v_addc_co_u32_e32 v6, vcc, 0, v6, vcc
	v_cmp_gt_i64_e32 vcc, s[22:23], v[8:9]
	v_readlane_b32 s23, v9, s99
	s_sub_i32 s22, 63, s99
	s_add_i32 s99, s99, 1
	v_addc_co_u32_e32 v6, vcc, 0, v6, vcc
	v_cmp_gt_i64_e32 vcc, s[24:25], v[8:9]
	v_readlane_b32 s25, v9, s99
	s_sub_i32 s24, 63, s99
	s_add_i32 s99, s99, 1
	v_addc_co_u32_e32 v6, vcc, 0, v6, vcc
	v_cmp_gt_i64_e32 vcc, s[22:23], v[8:9]
	v_readlane_b32 s23, v9, s99
	s_sub_i32 s22, 63, s99
	s_add_i32 s99, s99, 1
	v_addc_co_u32_e32 v6, vcc, 0, v6, vcc
	v_cmp_gt_i64_e32 vcc, s[24:25], v[8:9]
	v_readlane_b32 s25, v9, s99
; __device__ __forceinline__ void phase_nrr(const Frame& F, const Args& a, int l, const bf16_t* XA, const float* g, const float* modl, unsigned char* XN8) {
;     ...
;             const bool keep = grank < 4; const float val = keep ? bb : -INFINITY;
;             int rank = 0;
; #pragma unroll 8
;             for (int e2 = 0; e2 < 64; ++e2) { const float v = __int_as_float(__builtin_amdgcn_readlane(__float_as_int(val), e2)); rank += (v > val || (v == val && e2 < lane)) ? 1 : 0; }
;             const bool sel = rank < TOPK;
;             const float ssum = wave_sum(sel ? sc : 0.f);
;             if (sel) { const int p = atomicAdd((int*)(hist + lane), 1); top_e[t * TOPK + rank] = lane; gate[t * TOPK + rank] = sc / ssum * 2.5f; lpos[t * TOPK + rank] = p; }
	s_sub_i32 s24, 63, s99
	s_add_i32 s99, s99, 1
	v_addc_co_u32_e32 v6, vcc, 0, v6, vcc
	v_cmp_gt_i64_e32 vcc, s[22:23], v[8:9]
	v_readlane_b32 s23, v9, s99
	s_sub_i32 s22, 63, s99
	s_nop 0
	v_addc_co_u32_e32 v6, vcc, 0, v6, vcc
	v_cmp_gt_i64_e32 vcc, s[24:25], v[8:9]
	v_readlane_b32 s25, v9, s100
	s_sub_i32 s24, 63, s100
	s_add_i32 s100, s100, 1
	v_addc_co_u32_e32 v6, vcc, 0, v6, vcc
	v_cmp_gt_i64_e32 vcc, s[22:23], v[8:9]
	v_readlane_b32 s23, v9, s100
	s_sub_i32 s22, 63, s100
	s_add_i32 s100, s100, 1
	v_addc_co_u32_e32 v6, vcc, 0, v6, vcc
	v_cmp_gt_i64_e32 vcc, s[24:25], v[8:9]
	v_readlane_b32 s25, v9, s100
	s_sub_i32 s24, 63, s100
	s_add_i32 s100, s100, 1
	v_addc_co_u32_e32 v6, vcc, 0, v6, vcc
	v_cmp_gt_i64_e32 vcc, s[22:23], v[8:9]
	v_readlane_b32 s23, v9, s100
	s_sub_i32 s22, 63, s100
	s_add_i32 s100, s100, 1
	v_addc_co_u32_e32 v6, vcc, 0, v6, vcc
	v_cmp_gt_i64_e32 vcc, s[24:25], v[8:9]
	v_readlane_b32 s25, v9, s100
	s_sub_i32 s24, 63, s100
	s_add_i32 s100, s100, 1
	v_addc_co_u32_e32 v6, vcc, 0, v6, vcc
	v_cmp_gt_i64_e32 vcc, s[22:23], v[8:9]
	v_readlane_b32 s23, v9, s100
	s_sub_i32 s22, 63, s100
	s_add_i32 s100, s100, 1
	v_addc_co_u32_e32 v6, vcc, 0, v6, vcc
	v_cmp_gt_i64_e32 vcc, s[24:25], v[8:9]
	v_readlane_b32 s25, v9, s100
	s_sub_i32 s24, 63, s100
	s_add_i32 s100, s100, 1
	v_addc_co_u32_e32 v6, vcc, 0, v6, vcc
	v_cmp_gt_i64_e32 vcc, s[22:23], v[8:9]
	v_readlane_b32 s23, v9, s100
	s_sub_i32 s22, 63, s100
	s_nop 0
	v_addc_co_u32_e32 v6, vcc, 0, v6, vcc
	v_cmp_gt_i64_e32 vcc, s[24:25], v[8:9]
	v_readlane_b32 s25, v9, s101
	s_sub_i32 s24, 63, s101
	s_add_i32 s101, s101, 1
	v_addc_co_u32_e32 v6, vcc, 0, v6, vcc
	v_cmp_gt_i64_e32 vcc, s[22:23], v[8:9]
	v_readlane_b32 s23, v9, s101
	s_sub_i32 s22, 63, s101
	s_add_i32 s101, s101, 1
	v_addc_co_u32_e32 v6, vcc, 0, v6, vcc
	v_cmp_gt_i64_e32 vcc, s[24:25], v[8:9]
	v_readlane_b32 s25, v9, s101
	s_sub_i32 s24, 63, s101
	s_add_i32 s101, s101, 1
	v_addc_co_u32_e32 v6, vcc, 0, v6, vcc
	v_cmp_gt_i64_e32 vcc, s[22:23], v[8:9]
	v_readlane_b32 s23, v9, s101
	s_sub_i32 s22, 63, s101
	s_add_i32 s101, s101, 1
	v_addc_co_u32_e32 v6, vcc, 0, v6, vcc
	v_cmp_gt_i64_e32 vcc, s[24:25], v[8:9]
	v_readlane_b32 s25, v9, s101
	s_sub_i32 s24, 63, s101
	s_add_i32 s101, s101, 1
	v_addc_co_u32_e32 v6, vcc, 0, v6, vcc
	v_cmp_gt_i64_e32 vcc, s[22:23], v[8:9]
	v_readlane_b32 s23, v9, s101
	s_sub_i32 s22, 63, s101
	s_add_i32 s101, s101, 1
	v_addc_co_u32_e32 v6, vcc, 0, v6, vcc
	v_cmp_gt_i64_e32 vcc, s[24:25], v[8:9]
	v_readlane_b32 s25, v9, s101
	s_sub_i32 s24, 63, s101
	s_add_i32 s101, s101, 1
	v_addc_co_u32_e32 v6, vcc, 0, v6, vcc
	v_cmp_gt_i64_e32 vcc, s[22:23], v[8:9]
	v_readlane_b32 s23, v9, s101
	s_sub_i32 s22, 63, s101
	s_nop 0
	v_addc_co_u32_e32 v6, vcc, 0, v6, vcc
	v_cmp_gt_i64_e32 vcc, s[24:25], v[8:9]
	s_nop 1
	v_addc_co_u32_e32 v6, vcc, 0, v6, vcc
	v_cmp_gt_i64_e32 vcc, s[22:23], v[8:9]
	s_nop 1
	v_addc_co_u32_e32 v6, vcc, 0, v6, vcc
	v_cmp_gt_u32_e32 vcc, 6, v6
	s_nop 1
	v_cndmask_b32_e32 v5, 0, v2, vcc
	s_nop 1
	v_add_f32_dpp v5, v5, v5 quad_perm:[1,0,3,2] row_mask:0xf bank_mask:0xf
	s_nop 1
	v_add_f32_dpp v5, v5, v5 quad_perm:[2,3,0,1] row_mask:0xf bank_mask:0xf
	s_nop 1
	v_add_f32_dpp v5, v5, v5 row_half_mirror row_mask:0xf bank_mask:0xf
	s_nop 1
	v_add_f32_dpp v5, v5, v5 row_mirror row_mask:0xf bank_mask:0xf
	v_mov_b32_e32 v7, v5
	s_nop 1
	v_permlane16_swap_b32_e32 v7, v5
	s_waitcnt lgkmcnt(0)
	v_add_f32_e32 v5, v5, v7
	v_mov_b32_e32 v7, v5
	s_nop 1
	v_permlane32_swap_b32_e32 v7, v5
	s_and_saveexec_b64 s[2:3], vcc
	s_cbranch_execz .LBB0_563
	s_waitcnt lgkmcnt(0)
	v_add_f32_e32 v5, v5, v7
	v_div_scale_f32 v11, s[4:5], v5, v5, v2
	v_add3_u32 v6, s36, 36, v6
	v_rcp_f32_e32 v12, v11
	v_ashrrev_i32_e32 v7, 31, v6
	v_lshlrev_b64 v[6:7], 2, v[6:7]
	v_lshl_add_u64 v[8:9], s[26:27], 0, v[6:7]
	ds_add_rtn_u32 v10, v227, v243
	global_store_dword v[8:9], v230, off
	v_fma_f32 v8, -v11, v12, 1.0
	v_fmac_f32_e32 v12, v8, v12
	v_div_scale_f32 v8, vcc, v2, v5, v2
	v_mul_f32_e32 v9, v8, v12
	v_fma_f32 v13, -v11, v9, v8
	v_fmac_f32_e32 v9, v13, v12
	v_fma_f32 v8, -v11, v9, v8
	v_div_fmas_f32 v8, v8, v12, v9
	v_div_fixup_f32 v2, v8, v5, v2
	v_mul_f32_e32 v2, 0x40200000, v2
	v_lshl_add_u64 v[8:9], s[28:29], 0, v[6:7]
	v_lshl_add_u64 v[6:7], s[30:31], 0, v[6:7]
	global_store_dword v[8:9], v2, off
	s_waitcnt lgkmcnt(0)
	global_store_dword v[6:7], v10, off
; __device__ __forceinline__ void phase_nrr(const Frame& F, const Args& a, int l, const bf16_t* XA, const float* g, const float* modl, unsigned char* XN8) {
;     ...
;         for (int i = 0; i < 8; ++i) { const int t = tb + i;
;             const float lg = Pl[(w * 8 + i) * NE + lane] + Pl[(64 + w * 8 + i) * NE + lane]; const float sc = 1.f / (1.f + __expf(-lg)); const float bb = sc + bias;
;             float m1 = bb; m1 = fmaxf(m1, __shfl_xor(m1, 1)); m1 = fmaxf(m1, __shfl_xor(m1, 2)); m1 = fmaxf(m1, __shfl_xor(m1, 4));
;             const unsigned long long eq = __ballot(bb == m1); const int gbase = lane & ~7; const unsigned grpmask = (unsigned)((eq >> gbase) & 0xffull);
;             const int first = gbase + __builtin_ctz(grpmask);
;             float m2 = (lane == first) ? -INFINITY : bb; m2 = fmaxf(m2, __shfl_xor(m2, 1)); m2 = fmaxf(m2, __shfl_xor(m2, 2)); m2 = fmaxf(m2, __shfl_xor(m2, 4));
;             const float gsum = m1 + m2; const int gq = lane >> 3;
;             int grank = 0;
; #pragma unroll
;             for (int g2 = 0; g2 < 8; ++g2) { const float v = __int_as_float(__builtin_amdgcn_readlane(__float_as_int(gsum), g2 * 8)); grank += (v > gsum || (v == gsum && g2 < gq)) ? 1 : 0; }
;             const bool keep = grank < 4; const float val = keep ? bb : -INFINITY;
;             int rank = 0;
; #pragma unroll 8
;             for (int e2 = 0; e2 < 64; ++e2) { const float v = __int_as_float(__builtin_amdgcn_readlane(__float_as_int(val), e2)); rank += (v > val || (v == val && e2 < lane)) ? 1 : 0; }
.LBB0_563:
	s_or_b64 exec, exec, s[2:3]
	v_add_u32_e32 v2, s87, v226
	ds_read_b32 v2, v2
	ds_read_b32 v4, v4 offset:18176
	s_waitcnt lgkmcnt(0)
	v_add_f32_e32 v2, v2, v4
	v_mul_f32_e32 v2, 0xbfb8aa3b, v2
	v_exp_f32_e32 v2, v2
	s_nop 0
	v_add_f32_e32 v2, 1.0, v2
	v_div_scale_f32 v4, s[2:3], v2, v2, 1.0
	v_rcp_f32_e32 v5, v4
	s_mov_b32 s2, 0
	v_fma_f32 v6, -v4, v5, 1.0
	v_fmac_f32_e32 v5, v6, v5
	v_div_scale_f32 v6, vcc, 1.0, v2, 1.0
	v_mul_f32_e32 v7, v6, v5
	v_fma_f32 v8, -v4, v7, v6
	v_fmac_f32_e32 v7, v8, v5
	v_fma_f32 v4, -v4, v7, v6
	v_div_fmas_f32 v4, v4, v5, v7
	v_div_fixup_f32 v2, v4, v2, 1.0
	v_add_f32_e32 v3, v3, v2
	s_nop 1
	s_waitcnt lgkmcnt(0)
	v_max_f32_dpp v4, v3, v3 quad_perm:[1,0,3,2] row_mask:0xf bank_mask:0xf
	s_nop 1
	s_waitcnt lgkmcnt(0)
	v_max_f32_dpp v4, v4, v4 quad_perm:[2,3,0,1] row_mask:0xf bank_mask:0xf
	s_nop 1
	s_waitcnt lgkmcnt(0)
	v_max_f32_dpp v6, v4, v4 row_half_mirror row_mask:0xf bank_mask:0xf
	v_cmp_eq_f32_e32 vcc, v3, v6
	s_nop 1
	v_lshrrev_b64 v[4:5], v200, vcc
	v_ffbl_b32_sdwa v4, v4 dst_sel:DWORD dst_unused:UNUSED_PAD src0_sel:BYTE_0
	v_add_u32_e32 v4, v4, v200
	v_cmp_ne_u32_e32 vcc, v230, v4
	s_nop 1
	v_cndmask_b32_e32 v4, v245, v3, vcc
	s_nop 1
	s_waitcnt lgkmcnt(0)
	v_max_f32_dpp v4, v4, v4 quad_perm:[1,0,3,2] row_mask:0xf bank_mask:0xf
	s_nop 1
	s_waitcnt lgkmcnt(0)
	v_max_f32_dpp v4, v4, v4 quad_perm:[2,3,0,1] row_mask:0xf bank_mask:0xf
	s_nop 1
	s_waitcnt lgkmcnt(0)
	v_max_f32_dpp v4, v4, v4 row_half_mirror row_mask:0xf bank_mask:0xf
	v_add_f32_e32 v4, v6, v4
	s_nop 0
	v_readlane_b32 s3, v4, 0
	s_nop 1
	v_cmp_eq_f32_e64 s[22:23], s3, v4
	v_cmp_gt_f32_e32 vcc, s3, v4
	s_and_b64 s[4:5], s[6:7], s[22:23]
	v_readlane_b32 s3, v4, 8
	s_or_b64 s[4:5], vcc, s[4:5]
	v_cndmask_b32_e64 v5, 0, 1, s[4:5]
	v_cmp_eq_f32_e64 s[22:23], s3, v4
	v_cmp_gt_f32_e32 vcc, s3, v4
	s_and_b64 s[4:5], s[8:9], s[22:23]
	v_readlane_b32 s3, v4, 16
	s_or_b64 s[4:5], vcc, s[4:5]
	v_cndmask_b32_e64 v6, 0, 1, s[4:5]
	v_cmp_eq_f32_e64 s[22:23], s3, v4
	v_cmp_gt_f32_e32 vcc, s3, v4
	s_and_b64 s[4:5], s[10:11], s[22:23]
	v_readlane_b32 s3, v4, 24
	s_or_b64 s[4:5], vcc, s[4:5]
	v_cndmask_b32_e64 v7, 0, 1, s[4:5]
	v_cmp_eq_f32_e64 s[22:23], s3, v4
	v_cmp_gt_f32_e32 vcc, s3, v4
	s_and_b64 s[4:5], s[12:13], s[22:23]
	v_readlane_b32 s3, v4, 32
	s_or_b64 s[4:5], vcc, s[4:5]
	v_cndmask_b32_e64 v8, 0, 1, s[4:5]
	v_cmp_eq_f32_e64 s[22:23], s3, v4
	v_cmp_gt_f32_e32 vcc, s3, v4
	s_and_b64 s[4:5], s[14:15], s[22:23]
	v_readlane_b32 s3, v4, 40
	s_or_b64 s[4:5], vcc, s[4:5]
	v_cndmask_b32_e64 v9, 0, 1, s[4:5]
	v_cmp_eq_f32_e64 s[22:23], s3, v4
	v_cmp_gt_f32_e32 vcc, s3, v4
	s_and_b64 s[4:5], s[16:17], s[22:23]
	v_readlane_b32 s3, v4, 48
	s_or_b64 s[4:5], vcc, s[4:5]
	v_cndmask_b32_e64 v10, 0, 1, s[4:5]
	v_cmp_eq_f32_e64 s[22:23], s3, v4
	v_cmp_gt_f32_e32 vcc, s3, v4
	s_and_b64 s[4:5], s[18:19], s[22:23]
	v_readlane_b32 s3, v4, 56
	s_or_b64 s[4:5], vcc, s[4:5]
	v_cndmask_b32_e64 v11, 0, 1, s[4:5]
	v_cmp_gt_f32_e32 vcc, s3, v4
	s_nop 1
	v_cndmask_b32_e64 v4, 0, 1, vcc
	v_add_u32_e32 v4, v6, v4
	v_add3_u32 v4, v4, v5, v7
	v_add3_u32 v4, v4, v8, v9
	v_add3_u32 v4, v4, v10, v11
	v_cmp_eq_u32_e32 vcc, 0, v4
	s_ff1_i32_b64 s98, vcc
	v_cmp_eq_u32_e32 vcc, 1, v4
	s_ff1_i32_b64 s99, vcc
	v_cmp_eq_u32_e32 vcc, 2, v4
	s_ff1_i32_b64 s100, vcc
	v_cmp_eq_u32_e32 vcc, 3, v4
	s_ff1_i32_b64 s101, vcc
	v_cmp_gt_u32_e32 vcc, 4, v4
	v_mov_b32_e32 v4, 0
	s_nop 0
	v_cndmask_b32_e32 v3, v245, v3, vcc
	v_ashrrev_i32_e32 v9, 31, v3
	v_sub_u32_e32 v8, 63, v230
	v_and_b32_e32 v9, 0x7fffffff, v9
	v_xor_b32_e32 v9, v3, v9
	s_nop 0
	v_readlane_b32 s25, v9, s98
	s_sub_i32 s24, 63, s98
	s_add_i32 s98, s98, 1
	v_readlane_b32 s23, v9, s98
	s_sub_i32 s22, 63, s98
	s_add_i32 s98, s98, 1
	v_cmp_gt_i64_e32 vcc, s[24:25], v[8:9]
	v_readlane_b32 s25, v9, s98
	s_sub_i32 s24, 63, s98
	s_add_i32 s98, s98, 1
	v_addc_co_u32_e32 v4, vcc, 0, v4, vcc
	v_cmp_gt_i64_e32 vcc, s[22:23], v[8:9]
	v_readlane_b32 s23, v9, s98
	s_sub_i32 s22, 63, s98
	s_add_i32 s98, s98, 1
	v_addc_co_u32_e32 v4, vcc, 0, v4, vcc
	v_cmp_gt_i64_e32 vcc, s[24:25], v[8:9]
	v_readlane_b32 s25, v9, s98
	s_sub_i32 s24, 63, s98
	s_add_i32 s98, s98, 1
	v_addc_co_u32_e32 v4, vcc, 0, v4, vcc
	v_cmp_gt_i64_e32 vcc, s[22:23], v[8:9]
	v_readlane_b32 s23, v9, s98
	s_sub_i32 s22, 63, s98
	s_add_i32 s98, s98, 1
	v_addc_co_u32_e32 v4, vcc, 0, v4, vcc
	v_cmp_gt_i64_e32 vcc, s[24:25], v[8:9]
	v_readlane_b32 s25, v9, s98
	s_sub_i32 s24, 63, s98
	s_add_i32 s98, s98, 1
	v_addc_co_u32_e32 v4, vcc, 0, v4, vcc
	v_cmp_gt_i64_e32 vcc, s[22:23], v[8:9]
	v_readlane_b32 s23, v9, s98
	s_sub_i32 s22, 63, s98
	s_nop 0
	v_addc_co_u32_e32 v4, vcc, 0, v4, vcc
	v_cmp_gt_i64_e32 vcc, s[24:25], v[8:9]
	v_readlane_b32 s25, v9, s99
	s_sub_i32 s24, 63, s99
	s_add_i32 s99, s99, 1
	v_addc_co_u32_e32 v4, vcc, 0, v4, vcc
	v_cmp_gt_i64_e32 vcc, s[22:23], v[8:9]
	v_readlane_b32 s23, v9, s99
	s_sub_i32 s22, 63, s99
	s_add_i32 s99, s99, 1
	v_addc_co_u32_e32 v4, vcc, 0, v4, vcc
	v_cmp_gt_i64_e32 vcc, s[24:25], v[8:9]
; __device__ __forceinline__ void phase_nrr(const Frame& F, const Args& a, int l, const bf16_t* XA, const float* g, const float* modl, unsigned char* XN8) {
;     ...
;             const bool keep = grank < 4; const float val = keep ? bb : -INFINITY;
;             int rank = 0;
; #pragma unroll 8
;             for (int e2 = 0; e2 < 64; ++e2) { const float v = __int_as_float(__builtin_amdgcn_readlane(__float_as_int(val), e2)); rank += (v > val || (v == val && e2 < lane)) ? 1 : 0; }
;             const bool sel = rank < TOPK;
;             const float ssum = wave_sum(sel ? sc : 0.f);
;             if (sel) { const int p = atomicAdd((int*)(hist + lane), 1); top_e[t * TOPK + rank] = lane; gate[t * TOPK + rank] = sc / ssum * 2.5f; lpos[t * TOPK + rank] = p; }
	v_readlane_b32 s25, v9, s99
	s_sub_i32 s24, 63, s99
	s_add_i32 s99, s99, 1
	v_addc_co_u32_e32 v4, vcc, 0, v4, vcc
	v_cmp_gt_i64_e32 vcc, s[22:23], v[8:9]
	v_readlane_b32 s23, v9, s99
	s_sub_i32 s22, 63, s99
	s_add_i32 s99, s99, 1
	v_addc_co_u32_e32 v4, vcc, 0, v4, vcc
	v_cmp_gt_i64_e32 vcc, s[24:25], v[8:9]
	v_readlane_b32 s25, v9, s99
	s_sub_i32 s24, 63, s99
	s_add_i32 s99, s99, 1
	v_addc_co_u32_e32 v4, vcc, 0, v4, vcc
	v_cmp_gt_i64_e32 vcc, s[22:23], v[8:9]
	v_readlane_b32 s23, v9, s99
	s_sub_i32 s22, 63, s99
	s_add_i32 s99, s99, 1
	v_addc_co_u32_e32 v4, vcc, 0, v4, vcc
	v_cmp_gt_i64_e32 vcc, s[24:25], v[8:9]
	v_readlane_b32 s25, v9, s99
	s_sub_i32 s24, 63, s99
	s_add_i32 s99, s99, 1
	v_addc_co_u32_e32 v4, vcc, 0, v4, vcc
	v_cmp_gt_i64_e32 vcc, s[22:23], v[8:9]
	v_readlane_b32 s23, v9, s99
	s_sub_i32 s22, 63, s99
	s_nop 0
	v_addc_co_u32_e32 v4, vcc, 0, v4, vcc
	v_cmp_gt_i64_e32 vcc, s[24:25], v[8:9]
	v_readlane_b32 s25, v9, s100
	s_sub_i32 s24, 63, s100
	s_add_i32 s100, s100, 1
	v_addc_co_u32_e32 v4, vcc, 0, v4, vcc
	v_cmp_gt_i64_e32 vcc, s[22:23], v[8:9]
	v_readlane_b32 s23, v9, s100
	s_sub_i32 s22, 63, s100
	s_add_i32 s100, s100, 1
	v_addc_co_u32_e32 v4, vcc, 0, v4, vcc
	v_cmp_gt_i64_e32 vcc, s[24:25], v[8:9]
	v_readlane_b32 s25, v9, s100
	s_sub_i32 s24, 63, s100
	s_add_i32 s100, s100, 1
	v_addc_co_u32_e32 v4, vcc, 0, v4, vcc
	v_cmp_gt_i64_e32 vcc, s[22:23], v[8:9]
	v_readlane_b32 s23, v9, s100
	s_sub_i32 s22, 63, s100
	s_add_i32 s100, s100, 1
	v_addc_co_u32_e32 v4, vcc, 0, v4, vcc
	v_cmp_gt_i64_e32 vcc, s[24:25], v[8:9]
	v_readlane_b32 s25, v9, s100
	s_sub_i32 s24, 63, s100
	s_add_i32 s100, s100, 1
	v_addc_co_u32_e32 v4, vcc, 0, v4, vcc
	v_cmp_gt_i64_e32 vcc, s[22:23], v[8:9]
	v_readlane_b32 s23, v9, s100
	s_sub_i32 s22, 63, s100
	s_add_i32 s100, s100, 1
	v_addc_co_u32_e32 v4, vcc, 0, v4, vcc
	v_cmp_gt_i64_e32 vcc, s[24:25], v[8:9]
	v_readlane_b32 s25, v9, s100
	s_sub_i32 s24, 63, s100
	s_add_i32 s100, s100, 1
	v_addc_co_u32_e32 v4, vcc, 0, v4, vcc
	v_cmp_gt_i64_e32 vcc, s[22:23], v[8:9]
	v_readlane_b32 s23, v9, s100
	s_sub_i32 s22, 63, s100
	s_nop 0
	v_addc_co_u32_e32 v4, vcc, 0, v4, vcc
	v_cmp_gt_i64_e32 vcc, s[24:25], v[8:9]
	v_readlane_b32 s25, v9, s101
	s_sub_i32 s24, 63, s101
	s_add_i32 s101, s101, 1
	v_addc_co_u32_e32 v4, vcc, 0, v4, vcc
	v_cmp_gt_i64_e32 vcc, s[22:23], v[8:9]
	v_readlane_b32 s23, v9, s101
	s_sub_i32 s22, 63, s101
	s_add_i32 s101, s101, 1
	v_addc_co_u32_e32 v4, vcc, 0, v4, vcc
	v_cmp_gt_i64_e32 vcc, s[24:25], v[8:9]
	v_readlane_b32 s25, v9, s101
	s_sub_i32 s24, 63, s101
	s_add_i32 s101, s101, 1
	v_addc_co_u32_e32 v4, vcc, 0, v4, vcc
	v_cmp_gt_i64_e32 vcc, s[22:23], v[8:9]
	v_readlane_b32 s23, v9, s101
	s_sub_i32 s22, 63, s101
	s_add_i32 s101, s101, 1
	v_addc_co_u32_e32 v4, vcc, 0, v4, vcc
	v_cmp_gt_i64_e32 vcc, s[24:25], v[8:9]
	v_readlane_b32 s25, v9, s101
	s_sub_i32 s24, 63, s101
	s_add_i32 s101, s101, 1
	v_addc_co_u32_e32 v4, vcc, 0, v4, vcc
	v_cmp_gt_i64_e32 vcc, s[22:23], v[8:9]
	v_readlane_b32 s23, v9, s101
	s_sub_i32 s22, 63, s101
	s_add_i32 s101, s101, 1
	v_addc_co_u32_e32 v4, vcc, 0, v4, vcc
	v_cmp_gt_i64_e32 vcc, s[24:25], v[8:9]
	v_readlane_b32 s25, v9, s101
	s_sub_i32 s24, 63, s101
	s_add_i32 s101, s101, 1
	v_addc_co_u32_e32 v4, vcc, 0, v4, vcc
	v_cmp_gt_i64_e32 vcc, s[22:23], v[8:9]
	v_readlane_b32 s23, v9, s101
	s_sub_i32 s22, 63, s101
	s_nop 0
	v_addc_co_u32_e32 v4, vcc, 0, v4, vcc
	v_cmp_gt_i64_e32 vcc, s[24:25], v[8:9]
	s_nop 1
	v_addc_co_u32_e32 v4, vcc, 0, v4, vcc
	v_cmp_gt_i64_e32 vcc, s[22:23], v[8:9]
	s_nop 1
	v_addc_co_u32_e32 v4, vcc, 0, v4, vcc
	v_cmp_gt_u32_e32 vcc, 6, v4
	s_nop 1
	v_cndmask_b32_e32 v3, 0, v2, vcc
	s_nop 1
	v_add_f32_dpp v3, v3, v3 quad_perm:[1,0,3,2] row_mask:0xf bank_mask:0xf
	s_nop 1
	v_add_f32_dpp v3, v3, v3 quad_perm:[2,3,0,1] row_mask:0xf bank_mask:0xf
	s_nop 1
	v_add_f32_dpp v3, v3, v3 row_half_mirror row_mask:0xf bank_mask:0xf
	s_nop 1
	v_add_f32_dpp v3, v3, v3 row_mirror row_mask:0xf bank_mask:0xf
	v_mov_b32_e32 v5, v3
	s_nop 1
	v_permlane16_swap_b32_e32 v5, v3
	s_waitcnt lgkmcnt(0)
	v_add_f32_e32 v3, v3, v5
	v_mov_b32_e32 v5, v3
	s_nop 1
	v_permlane32_swap_b32_e32 v5, v3
	s_and_saveexec_b64 s[2:3], vcc
	s_cbranch_execz .LBB0_567
	s_waitcnt lgkmcnt(0)
	v_add_f32_e32 v3, v3, v5
	v_div_scale_f32 v9, s[4:5], v3, v3, v2
	v_add3_u32 v4, s36, 42, v4
	v_rcp_f32_e32 v10, v9
	v_ashrrev_i32_e32 v5, 31, v4
	v_lshlrev_b64 v[4:5], 2, v[4:5]
	v_lshl_add_u64 v[6:7], s[26:27], 0, v[4:5]
	ds_add_rtn_u32 v8, v227, v243
	global_store_dword v[6:7], v230, off
	v_fma_f32 v6, -v9, v10, 1.0
	v_fmac_f32_e32 v10, v6, v10
	v_div_scale_f32 v6, vcc, v2, v3, v2
	v_mul_f32_e32 v7, v6, v10
	v_fma_f32 v11, -v9, v7, v6
	v_fmac_f32_e32 v7, v11, v10
	v_fma_f32 v6, -v9, v7, v6
	v_div_fmas_f32 v6, v6, v10, v7
	v_div_fixup_f32 v2, v6, v3, v2
	v_mul_f32_e32 v6, 0x40200000, v2
	v_lshl_add_u64 v[2:3], s[28:29], 0, v[4:5]
	global_store_dword v[2:3], v6, off
	v_lshl_add_u64 v[2:3], s[30:31], 0, v[4:5]
	s_waitcnt lgkmcnt(0)
	global_store_dword v[2:3], v8, off

;     __device__ __forceinline__ void operator()(const f32x4 (&acc)[2][2][4][2], const Unit& u, int wr, int wc, int fr, int fq) const {
;     ...
;                 for (int m = 0; m < 4; ++m) { float s_ = 0.f;
; #pragma unroll
;                     for (int q = 0; q < 4; ++q) { const f32x4 v = acc[ai][q >> 1][m][q & 1]; s_ += v[0] * v[0] + v[1] * v[1] + v[2] * v[2] + v[3] * v[3]; }
;                     s_ += __shfl_xor(s_, 16); s_ += __shfl_xor(s_, 32);
;                     if (fq == 0) xb[(ai * HALF + m * 16) * 4 + wc] = s_; }
.LBB0_1024:
	v_mov_b32_e32 v2, v1
	s_nop 15
	s_nop 7
	s_cmp_lt_i32 s66, 16
	v_add_u32_e32 v2, s54, v2
	s_cselect_b64 s[22:23], -1, 0
	s_cmp_gt_i32 s66, 15
	v_lshl_add_u32 v18, v2, 4, s60
	s_cbranch_scc1 .LBB0_1042
	v_mul_f32_e32 v4, v191, v191
	v_mul_f32_e32 v5, v187, v187
	v_fmac_f32_e32 v4, v190, v190
	v_fmac_f32_e32 v5, v186, v186
	v_fmac_f32_e32 v4, v192, v192
	v_fmac_f32_e32 v5, v188, v188
	v_fmac_f32_e32 v4, v193, v193
	v_fmac_f32_e32 v5, v189, v189
	v_add_f32_e32 v4, v4, v5
	v_mul_f32_e32 v5, v183, v183
	v_fmac_f32_e32 v5, v182, v182
	v_fmac_f32_e32 v5, v184, v184
	v_fmac_f32_e32 v5, v185, v185
	v_and_b32_e32 v3, 64, v250
	v_add_f32_e32 v4, v4, v5
	v_mul_f32_e32 v5, v179, v179
	v_xor_b32_e32 v2, 16, v250
	v_add_u32_e32 v3, 64, v3
	v_fmac_f32_e32 v5, v178, v178
	v_cmp_lt_i32_e32 vcc, v2, v3
	v_fmac_f32_e32 v5, v180, v180
	v_fmac_f32_e32 v5, v181, v181
	v_cndmask_b32_e32 v2, v250, v2, vcc
	v_lshlrev_b32_e32 v2, 2, v2
	v_add_f32_e32 v5, v4, v5
	v_mov_b32_e32 v6, v5
	s_nop 1
	v_permlane16_swap_b32_e32 v6, v5
	v_xor_b32_e32 v4, 32, v250
	v_cmp_lt_i32_e32 vcc, v4, v3
	s_waitcnt lgkmcnt(0)
	v_add_f32_e32 v5, v5, v6
	v_cndmask_b32_e32 v3, v250, v4, vcc
	v_lshlrev_b32_e32 v4, 2, v3
	v_mov_b32_e32 v6, v5
	s_nop 1
	v_permlane32_swap_b32_e32 v6, v5
	v_lshl_add_u32 v3, s52, 2, v18
	s_and_saveexec_b64 s[8:9], s[0:1]
	s_cbranch_execz .LBB0_1027
	s_waitcnt lgkmcnt(0)
	v_add_f32_e32 v5, v5, v6
	ds_write_b32 v3, v5
.LBB0_1027:
	s_or_b64 exec, exec, s[8:9]
	v_mul_f32_e32 v5, v175, v175
	s_waitcnt lgkmcnt(0)
	v_mul_f32_e32 v6, v171, v171
	v_fmac_f32_e32 v5, v174, v174
	v_fmac_f32_e32 v6, v170, v170
	v_fmac_f32_e32 v5, v176, v176
	v_fmac_f32_e32 v6, v172, v172
	v_fmac_f32_e32 v5, v177, v177
	v_fmac_f32_e32 v6, v173, v173
	v_add_f32_e32 v5, v5, v6
	v_mul_f32_e32 v6, v167, v167
	v_fmac_f32_e32 v6, v166, v166
	v_fmac_f32_e32 v6, v168, v168
	v_fmac_f32_e32 v6, v169, v169
	v_add_f32_e32 v5, v5, v6
	v_mul_f32_e32 v6, v163, v163
	v_fmac_f32_e32 v6, v162, v162
	v_fmac_f32_e32 v6, v164, v164
	v_fmac_f32_e32 v6, v165, v165
	v_add_f32_e32 v5, v5, v6
	v_mov_b32_e32 v6, v5
	s_nop 1
	v_permlane16_swap_b32_e32 v6, v5
	s_waitcnt lgkmcnt(0)
	v_add_f32_e32 v5, v5, v6
	v_mov_b32_e32 v6, v5
	s_nop 1
	v_permlane32_swap_b32_e32 v6, v5
	s_and_saveexec_b64 s[8:9], s[0:1]
	s_cbranch_execz .LBB0_1029
	s_waitcnt lgkmcnt(0)
	v_add_f32_e32 v5, v5, v6
	ds_write_b32 v3, v5 offset:256
.LBB0_1029:
	s_or_b64 exec, exec, s[8:9]
	v_mul_f32_e32 v5, v159, v159
	s_waitcnt lgkmcnt(0)
	v_mul_f32_e32 v6, v155, v155
	v_fmac_f32_e32 v5, v158, v158
	v_fmac_f32_e32 v6, v154, v154
	v_fmac_f32_e32 v5, v160, v160
	v_fmac_f32_e32 v6, v156, v156
	v_fmac_f32_e32 v5, v161, v161
	v_fmac_f32_e32 v6, v157, v157
	v_add_f32_e32 v5, v5, v6
	v_mul_f32_e32 v6, v151, v151
	v_fmac_f32_e32 v6, v150, v150
	v_fmac_f32_e32 v6, v152, v152
	v_fmac_f32_e32 v6, v153, v153
	v_add_f32_e32 v5, v5, v6
	v_mul_f32_e32 v6, v147, v147
	v_fmac_f32_e32 v6, v146, v146
	v_fmac_f32_e32 v6, v148, v148
	v_fmac_f32_e32 v6, v149, v149
	v_add_f32_e32 v5, v5, v6
	v_mov_b32_e32 v6, v5
	s_nop 1
	v_permlane16_swap_b32_e32 v6, v5
	s_waitcnt lgkmcnt(0)
	v_add_f32_e32 v5, v5, v6
	v_mov_b32_e32 v6, v5
	s_nop 1
	v_permlane32_swap_b32_e32 v6, v5
	s_and_saveexec_b64 s[8:9], s[0:1]
	s_cbranch_execz .LBB0_1031
	s_waitcnt lgkmcnt(0)
	v_add_f32_e32 v5, v5, v6
	ds_write_b32 v3, v5 offset:512
.LBB0_1031:
	s_or_b64 exec, exec, s[8:9]
	v_mul_f32_e32 v5, v143, v143
	s_waitcnt lgkmcnt(0)
	v_mul_f32_e32 v6, v139, v139
	v_fmac_f32_e32 v5, v142, v142
	v_fmac_f32_e32 v6, v138, v138
	v_fmac_f32_e32 v5, v144, v144
	v_fmac_f32_e32 v6, v140, v140
	v_fmac_f32_e32 v5, v145, v145
	v_fmac_f32_e32 v6, v141, v141
	v_add_f32_e32 v5, v5, v6
	v_mul_f32_e32 v6, v135, v135
	v_fmac_f32_e32 v6, v134, v134
	v_fmac_f32_e32 v6, v136, v136
	v_fmac_f32_e32 v6, v137, v137
	v_add_f32_e32 v5, v5, v6
	v_mul_f32_e32 v6, v131, v131
	v_fmac_f32_e32 v6, v130, v130
	v_fmac_f32_e32 v6, v132, v132
	v_fmac_f32_e32 v6, v133, v133
	v_add_f32_e32 v5, v5, v6
	v_mov_b32_e32 v6, v5
	s_nop 1
	v_permlane16_swap_b32_e32 v6, v5
	s_waitcnt lgkmcnt(0)
	v_add_f32_e32 v5, v5, v6
	v_mov_b32_e32 v6, v5
	s_nop 1
	v_permlane32_swap_b32_e32 v6, v5
	s_and_saveexec_b64 s[8:9], s[0:1]
	s_cbranch_execz .LBB0_1033
	s_waitcnt lgkmcnt(0)
	v_add_f32_e32 v5, v5, v6
	ds_write_b32 v3, v5 offset:768
;     __device__ __forceinline__ void operator()(const f32x4 (&acc)[2][2][4][2], const Unit& u, int wr, int wc, int fr, int fq) const {
;     ...
;                 for (int m = 0; m < 4; ++m) { float s_ = 0.f;
; #pragma unroll
;                     for (int q = 0; q < 4; ++q) { const f32x4 v = acc[ai][q >> 1][m][q & 1]; s_ += v[0] * v[0] + v[1] * v[1] + v[2] * v[2] + v[3] * v[3]; }
;                     s_ += __shfl_xor(s_, 16); s_ += __shfl_xor(s_, 32);
;                     if (fq == 0) xb[(ai * HALF + m * 16) * 4 + wc] = s_; }
.LBB0_1033:
	s_or_b64 exec, exec, s[8:9]
	v_mul_f32_e32 v5, v127, v127
	s_waitcnt lgkmcnt(0)
	v_mul_f32_e32 v6, v123, v123
	v_fmac_f32_e32 v5, v126, v126
	v_fmac_f32_e32 v6, v122, v122
	v_fmac_f32_e32 v5, v128, v128
	v_fmac_f32_e32 v6, v124, v124
	v_fmac_f32_e32 v5, v129, v129
	v_fmac_f32_e32 v6, v125, v125
	v_add_f32_e32 v5, v5, v6
	v_mul_f32_e32 v6, v119, v119
	v_fmac_f32_e32 v6, v118, v118
	v_fmac_f32_e32 v6, v120, v120
	v_fmac_f32_e32 v6, v121, v121
	v_add_f32_e32 v5, v5, v6
	v_mul_f32_e32 v6, v115, v115
	v_fmac_f32_e32 v6, v114, v114
	v_fmac_f32_e32 v6, v116, v116
	v_fmac_f32_e32 v6, v117, v117
	v_add_f32_e32 v5, v5, v6
	v_mov_b32_e32 v6, v5
	s_nop 1
	v_permlane16_swap_b32_e32 v6, v5
	s_waitcnt lgkmcnt(0)
	v_add_f32_e32 v5, v5, v6
	v_mov_b32_e32 v6, v5
	s_nop 1
	v_permlane32_swap_b32_e32 v6, v5
	s_and_saveexec_b64 s[8:9], s[0:1]
	s_cbranch_execz .LBB0_1035
	s_waitcnt lgkmcnt(0)
	v_add_f32_e32 v5, v5, v6
	ds_write_b32 v3, v5 offset:2048
.LBB0_1035:
	s_or_b64 exec, exec, s[8:9]
	v_mul_f32_e32 v5, v111, v111
	s_waitcnt lgkmcnt(0)
	v_mul_f32_e32 v6, v107, v107
	v_fmac_f32_e32 v5, v110, v110
	v_fmac_f32_e32 v6, v106, v106
	v_fmac_f32_e32 v5, v112, v112
	v_fmac_f32_e32 v6, v108, v108
	v_fmac_f32_e32 v5, v113, v113
	v_fmac_f32_e32 v6, v109, v109
	v_add_f32_e32 v5, v5, v6
	v_mul_f32_e32 v6, v103, v103
	v_fmac_f32_e32 v6, v102, v102
	v_fmac_f32_e32 v6, v104, v104
	v_fmac_f32_e32 v6, v105, v105
	v_add_f32_e32 v5, v5, v6
	v_mul_f32_e32 v6, v99, v99
	v_fmac_f32_e32 v6, v98, v98
	v_fmac_f32_e32 v6, v100, v100
	v_fmac_f32_e32 v6, v101, v101
	v_add_f32_e32 v5, v5, v6
	v_mov_b32_e32 v6, v5
	s_nop 1
	v_permlane16_swap_b32_e32 v6, v5
	s_waitcnt lgkmcnt(0)
	v_add_f32_e32 v5, v5, v6
	v_mov_b32_e32 v6, v5
	s_nop 1
	v_permlane32_swap_b32_e32 v6, v5
	s_and_saveexec_b64 s[8:9], s[0:1]
	s_cbranch_execz .LBB0_1037
	s_waitcnt lgkmcnt(0)
	v_add_f32_e32 v5, v5, v6
	ds_write_b32 v3, v5 offset:2304
.LBB0_1037:
	s_or_b64 exec, exec, s[8:9]
	v_mul_f32_e32 v5, v95, v95
	s_waitcnt lgkmcnt(0)
	v_mul_f32_e32 v6, v91, v91
	v_fmac_f32_e32 v5, v94, v94
	v_fmac_f32_e32 v6, v90, v90
	v_fmac_f32_e32 v5, v96, v96
	v_fmac_f32_e32 v6, v92, v92
	v_fmac_f32_e32 v5, v97, v97
	v_fmac_f32_e32 v6, v93, v93
	v_add_f32_e32 v5, v5, v6
	v_mul_f32_e32 v6, v87, v87
	v_fmac_f32_e32 v6, v86, v86
	v_fmac_f32_e32 v6, v88, v88
	v_fmac_f32_e32 v6, v89, v89
	v_add_f32_e32 v5, v5, v6
	v_mul_f32_e32 v6, v83, v83
	v_fmac_f32_e32 v6, v82, v82
	v_fmac_f32_e32 v6, v84, v84
	v_fmac_f32_e32 v6, v85, v85
	v_add_f32_e32 v5, v5, v6
	v_mov_b32_e32 v6, v5
	s_nop 1
	v_permlane16_swap_b32_e32 v6, v5
	s_waitcnt lgkmcnt(0)
	v_add_f32_e32 v5, v5, v6
	v_mov_b32_e32 v6, v5
	s_nop 1
	v_permlane32_swap_b32_e32 v6, v5
	s_and_saveexec_b64 s[8:9], s[0:1]
	s_cbranch_execz .LBB0_1039
	s_waitcnt lgkmcnt(0)
	v_add_f32_e32 v5, v5, v6
	ds_write_b32 v3, v5 offset:2560
.LBB0_1039:
	s_or_b64 exec, exec, s[8:9]
	v_mul_f32_e32 v5, v79, v79
	s_waitcnt lgkmcnt(0)
	v_mul_f32_e32 v6, v75, v75
	v_fmac_f32_e32 v5, v78, v78
	v_fmac_f32_e32 v6, v74, v74
	v_fmac_f32_e32 v5, v80, v80
	v_fmac_f32_e32 v6, v76, v76
	v_fmac_f32_e32 v5, v81, v81
	v_fmac_f32_e32 v6, v77, v77
	v_add_f32_e32 v5, v5, v6
	v_mul_f32_e32 v6, v71, v71
	v_fmac_f32_e32 v6, v70, v70
	v_fmac_f32_e32 v6, v72, v72
	v_fmac_f32_e32 v6, v73, v73
	v_add_f32_e32 v5, v5, v6
	v_mul_f32_e32 v6, v67, v67
	v_fmac_f32_e32 v6, v66, v66
	v_fmac_f32_e32 v6, v68, v68
	v_fmac_f32_e32 v6, v69, v69
	v_add_f32_e32 v5, v5, v6
	v_mov_b32_e32 v2, v5
	s_nop 1
	v_permlane16_swap_b32_e32 v2, v5
	s_waitcnt lgkmcnt(0)
	v_add_f32_e32 v2, v5, v2
	v_mov_b32_e32 v4, v2
	s_nop 1
	v_permlane32_swap_b32_e32 v4, v2
	s_and_saveexec_b64 s[8:9], s[0:1]
	s_cbranch_execz .LBB0_1041
	s_waitcnt lgkmcnt(0)
	v_add_f32_e32 v2, v2, v4
	ds_write_b32 v3, v2 offset:2816

; #define LAS __attribute__((address_space(3)))
; __device__ __forceinline__ void phase_nrr(const Frame& F, const Args& a, int l, const bf16_t* XA, const float* g, const float* modl, unsigned char* XN8) {
;     ...
; #pragma unroll
;         for (int rb = 0; rb < 4; ++rb) *(LAS f32x4*)(Pl + (size_t)((kq * 64 + 16 * rb + fr) * NE + 16 * eb + 4 * fq)) = acc[rb];
;         __syncthreads();
;         const float bias = rbias[lane];
; #pragma unroll
;         for (int i = 0; i < 8; ++i) { const int t = tb + i;
;             const float lg = Pl[(w * 8 + i) * NE + lane] + Pl[(64 + w * 8 + i) * NE + lane]; const float sc = 1.f / (1.f + __expf(-lg)); const float bb = sc + bias;
;             float m1 = bb; m1 = fmaxf(m1, __shfl_xor(m1, 1)); m1 = fmaxf(m1, __shfl_xor(m1, 2)); m1 = fmaxf(m1, __shfl_xor(m1, 4));
;             const unsigned long long eq = __ballot(bb == m1); const int gbase = lane & ~7; const unsigned grpmask = (unsigned)((eq >> gbase) & 0xffull);
;             const int first = gbase + __builtin_ctz(grpmask);
;             float m2 = (lane == first) ? -INFINITY : bb; m2 = fmaxf(m2, __shfl_xor(m2, 1)); m2 = fmaxf(m2, __shfl_xor(m2, 2)); m2 = fmaxf(m2, __shfl_xor(m2, 4));
;             const float gsum = m1 + m2; const int gq = lane >> 3;
;             int grank = 0;
; #pragma unroll
;             for (int g2 = 0; g2 < 8; ++g2) { const float v = __int_as_float(__builtin_amdgcn_readlane(__float_as_int(gsum), g2 * 8)); grank += (v > gsum || (v == gsum && g2 < gq)) ? 1 : 0; }
;             const bool keep = grank < 4; const float val = keep ? bb : -INFINITY;
;             int rank = 0;
; #pragma unroll 8
;             for (int e2 = 0; e2 < 64; ++e2) { const float v = __int_as_float(__builtin_amdgcn_readlane(__float_as_int(val), e2)); rank += (v > val || (v == val && e2 < lane)) ? 1 : 0; }
.LBB0_1308:
	s_barrier
	ds_write_b128 v242, v[110:113]
	ds_write_b128 v242, v[118:121] offset:4096
	s_nop 0
	ds_write_b128 v242, v[126:129] offset:8192
	s_nop 1
	ds_write_b128 v242, v[130:133] offset:12288
	s_waitcnt lgkmcnt(0)
	s_barrier
	global_load_dword v3, v[198:199], off offset:256
	s_waitcnt vmcnt(15)
	v_add_u32_e32 v4, s33, v226
	ds_read2st64_b32 v[6:7], v4 offset1:64
	s_mov_b32 s3, 0
	s_waitcnt lgkmcnt(0)
	v_add_f32_e32 v2, v6, v7
	v_mul_f32_e32 v2, 0xbfb8aa3b, v2
	v_exp_f32_e32 v2, v2
	s_nop 0
	v_add_f32_e32 v2, 1.0, v2
	v_div_scale_f32 v5, s[20:21], v2, v2, 1.0
	v_rcp_f32_e32 v6, v5
	s_nop 0
	v_fma_f32 v7, -v5, v6, 1.0
	v_fmac_f32_e32 v6, v7, v6
	v_div_scale_f32 v7, vcc, 1.0, v2, 1.0
	v_mul_f32_e32 v8, v7, v6
	v_fma_f32 v9, -v5, v8, v7
	v_fmac_f32_e32 v8, v9, v6
	v_fma_f32 v5, -v5, v8, v7
	v_div_fmas_f32 v5, v5, v6, v8
	v_div_fixup_f32 v2, v5, v2, 1.0
	s_waitcnt vmcnt(0)
	v_add_f32_e32 v5, v3, v2
	s_nop 1
	s_waitcnt lgkmcnt(0)
	v_max_f32_dpp v6, v5, v5 quad_perm:[1,0,3,2] row_mask:0xf bank_mask:0xf
	s_nop 1
	s_waitcnt lgkmcnt(0)
	v_max_f32_dpp v6, v6, v6 quad_perm:[2,3,0,1] row_mask:0xf bank_mask:0xf
	s_nop 1
	s_waitcnt lgkmcnt(0)
	v_max_f32_dpp v8, v6, v6 row_half_mirror row_mask:0xf bank_mask:0xf
	v_cmp_eq_f32_e32 vcc, v5, v8
	s_nop 1
	v_lshrrev_b64 v[6:7], v200, vcc
	v_ffbl_b32_sdwa v6, v6 dst_sel:DWORD dst_unused:UNUSED_PAD src0_sel:BYTE_0
	v_add_u32_e32 v6, v6, v200
	v_cmp_ne_u32_e32 vcc, v230, v6
	s_nop 1
	v_cndmask_b32_e32 v6, v245, v5, vcc
	s_nop 1
	s_waitcnt lgkmcnt(0)
	v_max_f32_dpp v6, v6, v6 quad_perm:[1,0,3,2] row_mask:0xf bank_mask:0xf
	s_nop 1
	s_waitcnt lgkmcnt(0)
	v_max_f32_dpp v6, v6, v6 quad_perm:[2,3,0,1] row_mask:0xf bank_mask:0xf
	s_nop 1
	s_waitcnt lgkmcnt(0)
	v_max_f32_dpp v6, v6, v6 row_half_mirror row_mask:0xf bank_mask:0xf
	v_add_f32_e32 v6, v8, v6
	s_nop 0
	v_readlane_b32 s5, v6, 0
	s_nop 1
	v_cmp_eq_f32_e64 s[20:21], s5, v6
	v_cmp_gt_f32_e32 vcc, s5, v6
	s_and_b64 s[20:21], s[0:1], s[20:21]
	s_or_b64 s[20:21], vcc, s[20:21]
	v_readlane_b32 s5, v6, 8
	v_cndmask_b32_e64 v7, 0, 1, s[20:21]
	s_nop 0
	v_cmp_eq_f32_e64 s[20:21], s5, v6
	v_cmp_gt_f32_e32 vcc, s5, v6
	s_and_b64 s[20:21], s[6:7], s[20:21]
	s_or_b64 s[20:21], vcc, s[20:21]
	v_readlane_b32 s5, v6, 16
	v_cndmask_b32_e64 v8, 0, 1, s[20:21]
	s_nop 0
	v_cmp_eq_f32_e64 s[20:21], s5, v6
	v_cmp_gt_f32_e32 vcc, s5, v6
	s_and_b64 s[20:21], s[8:9], s[20:21]
	s_or_b64 s[20:21], vcc, s[20:21]
	v_readlane_b32 s5, v6, 24
	v_cndmask_b32_e64 v9, 0, 1, s[20:21]
	s_nop 0
	v_cmp_eq_f32_e64 s[20:21], s5, v6
	v_cmp_gt_f32_e32 vcc, s5, v6
	s_and_b64 s[20:21], s[10:11], s[20:21]
	s_or_b64 s[20:21], vcc, s[20:21]
	v_readlane_b32 s5, v6, 32
	v_cndmask_b32_e64 v10, 0, 1, s[20:21]
	s_nop 0
	v_cmp_eq_f32_e64 s[20:21], s5, v6
	v_cmp_gt_f32_e32 vcc, s5, v6
	s_and_b64 s[20:21], s[12:13], s[20:21]
	s_or_b64 s[20:21], vcc, s[20:21]
	v_readlane_b32 s5, v6, 40
	v_cndmask_b32_e64 v11, 0, 1, s[20:21]
	s_nop 0
	v_cmp_eq_f32_e64 s[20:21], s5, v6
	v_cmp_gt_f32_e32 vcc, s5, v6
	s_and_b64 s[20:21], s[14:15], s[20:21]
	s_or_b64 s[20:21], vcc, s[20:21]
	v_readlane_b32 s5, v6, 48
	v_cndmask_b32_e64 v12, 0, 1, s[20:21]
	s_nop 0
	v_cmp_eq_f32_e64 s[20:21], s5, v6
	v_cmp_gt_f32_e32 vcc, s5, v6
	s_and_b64 s[20:21], s[16:17], s[20:21]
	v_readlane_b32 s5, v6, 56
	s_or_b64 s[20:21], vcc, s[20:21]
	v_cndmask_b32_e64 v13, 0, 1, s[20:21]
	v_cmp_gt_f32_e32 vcc, s5, v6
	s_nop 1
	v_cndmask_b32_e64 v6, 0, 1, vcc
	v_add_u32_e32 v6, v8, v6
	v_add3_u32 v6, v6, v7, v9
	v_add3_u32 v6, v6, v10, v11
	v_add3_u32 v6, v6, v12, v13
	v_cmp_eq_u32_e32 vcc, 0, v6
	s_ff1_i32_b64 s98, vcc
	v_cmp_eq_u32_e32 vcc, 1, v6
	s_ff1_i32_b64 s99, vcc
	v_cmp_eq_u32_e32 vcc, 2, v6
	s_ff1_i32_b64 s100, vcc
	v_cmp_eq_u32_e32 vcc, 3, v6
	s_ff1_i32_b64 s101, vcc
	v_cmp_gt_u32_e32 vcc, 4, v6
	v_mov_b32_e32 v6, 0
	s_nop 0
	v_cndmask_b32_e32 v5, v245, v5, vcc
	v_ashrrev_i32_e32 v9, 31, v5
	v_sub_u32_e32 v8, 63, v230
	v_and_b32_e32 v9, 0x7fffffff, v9
	v_xor_b32_e32 v9, v5, v9
	s_nop 0
	v_readlane_b32 s23, v9, s98
	s_sub_i32 s22, 63, s98
	s_add_i32 s98, s98, 1
	v_readlane_b32 s21, v9, s98
	s_sub_i32 s20, 63, s98
	s_add_i32 s98, s98, 1
	v_cmp_gt_i64_e32 vcc, s[22:23], v[8:9]
	v_readlane_b32 s23, v9, s98
	s_sub_i32 s22, 63, s98
	s_add_i32 s98, s98, 1
	v_addc_co_u32_e32 v6, vcc, 0, v6, vcc
	v_cmp_gt_i64_e32 vcc, s[20:21], v[8:9]
	v_readlane_b32 s21, v9, s98
	s_sub_i32 s20, 63, s98
	s_add_i32 s98, s98, 1
	v_addc_co_u32_e32 v6, vcc, 0, v6, vcc
	v_cmp_gt_i64_e32 vcc, s[22:23], v[8:9]
	v_readlane_b32 s23, v9, s98
	s_sub_i32 s22, 63, s98
	s_add_i32 s98, s98, 1
	v_addc_co_u32_e32 v6, vcc, 0, v6, vcc
	v_cmp_gt_i64_e32 vcc, s[20:21], v[8:9]
	v_readlane_b32 s21, v9, s98
	s_sub_i32 s20, 63, s98
	s_add_i32 s98, s98, 1
	v_addc_co_u32_e32 v6, vcc, 0, v6, vcc
	v_cmp_gt_i64_e32 vcc, s[22:23], v[8:9]
	v_readlane_b32 s23, v9, s98
	s_sub_i32 s22, 63, s98
	s_add_i32 s98, s98, 1
	v_addc_co_u32_e32 v6, vcc, 0, v6, vcc
	v_cmp_gt_i64_e32 vcc, s[20:21], v[8:9]
	v_readlane_b32 s21, v9, s98
	s_sub_i32 s20, 63, s98
	s_nop 0
	v_addc_co_u32_e32 v6, vcc, 0, v6, vcc
	v_cmp_gt_i64_e32 vcc, s[22:23], v[8:9]
	v_readlane_b32 s23, v9, s99
	s_sub_i32 s22, 63, s99
	s_add_i32 s99, s99, 1
	v_addc_co_u32_e32 v6, vcc, 0, v6, vcc
	v_cmp_gt_i64_e32 vcc, s[20:21], v[8:9]
	v_readlane_b32 s21, v9, s99
	s_sub_i32 s20, 63, s99
	s_add_i32 s99, s99, 1
	v_addc_co_u32_e32 v6, vcc, 0, v6, vcc
	v_cmp_gt_i64_e32 vcc, s[22:23], v[8:9]
	v_readlane_b32 s23, v9, s99
	s_sub_i32 s22, 63, s99
	s_add_i32 s99, s99, 1
	v_addc_co_u32_e32 v6, vcc, 0, v6, vcc
	v_cmp_gt_i64_e32 vcc, s[20:21], v[8:9]
	v_readlane_b32 s21, v9, s99
	s_sub_i32 s20, 63, s99
	s_add_i32 s99, s99, 1
	v_addc_co_u32_e32 v6, vcc, 0, v6, vcc
; __device__ __forceinline__ void phase_nrr(const Frame& F, const Args& a, int l, const bf16_t* XA, const float* g, const float* modl, unsigned char* XN8) {
;     ...
;             const bool keep = grank < 4; const float val = keep ? bb : -INFINITY;
;             int rank = 0;
; #pragma unroll 8
;             for (int e2 = 0; e2 < 64; ++e2) { const float v = __int_as_float(__builtin_amdgcn_readlane(__float_as_int(val), e2)); rank += (v > val || (v == val && e2 < lane)) ? 1 : 0; }
;             const bool sel = rank < TOPK;
;             const float ssum = wave_sum(sel ? sc : 0.f);
;             if (sel) { const int p = atomicAdd((int*)(hist + lane), 1); top_e[t * TOPK + rank] = lane; gate[t * TOPK + rank] = sc / ssum * 2.5f; lpos[t * TOPK + rank] = p; }
	v_cmp_gt_i64_e32 vcc, s[22:23], v[8:9]
	v_readlane_b32 s23, v9, s99
	s_sub_i32 s22, 63, s99
	s_add_i32 s99, s99, 1
	v_addc_co_u32_e32 v6, vcc, 0, v6, vcc
	v_cmp_gt_i64_e32 vcc, s[20:21], v[8:9]
	v_readlane_b32 s21, v9, s99
	s_sub_i32 s20, 63, s99
	s_add_i32 s99, s99, 1
	v_addc_co_u32_e32 v6, vcc, 0, v6, vcc
	v_cmp_gt_i64_e32 vcc, s[22:23], v[8:9]
	v_readlane_b32 s23, v9, s99
	s_sub_i32 s22, 63, s99
	s_add_i32 s99, s99, 1
	v_addc_co_u32_e32 v6, vcc, 0, v6, vcc
	v_cmp_gt_i64_e32 vcc, s[20:21], v[8:9]
	v_readlane_b32 s21, v9, s99
	s_sub_i32 s20, 63, s99
	s_nop 0
	v_addc_co_u32_e32 v6, vcc, 0, v6, vcc
	v_cmp_gt_i64_e32 vcc, s[22:23], v[8:9]
	v_readlane_b32 s23, v9, s100
	s_sub_i32 s22, 63, s100
	s_add_i32 s100, s100, 1
	v_addc_co_u32_e32 v6, vcc, 0, v6, vcc
	v_cmp_gt_i64_e32 vcc, s[20:21], v[8:9]
	v_readlane_b32 s21, v9, s100
	s_sub_i32 s20, 63, s100
	s_add_i32 s100, s100, 1
	v_addc_co_u32_e32 v6, vcc, 0, v6, vcc
	v_cmp_gt_i64_e32 vcc, s[22:23], v[8:9]
	v_readlane_b32 s23, v9, s100
	s_sub_i32 s22, 63, s100
	s_add_i32 s100, s100, 1
	v_addc_co_u32_e32 v6, vcc, 0, v6, vcc
	v_cmp_gt_i64_e32 vcc, s[20:21], v[8:9]
	v_readlane_b32 s21, v9, s100
	s_sub_i32 s20, 63, s100
	s_add_i32 s100, s100, 1
	v_addc_co_u32_e32 v6, vcc, 0, v6, vcc
	v_cmp_gt_i64_e32 vcc, s[22:23], v[8:9]
	v_readlane_b32 s23, v9, s100
	s_sub_i32 s22, 63, s100
	s_add_i32 s100, s100, 1
	v_addc_co_u32_e32 v6, vcc, 0, v6, vcc
	v_cmp_gt_i64_e32 vcc, s[20:21], v[8:9]
	v_readlane_b32 s21, v9, s100
	s_sub_i32 s20, 63, s100
	s_add_i32 s100, s100, 1
	v_addc_co_u32_e32 v6, vcc, 0, v6, vcc
	v_cmp_gt_i64_e32 vcc, s[22:23], v[8:9]
	v_readlane_b32 s23, v9, s100
	s_sub_i32 s22, 63, s100
	s_add_i32 s100, s100, 1
	v_addc_co_u32_e32 v6, vcc, 0, v6, vcc
	v_cmp_gt_i64_e32 vcc, s[20:21], v[8:9]
	v_readlane_b32 s21, v9, s100
	s_sub_i32 s20, 63, s100
	s_nop 0
	v_addc_co_u32_e32 v6, vcc, 0, v6, vcc
	v_cmp_gt_i64_e32 vcc, s[22:23], v[8:9]
	v_readlane_b32 s23, v9, s101
	s_sub_i32 s22, 63, s101
	s_add_i32 s101, s101, 1
	v_addc_co_u32_e32 v6, vcc, 0, v6, vcc
	v_cmp_gt_i64_e32 vcc, s[20:21], v[8:9]
	v_readlane_b32 s21, v9, s101
	s_sub_i32 s20, 63, s101
	s_add_i32 s101, s101, 1
	v_addc_co_u32_e32 v6, vcc, 0, v6, vcc
	v_cmp_gt_i64_e32 vcc, s[22:23], v[8:9]
	v_readlane_b32 s23, v9, s101
	s_sub_i32 s22, 63, s101
	s_add_i32 s101, s101, 1
	v_addc_co_u32_e32 v6, vcc, 0, v6, vcc
	v_cmp_gt_i64_e32 vcc, s[20:21], v[8:9]
	v_readlane_b32 s21, v9, s101
	s_sub_i32 s20, 63, s101
	s_add_i32 s101, s101, 1
	v_addc_co_u32_e32 v6, vcc, 0, v6, vcc
	v_cmp_gt_i64_e32 vcc, s[22:23], v[8:9]
	v_readlane_b32 s23, v9, s101
	s_sub_i32 s22, 63, s101
	s_add_i32 s101, s101, 1
	v_addc_co_u32_e32 v6, vcc, 0, v6, vcc
	v_cmp_gt_i64_e32 vcc, s[20:21], v[8:9]
	v_readlane_b32 s21, v9, s101
	s_sub_i32 s20, 63, s101
	s_add_i32 s101, s101, 1
	v_addc_co_u32_e32 v6, vcc, 0, v6, vcc
	v_cmp_gt_i64_e32 vcc, s[22:23], v[8:9]
	v_readlane_b32 s23, v9, s101
	s_sub_i32 s22, 63, s101
	s_add_i32 s101, s101, 1
	v_addc_co_u32_e32 v6, vcc, 0, v6, vcc
	v_cmp_gt_i64_e32 vcc, s[20:21], v[8:9]
	v_readlane_b32 s21, v9, s101
	s_sub_i32 s20, 63, s101
	s_nop 0
	v_addc_co_u32_e32 v6, vcc, 0, v6, vcc
	v_cmp_gt_i64_e32 vcc, s[22:23], v[8:9]
	s_nop 1
	v_addc_co_u32_e32 v6, vcc, 0, v6, vcc
	v_cmp_gt_i64_e32 vcc, s[20:21], v[8:9]
	s_nop 1
	v_addc_co_u32_e32 v6, vcc, 0, v6, vcc
	v_cmp_gt_u32_e32 vcc, 6, v6
	s_mul_i32 s50, s24, 6
	s_nop 0
	v_cndmask_b32_e32 v5, 0, v2, vcc
	s_nop 1
	v_add_f32_dpp v5, v5, v5 quad_perm:[1,0,3,2] row_mask:0xf bank_mask:0xf
	s_nop 1
	v_add_f32_dpp v5, v5, v5 quad_perm:[2,3,0,1] row_mask:0xf bank_mask:0xf
	s_nop 1
	v_add_f32_dpp v5, v5, v5 row_half_mirror row_mask:0xf bank_mask:0xf
	s_nop 1
	v_add_f32_dpp v5, v5, v5 row_mirror row_mask:0xf bank_mask:0xf
	v_mov_b32_e32 v7, v5
	s_nop 1
	v_permlane16_swap_b32_e32 v7, v5
	s_waitcnt lgkmcnt(0)
	v_add_f32_e32 v5, v5, v7
	v_mov_b32_e32 v7, v5
	s_nop 1
	v_permlane32_swap_b32_e32 v7, v5
	s_and_saveexec_b64 s[20:21], vcc
	s_cbranch_execz .LBB0_1312
	s_waitcnt lgkmcnt(0)
	v_add_f32_e32 v5, v5, v7
	v_div_scale_f32 v11, s[22:23], v5, v5, v2
	v_or_b32_e32 v6, s50, v6
	v_rcp_f32_e32 v12, v11
	v_ashrrev_i32_e32 v7, 31, v6
	v_lshlrev_b64 v[6:7], 2, v[6:7]
	v_lshl_add_u64 v[8:9], s[42:43], 0, v[6:7]
	ds_add_rtn_u32 v10, v227, v243
	global_store_dword v[8:9], v230, off
	v_fma_f32 v8, -v11, v12, 1.0
	v_fmac_f32_e32 v12, v8, v12
	v_div_scale_f32 v8, vcc, v2, v5, v2
	v_mul_f32_e32 v9, v8, v12
	v_fma_f32 v13, -v11, v9, v8
	v_fmac_f32_e32 v9, v13, v12
	v_fma_f32 v8, -v11, v9, v8
	v_div_fmas_f32 v8, v8, v12, v9
	v_div_fixup_f32 v2, v8, v5, v2
	v_mul_f32_e32 v2, 0x40200000, v2
	v_lshl_add_u64 v[8:9], s[44:45], 0, v[6:7]
	v_lshl_add_u64 v[6:7], s[46:47], 0, v[6:7]
	global_store_dword v[8:9], v2, off
	s_waitcnt lgkmcnt(0)
	global_store_dword v[6:7], v10, off
; __device__ __forceinline__ void phase_nrr(const Frame& F, const Args& a, int l, const bf16_t* XA, const float* g, const float* modl, unsigned char* XN8) {
;     ...
;         for (int i = 0; i < 8; ++i) { const int t = tb + i;
;             const float lg = Pl[(w * 8 + i) * NE + lane] + Pl[(64 + w * 8 + i) * NE + lane]; const float sc = 1.f / (1.f + __expf(-lg)); const float bb = sc + bias;
;             float m1 = bb; m1 = fmaxf(m1, __shfl_xor(m1, 1)); m1 = fmaxf(m1, __shfl_xor(m1, 2)); m1 = fmaxf(m1, __shfl_xor(m1, 4));
;             const unsigned long long eq = __ballot(bb == m1); const int gbase = lane & ~7; const unsigned grpmask = (unsigned)((eq >> gbase) & 0xffull);
;             const int first = gbase + __builtin_ctz(grpmask);
;             float m2 = (lane == first) ? -INFINITY : bb; m2 = fmaxf(m2, __shfl_xor(m2, 1)); m2 = fmaxf(m2, __shfl_xor(m2, 2)); m2 = fmaxf(m2, __shfl_xor(m2, 4));
;             const float gsum = m1 + m2; const int gq = lane >> 3;
;             int grank = 0;
; #pragma unroll
;             for (int g2 = 0; g2 < 8; ++g2) { const float v = __int_as_float(__builtin_amdgcn_readlane(__float_as_int(gsum), g2 * 8)); grank += (v > gsum || (v == gsum && g2 < gq)) ? 1 : 0; }
;             const bool keep = grank < 4; const float val = keep ? bb : -INFINITY;
;             int rank = 0;
; #pragma unroll 8
;             for (int e2 = 0; e2 < 64; ++e2) { const float v = __int_as_float(__builtin_amdgcn_readlane(__float_as_int(val), e2)); rank += (v > val || (v == val && e2 < lane)) ? 1 : 0; }
.LBB0_1312:
	s_or_b64 exec, exec, s[20:21]
	v_add_u32_e32 v2, s76, v226
	ds_read_b32 v2, v2
	ds_read_b32 v5, v4 offset:16640
	s_mov_b32 s3, 0
	s_waitcnt lgkmcnt(0)
	v_add_f32_e32 v2, v2, v5
	v_mul_f32_e32 v2, 0xbfb8aa3b, v2
	v_exp_f32_e32 v2, v2
	s_nop 0
	v_add_f32_e32 v2, 1.0, v2
	v_div_scale_f32 v5, s[20:21], v2, v2, 1.0
	v_rcp_f32_e32 v6, v5
	v_div_scale_f32 v7, vcc, 1.0, v2, 1.0
	v_fma_f32 v8, -v5, v6, 1.0
	v_fmac_f32_e32 v6, v8, v6
	v_mul_f32_e32 v8, v7, v6
	v_fma_f32 v9, -v5, v8, v7
	v_fmac_f32_e32 v8, v9, v6
	v_fma_f32 v5, -v5, v8, v7
	v_div_fmas_f32 v5, v5, v6, v8
	v_div_fixup_f32 v5, v5, v2, 1.0
	v_add_f32_e32 v2, v3, v5
	s_nop 1
	s_waitcnt lgkmcnt(0)
	v_max_f32_dpp v6, v2, v2 quad_perm:[1,0,3,2] row_mask:0xf bank_mask:0xf
	s_nop 1
	s_waitcnt lgkmcnt(0)
	v_max_f32_dpp v6, v6, v6 quad_perm:[2,3,0,1] row_mask:0xf bank_mask:0xf
	s_nop 1
	s_waitcnt lgkmcnt(0)
	v_max_f32_dpp v8, v6, v6 row_half_mirror row_mask:0xf bank_mask:0xf
	v_cmp_eq_f32_e32 vcc, v2, v8
	s_nop 1
	v_lshrrev_b64 v[6:7], v200, vcc
	v_ffbl_b32_sdwa v6, v6 dst_sel:DWORD dst_unused:UNUSED_PAD src0_sel:BYTE_0
	v_add_u32_e32 v6, v6, v200
	v_cmp_ne_u32_e32 vcc, v230, v6
	s_nop 1
	v_cndmask_b32_e32 v6, v245, v2, vcc
	s_nop 1
	s_waitcnt lgkmcnt(0)
	v_max_f32_dpp v6, v6, v6 quad_perm:[1,0,3,2] row_mask:0xf bank_mask:0xf
	s_nop 1
	s_waitcnt lgkmcnt(0)
	v_max_f32_dpp v6, v6, v6 quad_perm:[2,3,0,1] row_mask:0xf bank_mask:0xf
	s_nop 1
	s_waitcnt lgkmcnt(0)
	v_max_f32_dpp v6, v6, v6 row_half_mirror row_mask:0xf bank_mask:0xf
	v_add_f32_e32 v6, v8, v6
	s_nop 0
	v_readlane_b32 s5, v6, 0
	v_readlane_b32 s24, v6, 8
	v_readlane_b32 s28, v6, 16
	v_cmp_eq_f32_e64 s[20:21], s5, v6
	v_cmp_gt_f32_e32 vcc, s5, v6
	v_cmp_gt_f32_e64 s[22:23], s24, v6
	v_cmp_eq_f32_e64 s[24:25], s24, v6
	s_and_b64 s[20:21], s[0:1], s[20:21]
	v_readlane_b32 s34, v6, 24
	v_cmp_gt_f32_e64 s[26:27], s28, v6
	v_cmp_eq_f32_e64 s[28:29], s28, v6
	s_and_b64 s[24:25], s[6:7], s[24:25]
	s_or_b64 s[20:21], vcc, s[20:21]
	v_readlane_b32 s40, v6, 32
	v_cmp_gt_f32_e64 s[30:31], s34, v6
	v_cmp_eq_f32_e64 s[34:35], s34, v6
	s_and_b64 s[28:29], s[8:9], s[28:29]
	v_cndmask_b32_e64 v7, 0, 1, s[20:21]
	s_or_b64 s[20:21], s[22:23], s[24:25]
	v_cmp_gt_f32_e64 s[36:37], s40, v6
	v_cmp_eq_f32_e64 s[40:41], s40, v6
	s_and_b64 s[34:35], s[10:11], s[34:35]
	v_cndmask_b32_e64 v8, 0, 1, s[20:21]
	s_or_b64 s[20:21], s[26:27], s[28:29]
	s_and_b64 s[40:41], s[12:13], s[40:41]
	v_cndmask_b32_e64 v9, 0, 1, s[20:21]
	s_or_b64 s[20:21], s[30:31], s[34:35]
	v_readlane_b32 s55, v6, 40
	v_cndmask_b32_e64 v10, 0, 1, s[20:21]
	s_or_b64 s[20:21], s[36:37], s[40:41]
	v_cndmask_b32_e64 v11, 0, 1, s[20:21]
	v_cmp_eq_f32_e64 s[20:21], s55, v6
	v_cmp_gt_f32_e32 vcc, s55, v6
	s_and_b64 s[20:21], s[14:15], s[20:21]
	s_or_b64 s[20:21], vcc, s[20:21]
	v_readlane_b32 s5, v6, 48
	v_cndmask_b32_e64 v12, 0, 1, s[20:21]
	s_nop 0
	v_cmp_eq_f32_e64 s[20:21], s5, v6
	v_cmp_gt_f32_e32 vcc, s5, v6
	s_and_b64 s[20:21], s[16:17], s[20:21]
	v_readlane_b32 s5, v6, 56
	s_or_b64 s[20:21], vcc, s[20:21]
	v_cndmask_b32_e64 v13, 0, 1, s[20:21]
	v_cmp_gt_f32_e32 vcc, s5, v6
	s_nop 1
	v_cndmask_b32_e64 v6, 0, 1, vcc
	v_add_u32_e32 v6, v8, v6
	v_add3_u32 v6, v6, v7, v9
	v_add3_u32 v6, v6, v10, v11
	v_add3_u32 v6, v6, v12, v13
	v_cmp_eq_u32_e32 vcc, 0, v6
	s_ff1_i32_b64 s98, vcc
	v_cmp_eq_u32_e32 vcc, 1, v6
	s_ff1_i32_b64 s99, vcc
	v_cmp_eq_u32_e32 vcc, 2, v6
	s_ff1_i32_b64 s100, vcc
	v_cmp_eq_u32_e32 vcc, 3, v6
	s_ff1_i32_b64 s101, vcc
	v_cmp_gt_u32_e32 vcc, 4, v6
	s_nop 1
	v_cndmask_b32_e32 v6, v245, v2, vcc
	v_mov_b32_e32 v2, 0
	v_ashrrev_i32_e32 v9, 31, v6
	v_sub_u32_e32 v8, 63, v230
	v_and_b32_e32 v9, 0x7fffffff, v9
	v_xor_b32_e32 v9, v6, v9
	s_nop 0
	v_readlane_b32 s23, v9, s98
	s_sub_i32 s22, 63, s98
	s_add_i32 s98, s98, 1
	v_readlane_b32 s21, v9, s98
	s_sub_i32 s20, 63, s98
	s_add_i32 s98, s98, 1
	v_cmp_gt_i64_e32 vcc, s[22:23], v[8:9]
	v_readlane_b32 s23, v9, s98
	s_sub_i32 s22, 63, s98
	s_add_i32 s98, s98, 1
	v_addc_co_u32_e32 v2, vcc, 0, v2, vcc
	v_cmp_gt_i64_e32 vcc, s[20:21], v[8:9]
	v_readlane_b32 s21, v9, s98
	s_sub_i32 s20, 63, s98
	s_add_i32 s98, s98, 1
	v_addc_co_u32_e32 v2, vcc, 0, v2, vcc
	v_cmp_gt_i64_e32 vcc, s[22:23], v[8:9]
	v_readlane_b32 s23, v9, s98
	s_sub_i32 s22, 63, s98
	s_add_i32 s98, s98, 1
	v_addc_co_u32_e32 v2, vcc, 0, v2, vcc
	v_cmp_gt_i64_e32 vcc, s[20:21], v[8:9]
	v_readlane_b32 s21, v9, s98
	s_sub_i32 s20, 63, s98
	s_add_i32 s98, s98, 1
	v_addc_co_u32_e32 v2, vcc, 0, v2, vcc
	v_cmp_gt_i64_e32 vcc, s[22:23], v[8:9]
	v_readlane_b32 s23, v9, s98
	s_sub_i32 s22, 63, s98
	s_add_i32 s98, s98, 1
	v_addc_co_u32_e32 v2, vcc, 0, v2, vcc
	v_cmp_gt_i64_e32 vcc, s[20:21], v[8:9]
	v_readlane_b32 s21, v9, s98
	s_sub_i32 s20, 63, s98
	s_nop 0
	v_addc_co_u32_e32 v2, vcc, 0, v2, vcc
	v_cmp_gt_i64_e32 vcc, s[22:23], v[8:9]
	v_readlane_b32 s23, v9, s99
	s_sub_i32 s22, 63, s99
	s_add_i32 s99, s99, 1
	v_addc_co_u32_e32 v2, vcc, 0, v2, vcc
	v_cmp_gt_i64_e32 vcc, s[20:21], v[8:9]
	v_readlane_b32 s21, v9, s99
	s_sub_i32 s20, 63, s99
	s_add_i32 s99, s99, 1
	v_addc_co_u32_e32 v2, vcc, 0, v2, vcc
	v_cmp_gt_i64_e32 vcc, s[22:23], v[8:9]
	v_readlane_b32 s23, v9, s99
	s_sub_i32 s22, 63, s99
	s_add_i32 s99, s99, 1
	v_addc_co_u32_e32 v2, vcc, 0, v2, vcc
	v_cmp_gt_i64_e32 vcc, s[20:21], v[8:9]
	v_readlane_b32 s21, v9, s99
	s_sub_i32 s20, 63, s99
	s_add_i32 s99, s99, 1
	v_addc_co_u32_e32 v2, vcc, 0, v2, vcc
	v_cmp_gt_i64_e32 vcc, s[22:23], v[8:9]
	v_readlane_b32 s23, v9, s99
	s_sub_i32 s22, 63, s99
	s_add_i32 s99, s99, 1
	v_addc_co_u32_e32 v2, vcc, 0, v2, vcc
	v_cmp_gt_i64_e32 vcc, s[20:21], v[8:9]
	v_readlane_b32 s21, v9, s99
	s_sub_i32 s20, 63, s99
	s_add_i32 s99, s99, 1
; __device__ __forceinline__ float wave_sum(float v) {
; #pragma unroll
;     for (int o = 1; o < 64; o <<= 1) v += __shfl_xor(v, o);
;     return v;
; __device__ __forceinline__ void phase_nrr(const Frame& F, const Args& a, int l, const bf16_t* XA, const float* g, const float* modl, unsigned char* XN8) {
;     ...
;             for (int e2 = 0; e2 < 64; ++e2) { const float v = __int_as_float(__builtin_amdgcn_readlane(__float_as_int(val), e2)); rank += (v > val || (v == val && e2 < lane)) ? 1 : 0; }
;             const bool sel = rank < TOPK;
;             const float ssum = wave_sum(sel ? sc : 0.f);
;             if (sel) { const int p = atomicAdd((int*)(hist + lane), 1); top_e[t * TOPK + rank] = lane; gate[t * TOPK + rank] = sc / ssum * 2.5f; lpos[t * TOPK + rank] = p; }
	v_addc_co_u32_e32 v2, vcc, 0, v2, vcc
	v_cmp_gt_i64_e32 vcc, s[22:23], v[8:9]
	v_readlane_b32 s23, v9, s99
	s_sub_i32 s22, 63, s99
	s_add_i32 s99, s99, 1
	v_addc_co_u32_e32 v2, vcc, 0, v2, vcc
	v_cmp_gt_i64_e32 vcc, s[20:21], v[8:9]
	v_readlane_b32 s21, v9, s99
	s_sub_i32 s20, 63, s99
	s_nop 0
	v_addc_co_u32_e32 v2, vcc, 0, v2, vcc
	v_cmp_gt_i64_e32 vcc, s[22:23], v[8:9]
	v_readlane_b32 s23, v9, s100
	s_sub_i32 s22, 63, s100
	s_add_i32 s100, s100, 1
	v_addc_co_u32_e32 v2, vcc, 0, v2, vcc
	v_cmp_gt_i64_e32 vcc, s[20:21], v[8:9]
	v_readlane_b32 s21, v9, s100
	s_sub_i32 s20, 63, s100
	s_add_i32 s100, s100, 1
	v_addc_co_u32_e32 v2, vcc, 0, v2, vcc
	v_cmp_gt_i64_e32 vcc, s[22:23], v[8:9]
	v_readlane_b32 s23, v9, s100
	s_sub_i32 s22, 63, s100
	s_add_i32 s100, s100, 1
	v_addc_co_u32_e32 v2, vcc, 0, v2, vcc
	v_cmp_gt_i64_e32 vcc, s[20:21], v[8:9]
	v_readlane_b32 s21, v9, s100
	s_sub_i32 s20, 63, s100
	s_add_i32 s100, s100, 1
	v_addc_co_u32_e32 v2, vcc, 0, v2, vcc
	v_cmp_gt_i64_e32 vcc, s[22:23], v[8:9]
	v_readlane_b32 s23, v9, s100
	s_sub_i32 s22, 63, s100
	s_add_i32 s100, s100, 1
	v_addc_co_u32_e32 v2, vcc, 0, v2, vcc
	v_cmp_gt_i64_e32 vcc, s[20:21], v[8:9]
	v_readlane_b32 s21, v9, s100
	s_sub_i32 s20, 63, s100
	s_add_i32 s100, s100, 1
	v_addc_co_u32_e32 v2, vcc, 0, v2, vcc
	v_cmp_gt_i64_e32 vcc, s[22:23], v[8:9]
	v_readlane_b32 s23, v9, s100
	s_sub_i32 s22, 63, s100
	s_add_i32 s100, s100, 1
	v_addc_co_u32_e32 v2, vcc, 0, v2, vcc
	v_cmp_gt_i64_e32 vcc, s[20:21], v[8:9]
	v_readlane_b32 s21, v9, s100
	s_sub_i32 s20, 63, s100
	s_nop 0
	v_addc_co_u32_e32 v2, vcc, 0, v2, vcc
	v_cmp_gt_i64_e32 vcc, s[22:23], v[8:9]
	v_readlane_b32 s23, v9, s101
	s_sub_i32 s22, 63, s101
	s_add_i32 s101, s101, 1
	v_addc_co_u32_e32 v2, vcc, 0, v2, vcc
	v_cmp_gt_i64_e32 vcc, s[20:21], v[8:9]
	v_readlane_b32 s21, v9, s101
	s_sub_i32 s20, 63, s101
	s_add_i32 s101, s101, 1
	v_addc_co_u32_e32 v2, vcc, 0, v2, vcc
	v_cmp_gt_i64_e32 vcc, s[22:23], v[8:9]
	v_readlane_b32 s23, v9, s101
	s_sub_i32 s22, 63, s101
	s_add_i32 s101, s101, 1
	v_addc_co_u32_e32 v2, vcc, 0, v2, vcc
	v_cmp_gt_i64_e32 vcc, s[20:21], v[8:9]
	v_readlane_b32 s21, v9, s101
	s_sub_i32 s20, 63, s101
	s_add_i32 s101, s101, 1
	v_addc_co_u32_e32 v2, vcc, 0, v2, vcc
	v_cmp_gt_i64_e32 vcc, s[22:23], v[8:9]
	v_readlane_b32 s23, v9, s101
	s_sub_i32 s22, 63, s101
	s_add_i32 s101, s101, 1
	v_addc_co_u32_e32 v2, vcc, 0, v2, vcc
	v_cmp_gt_i64_e32 vcc, s[20:21], v[8:9]
	v_readlane_b32 s21, v9, s101
	s_sub_i32 s20, 63, s101
	s_add_i32 s101, s101, 1
	v_addc_co_u32_e32 v2, vcc, 0, v2, vcc
	v_cmp_gt_i64_e32 vcc, s[22:23], v[8:9]
	v_readlane_b32 s23, v9, s101
	s_sub_i32 s22, 63, s101
	s_add_i32 s101, s101, 1
	v_addc_co_u32_e32 v2, vcc, 0, v2, vcc
	v_cmp_gt_i64_e32 vcc, s[20:21], v[8:9]
	v_readlane_b32 s21, v9, s101
	s_sub_i32 s20, 63, s101
	s_nop 0
	v_addc_co_u32_e32 v2, vcc, 0, v2, vcc
	v_cmp_gt_i64_e32 vcc, s[22:23], v[8:9]
	s_nop 1
	v_addc_co_u32_e32 v2, vcc, 0, v2, vcc
	v_cmp_gt_i64_e32 vcc, s[20:21], v[8:9]
	s_nop 1
	v_addc_co_u32_e32 v2, vcc, 0, v2, vcc
	v_cmp_gt_u32_e32 vcc, 6, v2
	s_nop 1
	v_cndmask_b32_e32 v6, 0, v5, vcc
	s_nop 1
	v_add_f32_dpp v6, v6, v6 quad_perm:[1,0,3,2] row_mask:0xf bank_mask:0xf
	s_nop 1
	v_add_f32_dpp v6, v6, v6 quad_perm:[2,3,0,1] row_mask:0xf bank_mask:0xf
	s_nop 1
	v_add_f32_dpp v6, v6, v6 row_half_mirror row_mask:0xf bank_mask:0xf
	s_nop 1
	v_add_f32_dpp v6, v6, v6 row_mirror row_mask:0xf bank_mask:0xf
	v_mov_b32_e32 v7, v6
	s_nop 1
	v_permlane16_swap_b32_e32 v7, v6
	s_waitcnt lgkmcnt(0)
	v_add_f32_e32 v6, v6, v7
	v_mov_b32_e32 v7, v6
	s_nop 1
	v_permlane32_swap_b32_e32 v7, v6
	s_and_saveexec_b64 s[20:21], vcc
	s_cbranch_execz .LBB0_1316
	s_waitcnt lgkmcnt(0)
	v_add_f32_e32 v10, v6, v7
	v_mad_u64_u32 v[6:7], s[22:23], s56, 6, v[2:3]
	v_div_scale_f32 v2, s[22:23], v10, v10, v5
	v_rcp_f32_e32 v12, v2
	v_ashrrev_i32_e32 v7, 31, v6
	v_lshlrev_b64 v[6:7], 2, v[6:7]
	v_lshl_add_u64 v[8:9], s[42:43], 0, v[6:7]
	ds_add_rtn_u32 v11, v227, v243
	global_store_dword v[8:9], v230, off
	v_fma_f32 v8, -v2, v12, 1.0
	v_fmac_f32_e32 v12, v8, v12
	v_div_scale_f32 v8, vcc, v5, v10, v5
	v_mul_f32_e32 v9, v8, v12
	v_fma_f32 v13, -v2, v9, v8
	v_fmac_f32_e32 v9, v13, v12
	v_fma_f32 v2, -v2, v9, v8
	v_div_fmas_f32 v2, v2, v12, v9
	v_div_fixup_f32 v2, v2, v10, v5
	v_mul_f32_e32 v2, 0x40200000, v2
	v_lshl_add_u64 v[8:9], s[44:45], 0, v[6:7]
	v_lshl_add_u64 v[6:7], s[46:47], 0, v[6:7]
	global_store_dword v[8:9], v2, off
	s_waitcnt lgkmcnt(0)
	global_store_dword v[6:7], v11, off
; __device__ __forceinline__ void phase_nrr(const Frame& F, const Args& a, int l, const bf16_t* XA, const float* g, const float* modl, unsigned char* XN8) {
;     ...
;         for (int i = 0; i < 8; ++i) { const int t = tb + i;
;             const float lg = Pl[(w * 8 + i) * NE + lane] + Pl[(64 + w * 8 + i) * NE + lane]; const float sc = 1.f / (1.f + __expf(-lg)); const float bb = sc + bias;
;             float m1 = bb; m1 = fmaxf(m1, __shfl_xor(m1, 1)); m1 = fmaxf(m1, __shfl_xor(m1, 2)); m1 = fmaxf(m1, __shfl_xor(m1, 4));
;             const unsigned long long eq = __ballot(bb == m1); const int gbase = lane & ~7; const unsigned grpmask = (unsigned)((eq >> gbase) & 0xffull);
;             const int first = gbase + __builtin_ctz(grpmask);
;             float m2 = (lane == first) ? -INFINITY : bb; m2 = fmaxf(m2, __shfl_xor(m2, 1)); m2 = fmaxf(m2, __shfl_xor(m2, 2)); m2 = fmaxf(m2, __shfl_xor(m2, 4));
;             const float gsum = m1 + m2; const int gq = lane >> 3;
;             int grank = 0;
; #pragma unroll
;             for (int g2 = 0; g2 < 8; ++g2) { const float v = __int_as_float(__builtin_amdgcn_readlane(__float_as_int(gsum), g2 * 8)); grank += (v > gsum || (v == gsum && g2 < gq)) ? 1 : 0; }
;             const bool keep = grank < 4; const float val = keep ? bb : -INFINITY;
;             int rank = 0;
; #pragma unroll 8
;             for (int e2 = 0; e2 < 64; ++e2) { const float v = __int_as_float(__builtin_amdgcn_readlane(__float_as_int(val), e2)); rank += (v > val || (v == val && e2 < lane)) ? 1 : 0; }
.LBB0_1316:
	s_or_b64 exec, exec, s[20:21]
	v_add_u32_e32 v2, s77, v226
	ds_read_b32 v2, v2
	ds_read_b32 v5, v4 offset:16896
	s_mov_b32 s3, 0
	s_waitcnt lgkmcnt(0)
	v_add_f32_e32 v2, v2, v5
	v_mul_f32_e32 v2, 0xbfb8aa3b, v2
	v_exp_f32_e32 v2, v2
	s_nop 0
	v_add_f32_e32 v2, 1.0, v2
	v_div_scale_f32 v5, s[20:21], v2, v2, 1.0
	v_rcp_f32_e32 v6, v5
	v_div_scale_f32 v7, vcc, 1.0, v2, 1.0
	v_fma_f32 v8, -v5, v6, 1.0
	v_fmac_f32_e32 v6, v8, v6
	v_mul_f32_e32 v8, v7, v6
	v_fma_f32 v9, -v5, v8, v7
	v_fmac_f32_e32 v8, v9, v6
	v_fma_f32 v5, -v5, v8, v7
	v_div_fmas_f32 v5, v5, v6, v8
	v_div_fixup_f32 v5, v5, v2, 1.0
	v_add_f32_e32 v2, v3, v5
	s_nop 1
	s_waitcnt lgkmcnt(0)
	v_max_f32_dpp v6, v2, v2 quad_perm:[1,0,3,2] row_mask:0xf bank_mask:0xf
	s_nop 1
	s_waitcnt lgkmcnt(0)
	v_max_f32_dpp v6, v6, v6 quad_perm:[2,3,0,1] row_mask:0xf bank_mask:0xf
	s_nop 1
	s_waitcnt lgkmcnt(0)
	v_max_f32_dpp v8, v6, v6 row_half_mirror row_mask:0xf bank_mask:0xf
	v_cmp_eq_f32_e32 vcc, v2, v8
	s_nop 1
	v_lshrrev_b64 v[6:7], v200, vcc
	v_ffbl_b32_sdwa v6, v6 dst_sel:DWORD dst_unused:UNUSED_PAD src0_sel:BYTE_0
	v_add_u32_e32 v6, v6, v200
	v_cmp_ne_u32_e32 vcc, v230, v6
	s_nop 1
	v_cndmask_b32_e32 v6, v245, v2, vcc
	s_nop 1
	s_waitcnt lgkmcnt(0)
	v_max_f32_dpp v6, v6, v6 quad_perm:[1,0,3,2] row_mask:0xf bank_mask:0xf
	s_nop 1
	s_waitcnt lgkmcnt(0)
	v_max_f32_dpp v6, v6, v6 quad_perm:[2,3,0,1] row_mask:0xf bank_mask:0xf
	s_nop 1
	s_waitcnt lgkmcnt(0)
	v_max_f32_dpp v6, v6, v6 row_half_mirror row_mask:0xf bank_mask:0xf
	v_add_f32_e32 v6, v8, v6
	s_nop 0
	v_readlane_b32 s5, v6, 0
	v_readlane_b32 s24, v6, 8
	v_readlane_b32 s28, v6, 16
	v_cmp_eq_f32_e64 s[20:21], s5, v6
	v_cmp_gt_f32_e32 vcc, s5, v6
	v_cmp_gt_f32_e64 s[22:23], s24, v6
	v_cmp_eq_f32_e64 s[24:25], s24, v6
	s_and_b64 s[20:21], s[0:1], s[20:21]
	v_readlane_b32 s34, v6, 24
	v_cmp_gt_f32_e64 s[26:27], s28, v6
	v_cmp_eq_f32_e64 s[28:29], s28, v6
	s_and_b64 s[24:25], s[6:7], s[24:25]
	s_or_b64 s[20:21], vcc, s[20:21]
	v_readlane_b32 s40, v6, 32
	v_cmp_gt_f32_e64 s[30:31], s34, v6
	v_cmp_eq_f32_e64 s[34:35], s34, v6
	s_and_b64 s[28:29], s[8:9], s[28:29]
	v_cndmask_b32_e64 v7, 0, 1, s[20:21]
	s_or_b64 s[20:21], s[22:23], s[24:25]
	v_cmp_gt_f32_e64 s[36:37], s40, v6
	v_cmp_eq_f32_e64 s[40:41], s40, v6
	s_and_b64 s[34:35], s[10:11], s[34:35]
	v_cndmask_b32_e64 v8, 0, 1, s[20:21]
	s_or_b64 s[20:21], s[26:27], s[28:29]
	s_and_b64 s[40:41], s[12:13], s[40:41]
	v_cndmask_b32_e64 v9, 0, 1, s[20:21]
	s_or_b64 s[20:21], s[30:31], s[34:35]
	v_readlane_b32 s55, v6, 40
	v_cndmask_b32_e64 v10, 0, 1, s[20:21]
	s_or_b64 s[20:21], s[36:37], s[40:41]
	v_cndmask_b32_e64 v11, 0, 1, s[20:21]
	v_cmp_eq_f32_e64 s[20:21], s55, v6
	v_cmp_gt_f32_e32 vcc, s55, v6
	s_and_b64 s[20:21], s[14:15], s[20:21]
	s_or_b64 s[20:21], vcc, s[20:21]
	v_readlane_b32 s5, v6, 48
	v_cndmask_b32_e64 v12, 0, 1, s[20:21]
	s_nop 0
	v_cmp_eq_f32_e64 s[20:21], s5, v6
	v_cmp_gt_f32_e32 vcc, s5, v6
	s_and_b64 s[20:21], s[16:17], s[20:21]
	v_readlane_b32 s5, v6, 56
	s_or_b64 s[20:21], vcc, s[20:21]
	v_cndmask_b32_e64 v13, 0, 1, s[20:21]
	v_cmp_gt_f32_e32 vcc, s5, v6
	s_nop 1
	v_cndmask_b32_e64 v6, 0, 1, vcc
	v_add_u32_e32 v6, v8, v6
	v_add3_u32 v6, v6, v7, v9
	v_add3_u32 v6, v6, v10, v11
	v_add3_u32 v6, v6, v12, v13
	v_cmp_eq_u32_e32 vcc, 0, v6
	s_ff1_i32_b64 s98, vcc
	v_cmp_eq_u32_e32 vcc, 1, v6
	s_ff1_i32_b64 s99, vcc
	v_cmp_eq_u32_e32 vcc, 2, v6
	s_ff1_i32_b64 s100, vcc
	v_cmp_eq_u32_e32 vcc, 3, v6
	s_ff1_i32_b64 s101, vcc
	v_cmp_gt_u32_e32 vcc, 4, v6
	s_nop 1
	v_cndmask_b32_e32 v6, v245, v2, vcc
	v_mov_b32_e32 v2, 0
	v_ashrrev_i32_e32 v9, 31, v6
	v_sub_u32_e32 v8, 63, v230
	v_and_b32_e32 v9, 0x7fffffff, v9
	v_xor_b32_e32 v9, v6, v9
	s_nop 0
	v_readlane_b32 s23, v9, s98
	s_sub_i32 s22, 63, s98
	s_add_i32 s98, s98, 1
	v_readlane_b32 s21, v9, s98
	s_sub_i32 s20, 63, s98
	s_add_i32 s98, s98, 1
	v_cmp_gt_i64_e32 vcc, s[22:23], v[8:9]
	v_readlane_b32 s23, v9, s98
	s_sub_i32 s22, 63, s98
	s_add_i32 s98, s98, 1
	v_addc_co_u32_e32 v2, vcc, 0, v2, vcc
	v_cmp_gt_i64_e32 vcc, s[20:21], v[8:9]
	v_readlane_b32 s21, v9, s98
	s_sub_i32 s20, 63, s98
	s_add_i32 s98, s98, 1
	v_addc_co_u32_e32 v2, vcc, 0, v2, vcc
	v_cmp_gt_i64_e32 vcc, s[22:23], v[8:9]
	v_readlane_b32 s23, v9, s98
	s_sub_i32 s22, 63, s98
	s_add_i32 s98, s98, 1
	v_addc_co_u32_e32 v2, vcc, 0, v2, vcc
	v_cmp_gt_i64_e32 vcc, s[20:21], v[8:9]
	v_readlane_b32 s21, v9, s98
	s_sub_i32 s20, 63, s98
	s_add_i32 s98, s98, 1
	v_addc_co_u32_e32 v2, vcc, 0, v2, vcc
	v_cmp_gt_i64_e32 vcc, s[22:23], v[8:9]
	v_readlane_b32 s23, v9, s98
	s_sub_i32 s22, 63, s98
	s_add_i32 s98, s98, 1
	v_addc_co_u32_e32 v2, vcc, 0, v2, vcc
	v_cmp_gt_i64_e32 vcc, s[20:21], v[8:9]
	v_readlane_b32 s21, v9, s98
	s_sub_i32 s20, 63, s98
	s_nop 0
	v_addc_co_u32_e32 v2, vcc, 0, v2, vcc
	v_cmp_gt_i64_e32 vcc, s[22:23], v[8:9]
	v_readlane_b32 s23, v9, s99
	s_sub_i32 s22, 63, s99
	s_add_i32 s99, s99, 1
	v_addc_co_u32_e32 v2, vcc, 0, v2, vcc
	v_cmp_gt_i64_e32 vcc, s[20:21], v[8:9]
	v_readlane_b32 s21, v9, s99
	s_sub_i32 s20, 63, s99
	s_add_i32 s99, s99, 1
	v_addc_co_u32_e32 v2, vcc, 0, v2, vcc
	v_cmp_gt_i64_e32 vcc, s[22:23], v[8:9]
	v_readlane_b32 s23, v9, s99
	s_sub_i32 s22, 63, s99
	s_add_i32 s99, s99, 1
	v_addc_co_u32_e32 v2, vcc, 0, v2, vcc
	v_cmp_gt_i64_e32 vcc, s[20:21], v[8:9]
	v_readlane_b32 s21, v9, s99
	s_sub_i32 s20, 63, s99
	s_add_i32 s99, s99, 1
	v_addc_co_u32_e32 v2, vcc, 0, v2, vcc
	v_cmp_gt_i64_e32 vcc, s[22:23], v[8:9]
	v_readlane_b32 s23, v9, s99
	s_sub_i32 s22, 63, s99
	s_add_i32 s99, s99, 1
	v_addc_co_u32_e32 v2, vcc, 0, v2, vcc
	v_cmp_gt_i64_e32 vcc, s[20:21], v[8:9]
	v_readlane_b32 s21, v9, s99
	s_sub_i32 s20, 63, s99
	s_add_i32 s99, s99, 1
; __device__ __forceinline__ float wave_sum(float v) {
; #pragma unroll
;     for (int o = 1; o < 64; o <<= 1) v += __shfl_xor(v, o);
;     return v;
; __device__ __forceinline__ void phase_nrr(const Frame& F, const Args& a, int l, const bf16_t* XA, const float* g, const float* modl, unsigned char* XN8) {
;     ...
;             for (int e2 = 0; e2 < 64; ++e2) { const float v = __int_as_float(__builtin_amdgcn_readlane(__float_as_int(val), e2)); rank += (v > val || (v == val && e2 < lane)) ? 1 : 0; }
;             const bool sel = rank < TOPK;
;             const float ssum = wave_sum(sel ? sc : 0.f);
;             if (sel) { const int p = atomicAdd((int*)(hist + lane), 1); top_e[t * TOPK + rank] = lane; gate[t * TOPK + rank] = sc / ssum * 2.5f; lpos[t * TOPK + rank] = p; }
	v_addc_co_u32_e32 v2, vcc, 0, v2, vcc
	v_cmp_gt_i64_e32 vcc, s[22:23], v[8:9]
	v_readlane_b32 s23, v9, s99
	s_sub_i32 s22, 63, s99
	s_add_i32 s99, s99, 1
	v_addc_co_u32_e32 v2, vcc, 0, v2, vcc
	v_cmp_gt_i64_e32 vcc, s[20:21], v[8:9]
	v_readlane_b32 s21, v9, s99
	s_sub_i32 s20, 63, s99
	s_nop 0
	v_addc_co_u32_e32 v2, vcc, 0, v2, vcc
	v_cmp_gt_i64_e32 vcc, s[22:23], v[8:9]
	v_readlane_b32 s23, v9, s100
	s_sub_i32 s22, 63, s100
	s_add_i32 s100, s100, 1
	v_addc_co_u32_e32 v2, vcc, 0, v2, vcc
	v_cmp_gt_i64_e32 vcc, s[20:21], v[8:9]
	v_readlane_b32 s21, v9, s100
	s_sub_i32 s20, 63, s100
	s_add_i32 s100, s100, 1
	v_addc_co_u32_e32 v2, vcc, 0, v2, vcc
	v_cmp_gt_i64_e32 vcc, s[22:23], v[8:9]
	v_readlane_b32 s23, v9, s100
	s_sub_i32 s22, 63, s100
	s_add_i32 s100, s100, 1
	v_addc_co_u32_e32 v2, vcc, 0, v2, vcc
	v_cmp_gt_i64_e32 vcc, s[20:21], v[8:9]
	v_readlane_b32 s21, v9, s100
	s_sub_i32 s20, 63, s100
	s_add_i32 s100, s100, 1
	v_addc_co_u32_e32 v2, vcc, 0, v2, vcc
	v_cmp_gt_i64_e32 vcc, s[22:23], v[8:9]
	v_readlane_b32 s23, v9, s100
	s_sub_i32 s22, 63, s100
	s_add_i32 s100, s100, 1
	v_addc_co_u32_e32 v2, vcc, 0, v2, vcc
	v_cmp_gt_i64_e32 vcc, s[20:21], v[8:9]
	v_readlane_b32 s21, v9, s100
	s_sub_i32 s20, 63, s100
	s_add_i32 s100, s100, 1
	v_addc_co_u32_e32 v2, vcc, 0, v2, vcc
	v_cmp_gt_i64_e32 vcc, s[22:23], v[8:9]
	v_readlane_b32 s23, v9, s100
	s_sub_i32 s22, 63, s100
	s_add_i32 s100, s100, 1
	v_addc_co_u32_e32 v2, vcc, 0, v2, vcc
	v_cmp_gt_i64_e32 vcc, s[20:21], v[8:9]
	v_readlane_b32 s21, v9, s100
	s_sub_i32 s20, 63, s100
	s_nop 0
	v_addc_co_u32_e32 v2, vcc, 0, v2, vcc
	v_cmp_gt_i64_e32 vcc, s[22:23], v[8:9]
	v_readlane_b32 s23, v9, s101
	s_sub_i32 s22, 63, s101
	s_add_i32 s101, s101, 1
	v_addc_co_u32_e32 v2, vcc, 0, v2, vcc
	v_cmp_gt_i64_e32 vcc, s[20:21], v[8:9]
	v_readlane_b32 s21, v9, s101
	s_sub_i32 s20, 63, s101
	s_add_i32 s101, s101, 1
	v_addc_co_u32_e32 v2, vcc, 0, v2, vcc
	v_cmp_gt_i64_e32 vcc, s[22:23], v[8:9]
	v_readlane_b32 s23, v9, s101
	s_sub_i32 s22, 63, s101
	s_add_i32 s101, s101, 1
	v_addc_co_u32_e32 v2, vcc, 0, v2, vcc
	v_cmp_gt_i64_e32 vcc, s[20:21], v[8:9]
	v_readlane_b32 s21, v9, s101
	s_sub_i32 s20, 63, s101
	s_add_i32 s101, s101, 1
	v_addc_co_u32_e32 v2, vcc, 0, v2, vcc
	v_cmp_gt_i64_e32 vcc, s[22:23], v[8:9]
	v_readlane_b32 s23, v9, s101
	s_sub_i32 s22, 63, s101
	s_add_i32 s101, s101, 1
	v_addc_co_u32_e32 v2, vcc, 0, v2, vcc
	v_cmp_gt_i64_e32 vcc, s[20:21], v[8:9]
	v_readlane_b32 s21, v9, s101
	s_sub_i32 s20, 63, s101
	s_add_i32 s101, s101, 1
	v_addc_co_u32_e32 v2, vcc, 0, v2, vcc
	v_cmp_gt_i64_e32 vcc, s[22:23], v[8:9]
	v_readlane_b32 s23, v9, s101
	s_sub_i32 s22, 63, s101
	s_add_i32 s101, s101, 1
	v_addc_co_u32_e32 v2, vcc, 0, v2, vcc
	v_cmp_gt_i64_e32 vcc, s[20:21], v[8:9]
	v_readlane_b32 s21, v9, s101
	s_sub_i32 s20, 63, s101
	s_nop 0
	v_addc_co_u32_e32 v2, vcc, 0, v2, vcc
	v_cmp_gt_i64_e32 vcc, s[22:23], v[8:9]
	s_nop 1
	v_addc_co_u32_e32 v2, vcc, 0, v2, vcc
	v_cmp_gt_i64_e32 vcc, s[20:21], v[8:9]
	s_nop 1
	v_addc_co_u32_e32 v2, vcc, 0, v2, vcc
	v_cmp_gt_u32_e32 vcc, 6, v2
	s_nop 1
	v_cndmask_b32_e32 v6, 0, v5, vcc
	s_nop 1
	v_add_f32_dpp v6, v6, v6 quad_perm:[1,0,3,2] row_mask:0xf bank_mask:0xf
	s_nop 1
	v_add_f32_dpp v6, v6, v6 quad_perm:[2,3,0,1] row_mask:0xf bank_mask:0xf
	s_nop 1
	v_add_f32_dpp v6, v6, v6 row_half_mirror row_mask:0xf bank_mask:0xf
	s_nop 1
	v_add_f32_dpp v6, v6, v6 row_mirror row_mask:0xf bank_mask:0xf
	v_mov_b32_e32 v7, v6
	s_nop 1
	v_permlane16_swap_b32_e32 v7, v6
	s_waitcnt lgkmcnt(0)
	v_add_f32_e32 v6, v6, v7
	v_mov_b32_e32 v7, v6
	s_nop 1
	v_permlane32_swap_b32_e32 v7, v6
	s_and_saveexec_b64 s[20:21], vcc
	s_cbranch_execz .LBB0_1320
	s_waitcnt lgkmcnt(0)
	v_add_f32_e32 v10, v6, v7
	v_mad_u64_u32 v[6:7], s[22:23], s54, 6, v[2:3]
	v_div_scale_f32 v2, s[22:23], v10, v10, v5
	v_rcp_f32_e32 v12, v2
	v_ashrrev_i32_e32 v7, 31, v6
	v_lshlrev_b64 v[6:7], 2, v[6:7]
	v_lshl_add_u64 v[8:9], s[42:43], 0, v[6:7]
	ds_add_rtn_u32 v11, v227, v243
	global_store_dword v[8:9], v230, off
	v_fma_f32 v8, -v2, v12, 1.0
	v_fmac_f32_e32 v12, v8, v12
	v_div_scale_f32 v8, vcc, v5, v10, v5
	v_mul_f32_e32 v9, v8, v12
	v_fma_f32 v13, -v2, v9, v8
	v_fmac_f32_e32 v9, v13, v12
	v_fma_f32 v2, -v2, v9, v8
	v_div_fmas_f32 v2, v2, v12, v9
	v_div_fixup_f32 v2, v2, v10, v5
	v_mul_f32_e32 v2, 0x40200000, v2
	v_lshl_add_u64 v[8:9], s[44:45], 0, v[6:7]
	v_lshl_add_u64 v[6:7], s[46:47], 0, v[6:7]
	global_store_dword v[8:9], v2, off
	s_waitcnt lgkmcnt(0)
	global_store_dword v[6:7], v11, off
; __device__ __forceinline__ void phase_nrr(const Frame& F, const Args& a, int l, const bf16_t* XA, const float* g, const float* modl, unsigned char* XN8) {
;     ...
;         for (int i = 0; i < 8; ++i) { const int t = tb + i;
;             const float lg = Pl[(w * 8 + i) * NE + lane] + Pl[(64 + w * 8 + i) * NE + lane]; const float sc = 1.f / (1.f + __expf(-lg)); const float bb = sc + bias;
;             float m1 = bb; m1 = fmaxf(m1, __shfl_xor(m1, 1)); m1 = fmaxf(m1, __shfl_xor(m1, 2)); m1 = fmaxf(m1, __shfl_xor(m1, 4));
;             const unsigned long long eq = __ballot(bb == m1); const int gbase = lane & ~7; const unsigned grpmask = (unsigned)((eq >> gbase) & 0xffull);
;             const int first = gbase + __builtin_ctz(grpmask);
;             float m2 = (lane == first) ? -INFINITY : bb; m2 = fmaxf(m2, __shfl_xor(m2, 1)); m2 = fmaxf(m2, __shfl_xor(m2, 2)); m2 = fmaxf(m2, __shfl_xor(m2, 4));
;             const float gsum = m1 + m2; const int gq = lane >> 3;
;             int grank = 0;
; #pragma unroll
;             for (int g2 = 0; g2 < 8; ++g2) { const float v = __int_as_float(__builtin_amdgcn_readlane(__float_as_int(gsum), g2 * 8)); grank += (v > gsum || (v == gsum && g2 < gq)) ? 1 : 0; }
;             const bool keep = grank < 4; const float val = keep ? bb : -INFINITY;
;             int rank = 0;
; #pragma unroll 8
;             for (int e2 = 0; e2 < 64; ++e2) { const float v = __int_as_float(__builtin_amdgcn_readlane(__float_as_int(val), e2)); rank += (v > val || (v == val && e2 < lane)) ? 1 : 0; }
.LBB0_1320:
	s_or_b64 exec, exec, s[20:21]
	v_add_u32_e32 v2, s78, v226
	ds_read_b32 v2, v2
	ds_read_b32 v5, v4 offset:17152
	s_mov_b32 s3, 0
	s_waitcnt lgkmcnt(0)
	v_add_f32_e32 v2, v2, v5
	v_mul_f32_e32 v2, 0xbfb8aa3b, v2
	v_exp_f32_e32 v2, v2
	s_nop 0
	v_add_f32_e32 v2, 1.0, v2
	v_div_scale_f32 v5, s[20:21], v2, v2, 1.0
	v_rcp_f32_e32 v6, v5
	v_div_scale_f32 v7, vcc, 1.0, v2, 1.0
	v_fma_f32 v8, -v5, v6, 1.0
	v_fmac_f32_e32 v6, v8, v6
	v_mul_f32_e32 v8, v7, v6
	v_fma_f32 v9, -v5, v8, v7
	v_fmac_f32_e32 v8, v9, v6
	v_fma_f32 v5, -v5, v8, v7
	v_div_fmas_f32 v5, v5, v6, v8
	v_div_fixup_f32 v5, v5, v2, 1.0
	v_add_f32_e32 v2, v3, v5
	s_nop 1
	s_waitcnt lgkmcnt(0)
	v_max_f32_dpp v6, v2, v2 quad_perm:[1,0,3,2] row_mask:0xf bank_mask:0xf
	s_nop 1
	s_waitcnt lgkmcnt(0)
	v_max_f32_dpp v6, v6, v6 quad_perm:[2,3,0,1] row_mask:0xf bank_mask:0xf
	s_nop 1
	s_waitcnt lgkmcnt(0)
	v_max_f32_dpp v8, v6, v6 row_half_mirror row_mask:0xf bank_mask:0xf
	v_cmp_eq_f32_e32 vcc, v2, v8
	s_nop 1
	v_lshrrev_b64 v[6:7], v200, vcc
	v_ffbl_b32_sdwa v6, v6 dst_sel:DWORD dst_unused:UNUSED_PAD src0_sel:BYTE_0
	v_add_u32_e32 v6, v6, v200
	v_cmp_ne_u32_e32 vcc, v230, v6
	s_nop 1
	v_cndmask_b32_e32 v6, v245, v2, vcc
	s_nop 1
	s_waitcnt lgkmcnt(0)
	v_max_f32_dpp v6, v6, v6 quad_perm:[1,0,3,2] row_mask:0xf bank_mask:0xf
	s_nop 1
	s_waitcnt lgkmcnt(0)
	v_max_f32_dpp v6, v6, v6 quad_perm:[2,3,0,1] row_mask:0xf bank_mask:0xf
	s_nop 1
	s_waitcnt lgkmcnt(0)
	v_max_f32_dpp v6, v6, v6 row_half_mirror row_mask:0xf bank_mask:0xf
	v_add_f32_e32 v6, v8, v6
	s_nop 0
	v_readlane_b32 s5, v6, 0
	v_readlane_b32 s24, v6, 8
	v_readlane_b32 s28, v6, 16
	v_cmp_eq_f32_e64 s[20:21], s5, v6
	v_cmp_gt_f32_e32 vcc, s5, v6
	v_cmp_gt_f32_e64 s[22:23], s24, v6
	v_cmp_eq_f32_e64 s[24:25], s24, v6
	s_and_b64 s[20:21], s[0:1], s[20:21]
	v_readlane_b32 s34, v6, 24
	v_cmp_gt_f32_e64 s[26:27], s28, v6
	v_cmp_eq_f32_e64 s[28:29], s28, v6
	s_and_b64 s[24:25], s[6:7], s[24:25]
	s_or_b64 s[20:21], vcc, s[20:21]
	v_readlane_b32 s40, v6, 32
	v_cmp_gt_f32_e64 s[30:31], s34, v6
	v_cmp_eq_f32_e64 s[34:35], s34, v6
	s_and_b64 s[28:29], s[8:9], s[28:29]
	v_cndmask_b32_e64 v7, 0, 1, s[20:21]
	s_or_b64 s[20:21], s[22:23], s[24:25]
	v_cmp_gt_f32_e64 s[36:37], s40, v6
	v_cmp_eq_f32_e64 s[40:41], s40, v6
	s_and_b64 s[34:35], s[10:11], s[34:35]
	v_cndmask_b32_e64 v8, 0, 1, s[20:21]
	s_or_b64 s[20:21], s[26:27], s[28:29]
	s_and_b64 s[40:41], s[12:13], s[40:41]
	v_cndmask_b32_e64 v9, 0, 1, s[20:21]
	s_or_b64 s[20:21], s[30:31], s[34:35]
	v_readlane_b32 s54, v6, 40
	v_cndmask_b32_e64 v10, 0, 1, s[20:21]
	s_or_b64 s[20:21], s[36:37], s[40:41]
	v_cndmask_b32_e64 v11, 0, 1, s[20:21]
	v_cmp_eq_f32_e64 s[20:21], s54, v6
	v_cmp_gt_f32_e32 vcc, s54, v6
	s_and_b64 s[20:21], s[14:15], s[20:21]
	s_or_b64 s[20:21], vcc, s[20:21]
	v_readlane_b32 s5, v6, 48
	v_cndmask_b32_e64 v12, 0, 1, s[20:21]
	s_nop 0
	v_cmp_eq_f32_e64 s[20:21], s5, v6
	v_cmp_gt_f32_e32 vcc, s5, v6
	s_and_b64 s[20:21], s[16:17], s[20:21]
	v_readlane_b32 s5, v6, 56
	s_or_b64 s[20:21], vcc, s[20:21]
	v_cndmask_b32_e64 v13, 0, 1, s[20:21]
	v_cmp_gt_f32_e32 vcc, s5, v6
	s_nop 1
	v_cndmask_b32_e64 v6, 0, 1, vcc
	v_add_u32_e32 v6, v8, v6
	v_add3_u32 v6, v6, v7, v9
	v_add3_u32 v6, v6, v10, v11
	v_add3_u32 v6, v6, v12, v13
	v_cmp_eq_u32_e32 vcc, 0, v6
	s_ff1_i32_b64 s98, vcc
	v_cmp_eq_u32_e32 vcc, 1, v6
	s_ff1_i32_b64 s99, vcc
	v_cmp_eq_u32_e32 vcc, 2, v6
	s_ff1_i32_b64 s100, vcc
	v_cmp_eq_u32_e32 vcc, 3, v6
	s_ff1_i32_b64 s101, vcc
	v_cmp_gt_u32_e32 vcc, 4, v6
	s_nop 1
	v_cndmask_b32_e32 v6, v245, v2, vcc
	v_mov_b32_e32 v2, 0
	v_ashrrev_i32_e32 v9, 31, v6
	v_sub_u32_e32 v8, 63, v230
	v_and_b32_e32 v9, 0x7fffffff, v9
	v_xor_b32_e32 v9, v6, v9
	s_nop 0
	v_readlane_b32 s23, v9, s98
	s_sub_i32 s22, 63, s98
	s_add_i32 s98, s98, 1
	v_readlane_b32 s21, v9, s98
	s_sub_i32 s20, 63, s98
	s_add_i32 s98, s98, 1
	v_cmp_gt_i64_e32 vcc, s[22:23], v[8:9]
	v_readlane_b32 s23, v9, s98
	s_sub_i32 s22, 63, s98
	s_add_i32 s98, s98, 1
	v_addc_co_u32_e32 v2, vcc, 0, v2, vcc
	v_cmp_gt_i64_e32 vcc, s[20:21], v[8:9]
	v_readlane_b32 s21, v9, s98
	s_sub_i32 s20, 63, s98
	s_add_i32 s98, s98, 1
	v_addc_co_u32_e32 v2, vcc, 0, v2, vcc
	v_cmp_gt_i64_e32 vcc, s[22:23], v[8:9]
	v_readlane_b32 s23, v9, s98
	s_sub_i32 s22, 63, s98
	s_add_i32 s98, s98, 1
	v_addc_co_u32_e32 v2, vcc, 0, v2, vcc
	v_cmp_gt_i64_e32 vcc, s[20:21], v[8:9]
	v_readlane_b32 s21, v9, s98
	s_sub_i32 s20, 63, s98
	s_add_i32 s98, s98, 1
	v_addc_co_u32_e32 v2, vcc, 0, v2, vcc
	v_cmp_gt_i64_e32 vcc, s[22:23], v[8:9]
	v_readlane_b32 s23, v9, s98
	s_sub_i32 s22, 63, s98
	s_add_i32 s98, s98, 1
	v_addc_co_u32_e32 v2, vcc, 0, v2, vcc
	v_cmp_gt_i64_e32 vcc, s[20:21], v[8:9]
	v_readlane_b32 s21, v9, s98
	s_sub_i32 s20, 63, s98
	s_nop 0
	v_addc_co_u32_e32 v2, vcc, 0, v2, vcc
	v_cmp_gt_i64_e32 vcc, s[22:23], v[8:9]
	v_readlane_b32 s23, v9, s99
	s_sub_i32 s22, 63, s99
	s_add_i32 s99, s99, 1
	v_addc_co_u32_e32 v2, vcc, 0, v2, vcc
	v_cmp_gt_i64_e32 vcc, s[20:21], v[8:9]
	v_readlane_b32 s21, v9, s99
	s_sub_i32 s20, 63, s99
	s_add_i32 s99, s99, 1
	v_addc_co_u32_e32 v2, vcc, 0, v2, vcc
	v_cmp_gt_i64_e32 vcc, s[22:23], v[8:9]
	v_readlane_b32 s23, v9, s99
	s_sub_i32 s22, 63, s99
	s_add_i32 s99, s99, 1
	v_addc_co_u32_e32 v2, vcc, 0, v2, vcc
	v_cmp_gt_i64_e32 vcc, s[20:21], v[8:9]
	v_readlane_b32 s21, v9, s99
	s_sub_i32 s20, 63, s99
	s_add_i32 s99, s99, 1
	v_addc_co_u32_e32 v2, vcc, 0, v2, vcc
	v_cmp_gt_i64_e32 vcc, s[22:23], v[8:9]
	v_readlane_b32 s23, v9, s99
	s_sub_i32 s22, 63, s99
	s_add_i32 s99, s99, 1
	v_addc_co_u32_e32 v2, vcc, 0, v2, vcc
	v_cmp_gt_i64_e32 vcc, s[20:21], v[8:9]
	v_readlane_b32 s21, v9, s99
	s_sub_i32 s20, 63, s99
	s_add_i32 s99, s99, 1
; __device__ __forceinline__ float wave_sum(float v) {
; #pragma unroll
;     for (int o = 1; o < 64; o <<= 1) v += __shfl_xor(v, o);
;     return v;
; __device__ __forceinline__ void phase_nrr(const Frame& F, const Args& a, int l, const bf16_t* XA, const float* g, const float* modl, unsigned char* XN8) {
;     ...
;             for (int e2 = 0; e2 < 64; ++e2) { const float v = __int_as_float(__builtin_amdgcn_readlane(__float_as_int(val), e2)); rank += (v > val || (v == val && e2 < lane)) ? 1 : 0; }
;             const bool sel = rank < TOPK;
;             const float ssum = wave_sum(sel ? sc : 0.f);
;             if (sel) { const int p = atomicAdd((int*)(hist + lane), 1); top_e[t * TOPK + rank] = lane; gate[t * TOPK + rank] = sc / ssum * 2.5f; lpos[t * TOPK + rank] = p; }
	v_addc_co_u32_e32 v2, vcc, 0, v2, vcc
	v_cmp_gt_i64_e32 vcc, s[22:23], v[8:9]
	v_readlane_b32 s23, v9, s99
	s_sub_i32 s22, 63, s99
	s_add_i32 s99, s99, 1
	v_addc_co_u32_e32 v2, vcc, 0, v2, vcc
	v_cmp_gt_i64_e32 vcc, s[20:21], v[8:9]
	v_readlane_b32 s21, v9, s99
	s_sub_i32 s20, 63, s99
	s_nop 0
	v_addc_co_u32_e32 v2, vcc, 0, v2, vcc
	v_cmp_gt_i64_e32 vcc, s[22:23], v[8:9]
	v_readlane_b32 s23, v9, s100
	s_sub_i32 s22, 63, s100
	s_add_i32 s100, s100, 1
	v_addc_co_u32_e32 v2, vcc, 0, v2, vcc
	v_cmp_gt_i64_e32 vcc, s[20:21], v[8:9]
	v_readlane_b32 s21, v9, s100
	s_sub_i32 s20, 63, s100
	s_add_i32 s100, s100, 1
	v_addc_co_u32_e32 v2, vcc, 0, v2, vcc
	v_cmp_gt_i64_e32 vcc, s[22:23], v[8:9]
	v_readlane_b32 s23, v9, s100
	s_sub_i32 s22, 63, s100
	s_add_i32 s100, s100, 1
	v_addc_co_u32_e32 v2, vcc, 0, v2, vcc
	v_cmp_gt_i64_e32 vcc, s[20:21], v[8:9]
	v_readlane_b32 s21, v9, s100
	s_sub_i32 s20, 63, s100
	s_add_i32 s100, s100, 1
	v_addc_co_u32_e32 v2, vcc, 0, v2, vcc
	v_cmp_gt_i64_e32 vcc, s[22:23], v[8:9]
	v_readlane_b32 s23, v9, s100
	s_sub_i32 s22, 63, s100
	s_add_i32 s100, s100, 1
	v_addc_co_u32_e32 v2, vcc, 0, v2, vcc
	v_cmp_gt_i64_e32 vcc, s[20:21], v[8:9]
	v_readlane_b32 s21, v9, s100
	s_sub_i32 s20, 63, s100
	s_add_i32 s100, s100, 1
	v_addc_co_u32_e32 v2, vcc, 0, v2, vcc
	v_cmp_gt_i64_e32 vcc, s[22:23], v[8:9]
	v_readlane_b32 s23, v9, s100
	s_sub_i32 s22, 63, s100
	s_add_i32 s100, s100, 1
	v_addc_co_u32_e32 v2, vcc, 0, v2, vcc
	v_cmp_gt_i64_e32 vcc, s[20:21], v[8:9]
	v_readlane_b32 s21, v9, s100
	s_sub_i32 s20, 63, s100
	s_nop 0
	v_addc_co_u32_e32 v2, vcc, 0, v2, vcc
	v_cmp_gt_i64_e32 vcc, s[22:23], v[8:9]
	v_readlane_b32 s23, v9, s101
	s_sub_i32 s22, 63, s101
	s_add_i32 s101, s101, 1
	v_addc_co_u32_e32 v2, vcc, 0, v2, vcc
	v_cmp_gt_i64_e32 vcc, s[20:21], v[8:9]
	v_readlane_b32 s21, v9, s101
	s_sub_i32 s20, 63, s101
	s_add_i32 s101, s101, 1
	v_addc_co_u32_e32 v2, vcc, 0, v2, vcc
	v_cmp_gt_i64_e32 vcc, s[22:23], v[8:9]
	v_readlane_b32 s23, v9, s101
	s_sub_i32 s22, 63, s101
	s_add_i32 s101, s101, 1
	v_addc_co_u32_e32 v2, vcc, 0, v2, vcc
	v_cmp_gt_i64_e32 vcc, s[20:21], v[8:9]
	v_readlane_b32 s21, v9, s101
	s_sub_i32 s20, 63, s101
	s_add_i32 s101, s101, 1
	v_addc_co_u32_e32 v2, vcc, 0, v2, vcc
	v_cmp_gt_i64_e32 vcc, s[22:23], v[8:9]
	v_readlane_b32 s23, v9, s101
	s_sub_i32 s22, 63, s101
	s_add_i32 s101, s101, 1
	v_addc_co_u32_e32 v2, vcc, 0, v2, vcc
	v_cmp_gt_i64_e32 vcc, s[20:21], v[8:9]
	v_readlane_b32 s21, v9, s101
	s_sub_i32 s20, 63, s101
	s_add_i32 s101, s101, 1
	v_addc_co_u32_e32 v2, vcc, 0, v2, vcc
	v_cmp_gt_i64_e32 vcc, s[22:23], v[8:9]
	v_readlane_b32 s23, v9, s101
	s_sub_i32 s22, 63, s101
	s_add_i32 s101, s101, 1
	v_addc_co_u32_e32 v2, vcc, 0, v2, vcc
	v_cmp_gt_i64_e32 vcc, s[20:21], v[8:9]
	v_readlane_b32 s21, v9, s101
	s_sub_i32 s20, 63, s101
	s_nop 0
	v_addc_co_u32_e32 v2, vcc, 0, v2, vcc
	v_cmp_gt_i64_e32 vcc, s[22:23], v[8:9]
	s_nop 1
	v_addc_co_u32_e32 v2, vcc, 0, v2, vcc
	v_cmp_gt_i64_e32 vcc, s[20:21], v[8:9]
	s_nop 1
	v_addc_co_u32_e32 v2, vcc, 0, v2, vcc
	v_cmp_gt_u32_e32 vcc, 6, v2
	s_nop 1
	v_cndmask_b32_e32 v6, 0, v5, vcc
	s_nop 1
	v_add_f32_dpp v6, v6, v6 quad_perm:[1,0,3,2] row_mask:0xf bank_mask:0xf
	s_nop 1
	v_add_f32_dpp v6, v6, v6 quad_perm:[2,3,0,1] row_mask:0xf bank_mask:0xf
	s_nop 1
	v_add_f32_dpp v6, v6, v6 row_half_mirror row_mask:0xf bank_mask:0xf
	s_nop 1
	v_add_f32_dpp v6, v6, v6 row_mirror row_mask:0xf bank_mask:0xf
	v_mov_b32_e32 v7, v6
	s_nop 1
	v_permlane16_swap_b32_e32 v7, v6
	s_waitcnt lgkmcnt(0)
	v_add_f32_e32 v6, v6, v7
	v_mov_b32_e32 v7, v6
	s_nop 1
	v_permlane32_swap_b32_e32 v7, v6
	s_and_saveexec_b64 s[20:21], vcc
	s_cbranch_execz .LBB0_1324
	s_waitcnt lgkmcnt(0)
	v_add_f32_e32 v10, v6, v7
	v_mad_u64_u32 v[6:7], s[4:5], s4, 6, v[2:3]
	v_div_scale_f32 v2, s[4:5], v10, v10, v5
	v_rcp_f32_e32 v12, v2
	v_ashrrev_i32_e32 v7, 31, v6
	v_lshlrev_b64 v[6:7], 2, v[6:7]
	v_lshl_add_u64 v[8:9], s[42:43], 0, v[6:7]
	ds_add_rtn_u32 v11, v227, v243
	global_store_dword v[8:9], v230, off
	v_fma_f32 v8, -v2, v12, 1.0
	v_fmac_f32_e32 v12, v8, v12
	v_div_scale_f32 v8, vcc, v5, v10, v5
	v_mul_f32_e32 v9, v8, v12
	v_fma_f32 v13, -v2, v9, v8
	v_fmac_f32_e32 v9, v13, v12
	v_fma_f32 v2, -v2, v9, v8
	v_div_fmas_f32 v2, v2, v12, v9
	v_div_fixup_f32 v2, v2, v10, v5
	v_mul_f32_e32 v2, 0x40200000, v2
	v_lshl_add_u64 v[8:9], s[44:45], 0, v[6:7]
	v_lshl_add_u64 v[6:7], s[46:47], 0, v[6:7]
	global_store_dword v[8:9], v2, off
	s_waitcnt lgkmcnt(0)
	global_store_dword v[6:7], v11, off
; __device__ __forceinline__ void phase_nrr(const Frame& F, const Args& a, int l, const bf16_t* XA, const float* g, const float* modl, unsigned char* XN8) {
;     ...
;         for (int i = 0; i < 8; ++i) { const int t = tb + i;
;             const float lg = Pl[(w * 8 + i) * NE + lane] + Pl[(64 + w * 8 + i) * NE + lane]; const float sc = 1.f / (1.f + __expf(-lg)); const float bb = sc + bias;
;             float m1 = bb; m1 = fmaxf(m1, __shfl_xor(m1, 1)); m1 = fmaxf(m1, __shfl_xor(m1, 2)); m1 = fmaxf(m1, __shfl_xor(m1, 4));
;             const unsigned long long eq = __ballot(bb == m1); const int gbase = lane & ~7; const unsigned grpmask = (unsigned)((eq >> gbase) & 0xffull);
;             const int first = gbase + __builtin_ctz(grpmask);
;             float m2 = (lane == first) ? -INFINITY : bb; m2 = fmaxf(m2, __shfl_xor(m2, 1)); m2 = fmaxf(m2, __shfl_xor(m2, 2)); m2 = fmaxf(m2, __shfl_xor(m2, 4));
;             const float gsum = m1 + m2; const int gq = lane >> 3;
;             int grank = 0;
; #pragma unroll
;             for (int g2 = 0; g2 < 8; ++g2) { const float v = __int_as_float(__builtin_amdgcn_readlane(__float_as_int(gsum), g2 * 8)); grank += (v > gsum || (v == gsum && g2 < gq)) ? 1 : 0; }
;             const bool keep = grank < 4; const float val = keep ? bb : -INFINITY;
;             int rank = 0;
; #pragma unroll 8
;             for (int e2 = 0; e2 < 64; ++e2) { const float v = __int_as_float(__builtin_amdgcn_readlane(__float_as_int(val), e2)); rank += (v > val || (v == val && e2 < lane)) ? 1 : 0; }
.LBB0_1324:
	s_or_b64 exec, exec, s[20:21]
	v_add_u32_e32 v2, s79, v226
	ds_read_b32 v2, v2
	ds_read_b32 v5, v4 offset:17408
	s_mov_b32 s3, 0
	s_waitcnt lgkmcnt(0)
	v_add_f32_e32 v2, v2, v5
	v_mul_f32_e32 v2, 0xbfb8aa3b, v2
	v_exp_f32_e32 v2, v2
	s_nop 0
	v_add_f32_e32 v2, 1.0, v2
	v_div_scale_f32 v5, s[4:5], v2, v2, 1.0
	v_rcp_f32_e32 v6, v5
	v_div_scale_f32 v7, vcc, 1.0, v2, 1.0
	v_fma_f32 v8, -v5, v6, 1.0
	v_fmac_f32_e32 v6, v8, v6
	v_mul_f32_e32 v8, v7, v6
	v_fma_f32 v9, -v5, v8, v7
	v_fmac_f32_e32 v8, v9, v6
	v_fma_f32 v5, -v5, v8, v7
	v_div_fmas_f32 v5, v5, v6, v8
	v_div_fixup_f32 v2, v5, v2, 1.0
	v_add_f32_e32 v5, v3, v2
	s_nop 1
	s_waitcnt lgkmcnt(0)
	v_max_f32_dpp v6, v5, v5 quad_perm:[1,0,3,2] row_mask:0xf bank_mask:0xf
	s_nop 1
	s_waitcnt lgkmcnt(0)
	v_max_f32_dpp v6, v6, v6 quad_perm:[2,3,0,1] row_mask:0xf bank_mask:0xf
	s_nop 1
	s_waitcnt lgkmcnt(0)
	v_max_f32_dpp v8, v6, v6 row_half_mirror row_mask:0xf bank_mask:0xf
	v_cmp_eq_f32_e32 vcc, v5, v8
	s_nop 1
	v_lshrrev_b64 v[6:7], v200, vcc
	v_ffbl_b32_sdwa v6, v6 dst_sel:DWORD dst_unused:UNUSED_PAD src0_sel:BYTE_0
	v_add_u32_e32 v6, v6, v200
	v_cmp_ne_u32_e32 vcc, v230, v6
	s_nop 1
	v_cndmask_b32_e32 v6, v245, v5, vcc
	s_nop 1
	s_waitcnt lgkmcnt(0)
	v_max_f32_dpp v6, v6, v6 quad_perm:[1,0,3,2] row_mask:0xf bank_mask:0xf
	s_nop 1
	s_waitcnt lgkmcnt(0)
	v_max_f32_dpp v6, v6, v6 quad_perm:[2,3,0,1] row_mask:0xf bank_mask:0xf
	s_nop 1
	s_waitcnt lgkmcnt(0)
	v_max_f32_dpp v6, v6, v6 row_half_mirror row_mask:0xf bank_mask:0xf
	v_add_f32_e32 v6, v8, v6
	s_nop 0
	v_readlane_b32 s4, v6, 0
	v_readlane_b32 s5, v6, 8
	v_readlane_b32 s28, v6, 16
	v_cmp_eq_f32_e64 s[20:21], s4, v6
	v_cmp_gt_f32_e32 vcc, s4, v6
	v_cmp_gt_f32_e64 s[22:23], s5, v6
	v_cmp_eq_f32_e64 s[24:25], s5, v6
	s_and_b64 s[4:5], s[0:1], s[20:21]
	v_readlane_b32 s34, v6, 24
	v_cmp_gt_f32_e64 s[26:27], s28, v6
	v_cmp_eq_f32_e64 s[28:29], s28, v6
	s_and_b64 s[20:21], s[6:7], s[24:25]
	s_or_b64 s[4:5], vcc, s[4:5]
	v_readlane_b32 s40, v6, 32
	v_cmp_gt_f32_e64 s[30:31], s34, v6
	v_cmp_eq_f32_e64 s[34:35], s34, v6
	s_and_b64 s[24:25], s[8:9], s[28:29]
	v_cndmask_b32_e64 v7, 0, 1, s[4:5]
	s_or_b64 s[4:5], s[22:23], s[20:21]
	v_cmp_gt_f32_e64 s[36:37], s40, v6
	v_cmp_eq_f32_e64 s[40:41], s40, v6
	s_and_b64 s[28:29], s[10:11], s[34:35]
	v_cndmask_b32_e64 v8, 0, 1, s[4:5]
	s_or_b64 s[4:5], s[26:27], s[24:25]
	v_readlane_b32 s54, v6, 40
	s_and_b64 s[34:35], s[12:13], s[40:41]
	v_cndmask_b32_e64 v9, 0, 1, s[4:5]
	s_or_b64 s[4:5], s[30:31], s[28:29]
	v_cndmask_b32_e64 v10, 0, 1, s[4:5]
	s_or_b64 s[4:5], s[36:37], s[34:35]
	v_cmp_eq_f32_e64 s[20:21], s54, v6
	v_cndmask_b32_e64 v11, 0, 1, s[4:5]
	v_cmp_gt_f32_e32 vcc, s54, v6
	s_and_b64 s[4:5], s[14:15], s[20:21]
	s_or_b64 s[4:5], vcc, s[4:5]
	v_cndmask_b32_e64 v12, 0, 1, s[4:5]
	v_readlane_b32 s4, v6, 48
	s_nop 1
	v_cmp_eq_f32_e64 s[20:21], s4, v6
	v_cmp_gt_f32_e32 vcc, s4, v6
	s_and_b64 s[4:5], s[16:17], s[20:21]
	s_or_b64 s[4:5], vcc, s[4:5]
	v_cndmask_b32_e64 v13, 0, 1, s[4:5]
	v_readlane_b32 s4, v6, 56
	s_nop 1
	v_cmp_gt_f32_e32 vcc, s4, v6
	s_nop 1
	v_cndmask_b32_e64 v6, 0, 1, vcc
	v_add_u32_e32 v6, v8, v6
	v_add3_u32 v6, v6, v7, v9
	v_add3_u32 v6, v6, v10, v11
	v_add3_u32 v6, v6, v12, v13
	v_cmp_eq_u32_e32 vcc, 0, v6
	s_ff1_i32_b64 s98, vcc
	v_cmp_eq_u32_e32 vcc, 1, v6
	s_ff1_i32_b64 s99, vcc
	v_cmp_eq_u32_e32 vcc, 2, v6
	s_ff1_i32_b64 s100, vcc
	v_cmp_eq_u32_e32 vcc, 3, v6
	s_ff1_i32_b64 s101, vcc
	v_cmp_gt_u32_e32 vcc, 4, v6
	v_mov_b32_e32 v6, 0
	s_nop 0
	v_cndmask_b32_e32 v5, v245, v5, vcc
	v_ashrrev_i32_e32 v9, 31, v5
	v_sub_u32_e32 v8, 63, v230
	v_and_b32_e32 v9, 0x7fffffff, v9
	v_xor_b32_e32 v9, v5, v9
	s_nop 0
	v_readlane_b32 s23, v9, s98
	s_sub_i32 s22, 63, s98
	s_add_i32 s98, s98, 1
	v_readlane_b32 s21, v9, s98
	s_sub_i32 s20, 63, s98
	s_add_i32 s98, s98, 1
	v_cmp_gt_i64_e32 vcc, s[22:23], v[8:9]
	v_readlane_b32 s23, v9, s98
	s_sub_i32 s22, 63, s98
	s_add_i32 s98, s98, 1
	v_addc_co_u32_e32 v6, vcc, 0, v6, vcc
	v_cmp_gt_i64_e32 vcc, s[20:21], v[8:9]
	v_readlane_b32 s21, v9, s98
	s_sub_i32 s20, 63, s98
	s_add_i32 s98, s98, 1
	v_addc_co_u32_e32 v6, vcc, 0, v6, vcc
	v_cmp_gt_i64_e32 vcc, s[22:23], v[8:9]
	v_readlane_b32 s23, v9, s98
	s_sub_i32 s22, 63, s98
	s_add_i32 s98, s98, 1
	v_addc_co_u32_e32 v6, vcc, 0, v6, vcc
	v_cmp_gt_i64_e32 vcc, s[20:21], v[8:9]
	v_readlane_b32 s21, v9, s98
	s_sub_i32 s20, 63, s98
	s_add_i32 s98, s98, 1
	v_addc_co_u32_e32 v6, vcc, 0, v6, vcc
	v_cmp_gt_i64_e32 vcc, s[22:23], v[8:9]
	v_readlane_b32 s23, v9, s98
	s_sub_i32 s22, 63, s98
	s_add_i32 s98, s98, 1
	v_addc_co_u32_e32 v6, vcc, 0, v6, vcc
	v_cmp_gt_i64_e32 vcc, s[20:21], v[8:9]
	v_readlane_b32 s21, v9, s98
	s_sub_i32 s20, 63, s98
	s_nop 0
	v_addc_co_u32_e32 v6, vcc, 0, v6, vcc
	v_cmp_gt_i64_e32 vcc, s[22:23], v[8:9]
	v_readlane_b32 s23, v9, s99
	s_sub_i32 s22, 63, s99
	s_add_i32 s99, s99, 1
	v_addc_co_u32_e32 v6, vcc, 0, v6, vcc
	v_cmp_gt_i64_e32 vcc, s[20:21], v[8:9]
	v_readlane_b32 s21, v9, s99
	s_sub_i32 s20, 63, s99
	s_add_i32 s99, s99, 1
	v_addc_co_u32_e32 v6, vcc, 0, v6, vcc
	v_cmp_gt_i64_e32 vcc, s[22:23], v[8:9]
	v_readlane_b32 s23, v9, s99
	s_sub_i32 s22, 63, s99
	s_add_i32 s99, s99, 1
	v_addc_co_u32_e32 v6, vcc, 0, v6, vcc
	v_cmp_gt_i64_e32 vcc, s[20:21], v[8:9]
	v_readlane_b32 s21, v9, s99
	s_sub_i32 s20, 63, s99
	s_add_i32 s99, s99, 1
	v_addc_co_u32_e32 v6, vcc, 0, v6, vcc
	v_cmp_gt_i64_e32 vcc, s[22:23], v[8:9]
	v_readlane_b32 s23, v9, s99
	s_sub_i32 s22, 63, s99
	s_add_i32 s99, s99, 1
	v_addc_co_u32_e32 v6, vcc, 0, v6, vcc
	v_cmp_gt_i64_e32 vcc, s[20:21], v[8:9]
	v_readlane_b32 s21, v9, s99
	s_sub_i32 s20, 63, s99
	s_add_i32 s99, s99, 1
	v_addc_co_u32_e32 v6, vcc, 0, v6, vcc
; __device__ __forceinline__ float wave_sum(float v) {
; #pragma unroll
;     for (int o = 1; o < 64; o <<= 1) v += __shfl_xor(v, o);
;     return v;
; __device__ __forceinline__ void phase_nrr(const Frame& F, const Args& a, int l, const bf16_t* XA, const float* g, const float* modl, unsigned char* XN8) {
;     ...
;             for (int e2 = 0; e2 < 64; ++e2) { const float v = __int_as_float(__builtin_amdgcn_readlane(__float_as_int(val), e2)); rank += (v > val || (v == val && e2 < lane)) ? 1 : 0; }
;             const bool sel = rank < TOPK;
;             const float ssum = wave_sum(sel ? sc : 0.f);
;             if (sel) { const int p = atomicAdd((int*)(hist + lane), 1); top_e[t * TOPK + rank] = lane; gate[t * TOPK + rank] = sc / ssum * 2.5f; lpos[t * TOPK + rank] = p; }
	v_cmp_gt_i64_e32 vcc, s[22:23], v[8:9]
	v_readlane_b32 s23, v9, s99
	s_sub_i32 s22, 63, s99
	s_add_i32 s99, s99, 1
	v_addc_co_u32_e32 v6, vcc, 0, v6, vcc
	v_cmp_gt_i64_e32 vcc, s[20:21], v[8:9]
	v_readlane_b32 s21, v9, s99
	s_sub_i32 s20, 63, s99
	s_nop 0
	v_addc_co_u32_e32 v6, vcc, 0, v6, vcc
	v_cmp_gt_i64_e32 vcc, s[22:23], v[8:9]
	v_readlane_b32 s23, v9, s100
	s_sub_i32 s22, 63, s100
	s_add_i32 s100, s100, 1
	v_addc_co_u32_e32 v6, vcc, 0, v6, vcc
	v_cmp_gt_i64_e32 vcc, s[20:21], v[8:9]
	v_readlane_b32 s21, v9, s100
	s_sub_i32 s20, 63, s100
	s_add_i32 s100, s100, 1
	v_addc_co_u32_e32 v6, vcc, 0, v6, vcc
	v_cmp_gt_i64_e32 vcc, s[22:23], v[8:9]
	v_readlane_b32 s23, v9, s100
	s_sub_i32 s22, 63, s100
	s_add_i32 s100, s100, 1
	v_addc_co_u32_e32 v6, vcc, 0, v6, vcc
	v_cmp_gt_i64_e32 vcc, s[20:21], v[8:9]
	v_readlane_b32 s21, v9, s100
	s_sub_i32 s20, 63, s100
	s_add_i32 s100, s100, 1
	v_addc_co_u32_e32 v6, vcc, 0, v6, vcc
	v_cmp_gt_i64_e32 vcc, s[22:23], v[8:9]
	v_readlane_b32 s23, v9, s100
	s_sub_i32 s22, 63, s100
	s_add_i32 s100, s100, 1
	v_addc_co_u32_e32 v6, vcc, 0, v6, vcc
	v_cmp_gt_i64_e32 vcc, s[20:21], v[8:9]
	v_readlane_b32 s21, v9, s100
	s_sub_i32 s20, 63, s100
	s_add_i32 s100, s100, 1
	v_addc_co_u32_e32 v6, vcc, 0, v6, vcc
	v_cmp_gt_i64_e32 vcc, s[22:23], v[8:9]
	v_readlane_b32 s23, v9, s100
	s_sub_i32 s22, 63, s100
	s_add_i32 s100, s100, 1
	v_addc_co_u32_e32 v6, vcc, 0, v6, vcc
	v_cmp_gt_i64_e32 vcc, s[20:21], v[8:9]
	v_readlane_b32 s21, v9, s100
	s_sub_i32 s20, 63, s100
	s_nop 0
	v_addc_co_u32_e32 v6, vcc, 0, v6, vcc
	v_cmp_gt_i64_e32 vcc, s[22:23], v[8:9]
	v_readlane_b32 s23, v9, s101
	s_sub_i32 s22, 63, s101
	s_add_i32 s101, s101, 1
	v_addc_co_u32_e32 v6, vcc, 0, v6, vcc
	v_cmp_gt_i64_e32 vcc, s[20:21], v[8:9]
	v_readlane_b32 s21, v9, s101
	s_sub_i32 s20, 63, s101
	s_add_i32 s101, s101, 1
	v_addc_co_u32_e32 v6, vcc, 0, v6, vcc
	v_cmp_gt_i64_e32 vcc, s[22:23], v[8:9]
	v_readlane_b32 s23, v9, s101
	s_sub_i32 s22, 63, s101
	s_add_i32 s101, s101, 1
	v_addc_co_u32_e32 v6, vcc, 0, v6, vcc
	v_cmp_gt_i64_e32 vcc, s[20:21], v[8:9]
	v_readlane_b32 s21, v9, s101
	s_sub_i32 s20, 63, s101
	s_add_i32 s101, s101, 1
	v_addc_co_u32_e32 v6, vcc, 0, v6, vcc
	v_cmp_gt_i64_e32 vcc, s[22:23], v[8:9]
	v_readlane_b32 s23, v9, s101
	s_sub_i32 s22, 63, s101
	s_add_i32 s101, s101, 1
	v_addc_co_u32_e32 v6, vcc, 0, v6, vcc
	v_cmp_gt_i64_e32 vcc, s[20:21], v[8:9]
	v_readlane_b32 s21, v9, s101
	s_sub_i32 s20, 63, s101
	s_add_i32 s101, s101, 1
	v_addc_co_u32_e32 v6, vcc, 0, v6, vcc
	v_cmp_gt_i64_e32 vcc, s[22:23], v[8:9]
	v_readlane_b32 s23, v9, s101
	s_sub_i32 s22, 63, s101
	s_add_i32 s101, s101, 1
	v_addc_co_u32_e32 v6, vcc, 0, v6, vcc
	v_cmp_gt_i64_e32 vcc, s[20:21], v[8:9]
	v_readlane_b32 s21, v9, s101
	s_sub_i32 s20, 63, s101
	s_nop 0
	v_addc_co_u32_e32 v6, vcc, 0, v6, vcc
	v_cmp_gt_i64_e32 vcc, s[22:23], v[8:9]
	s_nop 1
	v_addc_co_u32_e32 v6, vcc, 0, v6, vcc
	v_cmp_gt_i64_e32 vcc, s[20:21], v[8:9]
	s_nop 1
	v_addc_co_u32_e32 v6, vcc, 0, v6, vcc
	v_cmp_gt_u32_e32 vcc, 6, v6
	s_nop 1
	v_cndmask_b32_e32 v5, 0, v2, vcc
	s_nop 1
	v_add_f32_dpp v5, v5, v5 quad_perm:[1,0,3,2] row_mask:0xf bank_mask:0xf
	s_nop 1
	v_add_f32_dpp v5, v5, v5 quad_perm:[2,3,0,1] row_mask:0xf bank_mask:0xf
	s_nop 1
	v_add_f32_dpp v5, v5, v5 row_half_mirror row_mask:0xf bank_mask:0xf
	s_nop 1
	v_add_f32_dpp v5, v5, v5 row_mirror row_mask:0xf bank_mask:0xf
	v_mov_b32_e32 v7, v5
	s_nop 1
	v_permlane16_swap_b32_e32 v7, v5
	s_waitcnt lgkmcnt(0)
	v_add_f32_e32 v5, v5, v7
	v_mov_b32_e32 v7, v5
	s_nop 1
	v_permlane32_swap_b32_e32 v7, v5
	s_and_saveexec_b64 s[4:5], vcc
	s_cbranch_execz .LBB0_1328
	s_waitcnt lgkmcnt(0)
	v_add_f32_e32 v5, v5, v7
	s_mul_i32 s2, s2, 6
	v_or_b32_e32 v6, s2, v6
	v_div_scale_f32 v11, s[2:3], v5, v5, v2
	v_rcp_f32_e32 v12, v11
	v_ashrrev_i32_e32 v7, 31, v6
	v_lshlrev_b64 v[6:7], 2, v[6:7]
	v_lshl_add_u64 v[8:9], s[42:43], 0, v[6:7]
	ds_add_rtn_u32 v10, v227, v243
	global_store_dword v[8:9], v230, off
	v_fma_f32 v8, -v11, v12, 1.0
	v_fmac_f32_e32 v12, v8, v12
	v_div_scale_f32 v8, vcc, v2, v5, v2
	v_mul_f32_e32 v9, v8, v12
	v_fma_f32 v13, -v11, v9, v8
	v_fmac_f32_e32 v9, v13, v12
	v_fma_f32 v8, -v11, v9, v8
	v_div_fmas_f32 v8, v8, v12, v9
	v_div_fixup_f32 v2, v8, v5, v2
	v_mul_f32_e32 v2, 0x40200000, v2
	v_lshl_add_u64 v[8:9], s[44:45], 0, v[6:7]
	v_lshl_add_u64 v[6:7], s[46:47], 0, v[6:7]
	global_store_dword v[8:9], v2, off
	s_waitcnt lgkmcnt(0)
	global_store_dword v[6:7], v10, off
; __device__ __forceinline__ void phase_nrr(const Frame& F, const Args& a, int l, const bf16_t* XA, const float* g, const float* modl, unsigned char* XN8) {
;     ...
;         for (int i = 0; i < 8; ++i) { const int t = tb + i;
;             const float lg = Pl[(w * 8 + i) * NE + lane] + Pl[(64 + w * 8 + i) * NE + lane]; const float sc = 1.f / (1.f + __expf(-lg)); const float bb = sc + bias;
;             float m1 = bb; m1 = fmaxf(m1, __shfl_xor(m1, 1)); m1 = fmaxf(m1, __shfl_xor(m1, 2)); m1 = fmaxf(m1, __shfl_xor(m1, 4));
;             const unsigned long long eq = __ballot(bb == m1); const int gbase = lane & ~7; const unsigned grpmask = (unsigned)((eq >> gbase) & 0xffull);
;             const int first = gbase + __builtin_ctz(grpmask);
;             float m2 = (lane == first) ? -INFINITY : bb; m2 = fmaxf(m2, __shfl_xor(m2, 1)); m2 = fmaxf(m2, __shfl_xor(m2, 2)); m2 = fmaxf(m2, __shfl_xor(m2, 4));
;             const float gsum = m1 + m2; const int gq = lane >> 3;
;             int grank = 0;
; #pragma unroll
;             for (int g2 = 0; g2 < 8; ++g2) { const float v = __int_as_float(__builtin_amdgcn_readlane(__float_as_int(gsum), g2 * 8)); grank += (v > gsum || (v == gsum && g2 < gq)) ? 1 : 0; }
;             const bool keep = grank < 4; const float val = keep ? bb : -INFINITY;
;             int rank = 0;
; #pragma unroll 8
;             for (int e2 = 0; e2 < 64; ++e2) { const float v = __int_as_float(__builtin_amdgcn_readlane(__float_as_int(val), e2)); rank += (v > val || (v == val && e2 < lane)) ? 1 : 0; }
.LBB0_1328:
	s_or_b64 exec, exec, s[4:5]
	v_add_u32_e32 v2, s80, v226
	ds_read_b32 v2, v2
	ds_read_b32 v5, v4 offset:17664
	s_waitcnt lgkmcnt(0)
	v_add_f32_e32 v2, v2, v5
	v_mul_f32_e32 v2, 0xbfb8aa3b, v2
	v_exp_f32_e32 v2, v2
	s_nop 0
	v_add_f32_e32 v2, 1.0, v2
	v_div_scale_f32 v5, s[2:3], v2, v2, 1.0
	v_rcp_f32_e32 v6, v5
	v_div_scale_f32 v7, vcc, 1.0, v2, 1.0
	s_mov_b32 s2, 0
	v_fma_f32 v8, -v5, v6, 1.0
	v_fmac_f32_e32 v6, v8, v6
	v_mul_f32_e32 v8, v7, v6
	v_fma_f32 v9, -v5, v8, v7
	v_fmac_f32_e32 v8, v9, v6
	v_fma_f32 v5, -v5, v8, v7
	v_div_fmas_f32 v5, v5, v6, v8
	v_div_fixup_f32 v2, v5, v2, 1.0
	v_add_f32_e32 v5, v3, v2
	s_nop 1
	s_waitcnt lgkmcnt(0)
	v_max_f32_dpp v6, v5, v5 quad_perm:[1,0,3,2] row_mask:0xf bank_mask:0xf
	s_nop 1
	s_waitcnt lgkmcnt(0)
	v_max_f32_dpp v6, v6, v6 quad_perm:[2,3,0,1] row_mask:0xf bank_mask:0xf
	s_nop 1
	s_waitcnt lgkmcnt(0)
	v_max_f32_dpp v8, v6, v6 row_half_mirror row_mask:0xf bank_mask:0xf
	v_cmp_eq_f32_e32 vcc, v5, v8
	s_nop 1
	v_lshrrev_b64 v[6:7], v200, vcc
	v_ffbl_b32_sdwa v6, v6 dst_sel:DWORD dst_unused:UNUSED_PAD src0_sel:BYTE_0
	v_add_u32_e32 v6, v6, v200
	v_cmp_ne_u32_e32 vcc, v230, v6
	s_nop 1
	v_cndmask_b32_e32 v6, v245, v5, vcc
	s_nop 1
	s_waitcnt lgkmcnt(0)
	v_max_f32_dpp v6, v6, v6 quad_perm:[1,0,3,2] row_mask:0xf bank_mask:0xf
	s_nop 1
	s_waitcnt lgkmcnt(0)
	v_max_f32_dpp v6, v6, v6 quad_perm:[2,3,0,1] row_mask:0xf bank_mask:0xf
	s_nop 1
	s_waitcnt lgkmcnt(0)
	v_max_f32_dpp v6, v6, v6 row_half_mirror row_mask:0xf bank_mask:0xf
	v_add_f32_e32 v6, v8, v6
	s_nop 0
	v_readlane_b32 s3, v6, 0
	v_readlane_b32 s4, v6, 8
	v_readlane_b32 s5, v6, 16
	v_cmp_eq_f32_e64 s[20:21], s3, v6
	v_cmp_gt_f32_e32 vcc, s3, v6
	v_cmp_gt_f32_e64 s[22:23], s4, v6
	v_cmp_eq_f32_e64 s[24:25], s4, v6
	v_cmp_gt_f32_e64 s[26:27], s5, v6
	v_cmp_eq_f32_e64 s[28:29], s5, v6
	s_and_b64 s[4:5], s[0:1], s[20:21]
	v_readlane_b32 s34, v6, 24
	s_and_b64 s[20:21], s[6:7], s[24:25]
	s_or_b64 s[4:5], vcc, s[4:5]
	v_readlane_b32 s40, v6, 32
	v_cmp_gt_f32_e64 s[30:31], s34, v6
	v_cmp_eq_f32_e64 s[34:35], s34, v6
	s_and_b64 s[24:25], s[8:9], s[28:29]
	v_cndmask_b32_e64 v7, 0, 1, s[4:5]
	s_or_b64 s[4:5], s[22:23], s[20:21]
	v_cmp_gt_f32_e64 s[36:37], s40, v6
	v_cmp_eq_f32_e64 s[40:41], s40, v6
	s_and_b64 s[28:29], s[10:11], s[34:35]
	v_cndmask_b32_e64 v8, 0, 1, s[4:5]
	s_or_b64 s[4:5], s[26:27], s[24:25]
	v_readlane_b32 s54, v6, 40
	s_and_b64 s[34:35], s[12:13], s[40:41]
	v_cndmask_b32_e64 v9, 0, 1, s[4:5]
	s_or_b64 s[4:5], s[30:31], s[28:29]
	v_cndmask_b32_e64 v10, 0, 1, s[4:5]
	s_or_b64 s[4:5], s[36:37], s[34:35]
	v_cmp_eq_f32_e64 s[20:21], s54, v6
	v_cndmask_b32_e64 v11, 0, 1, s[4:5]
	v_cmp_gt_f32_e32 vcc, s54, v6
	s_and_b64 s[4:5], s[14:15], s[20:21]
	v_readlane_b32 s3, v6, 48
	s_or_b64 s[4:5], vcc, s[4:5]
	v_cndmask_b32_e64 v12, 0, 1, s[4:5]
	v_cmp_eq_f32_e64 s[20:21], s3, v6
	v_cmp_gt_f32_e32 vcc, s3, v6
	s_and_b64 s[4:5], s[16:17], s[20:21]
	v_readlane_b32 s3, v6, 56
	s_or_b64 s[4:5], vcc, s[4:5]
	v_cndmask_b32_e64 v13, 0, 1, s[4:5]
	v_cmp_gt_f32_e32 vcc, s3, v6
	s_nop 1
	v_cndmask_b32_e64 v6, 0, 1, vcc
	v_add_u32_e32 v6, v8, v6
	v_add3_u32 v6, v6, v7, v9
	v_add3_u32 v6, v6, v10, v11
	v_add3_u32 v6, v6, v12, v13
	v_cmp_eq_u32_e32 vcc, 0, v6
	s_ff1_i32_b64 s98, vcc
	v_cmp_eq_u32_e32 vcc, 1, v6
	s_ff1_i32_b64 s99, vcc
	v_cmp_eq_u32_e32 vcc, 2, v6
	s_ff1_i32_b64 s100, vcc
	v_cmp_eq_u32_e32 vcc, 3, v6
	s_ff1_i32_b64 s101, vcc
	v_cmp_gt_u32_e32 vcc, 4, v6
	v_mov_b32_e32 v6, 0
	s_nop 0
	v_cndmask_b32_e32 v5, v245, v5, vcc
	v_ashrrev_i32_e32 v9, 31, v5
	v_sub_u32_e32 v8, 63, v230
	v_and_b32_e32 v9, 0x7fffffff, v9
	v_xor_b32_e32 v9, v5, v9
	s_nop 0
	v_readlane_b32 s23, v9, s98
	s_sub_i32 s22, 63, s98
	s_add_i32 s98, s98, 1
	v_readlane_b32 s21, v9, s98
	s_sub_i32 s20, 63, s98
	s_add_i32 s98, s98, 1
	v_cmp_gt_i64_e32 vcc, s[22:23], v[8:9]
	v_readlane_b32 s23, v9, s98
	s_sub_i32 s22, 63, s98
	s_add_i32 s98, s98, 1
	v_addc_co_u32_e32 v6, vcc, 0, v6, vcc
	v_cmp_gt_i64_e32 vcc, s[20:21], v[8:9]
	v_readlane_b32 s21, v9, s98
	s_sub_i32 s20, 63, s98
	s_add_i32 s98, s98, 1
	v_addc_co_u32_e32 v6, vcc, 0, v6, vcc
	v_cmp_gt_i64_e32 vcc, s[22:23], v[8:9]
	v_readlane_b32 s23, v9, s98
	s_sub_i32 s22, 63, s98
	s_add_i32 s98, s98, 1
	v_addc_co_u32_e32 v6, vcc, 0, v6, vcc
	v_cmp_gt_i64_e32 vcc, s[20:21], v[8:9]
	v_readlane_b32 s21, v9, s98
	s_sub_i32 s20, 63, s98
	s_add_i32 s98, s98, 1
	v_addc_co_u32_e32 v6, vcc, 0, v6, vcc
	v_cmp_gt_i64_e32 vcc, s[22:23], v[8:9]
	v_readlane_b32 s23, v9, s98
	s_sub_i32 s22, 63, s98
	s_add_i32 s98, s98, 1
	v_addc_co_u32_e32 v6, vcc, 0, v6, vcc
	v_cmp_gt_i64_e32 vcc, s[20:21], v[8:9]
	v_readlane_b32 s21, v9, s98
	s_sub_i32 s20, 63, s98
	s_nop 0
	v_addc_co_u32_e32 v6, vcc, 0, v6, vcc
	v_cmp_gt_i64_e32 vcc, s[22:23], v[8:9]
	v_readlane_b32 s23, v9, s99
	s_sub_i32 s22, 63, s99
	s_add_i32 s99, s99, 1
	v_addc_co_u32_e32 v6, vcc, 0, v6, vcc
	v_cmp_gt_i64_e32 vcc, s[20:21], v[8:9]
	v_readlane_b32 s21, v9, s99
	s_sub_i32 s20, 63, s99
	s_add_i32 s99, s99, 1
	v_addc_co_u32_e32 v6, vcc, 0, v6, vcc
	v_cmp_gt_i64_e32 vcc, s[22:23], v[8:9]
	v_readlane_b32 s23, v9, s99
	s_sub_i32 s22, 63, s99
	s_add_i32 s99, s99, 1
	v_addc_co_u32_e32 v6, vcc, 0, v6, vcc
	v_cmp_gt_i64_e32 vcc, s[20:21], v[8:9]
	v_readlane_b32 s21, v9, s99
	s_sub_i32 s20, 63, s99
	s_add_i32 s99, s99, 1
	v_addc_co_u32_e32 v6, vcc, 0, v6, vcc
	v_cmp_gt_i64_e32 vcc, s[22:23], v[8:9]
	v_readlane_b32 s23, v9, s99
	s_sub_i32 s22, 63, s99
	s_add_i32 s99, s99, 1
	v_addc_co_u32_e32 v6, vcc, 0, v6, vcc
	v_cmp_gt_i64_e32 vcc, s[20:21], v[8:9]
	v_readlane_b32 s21, v9, s99
	s_sub_i32 s20, 63, s99
	s_add_i32 s99, s99, 1
	v_addc_co_u32_e32 v6, vcc, 0, v6, vcc
	v_cmp_gt_i64_e32 vcc, s[22:23], v[8:9]
; __device__ __forceinline__ float wave_sum(float v) {
; #pragma unroll
;     for (int o = 1; o < 64; o <<= 1) v += __shfl_xor(v, o);
;     return v;
; __device__ __forceinline__ void phase_nrr(const Frame& F, const Args& a, int l, const bf16_t* XA, const float* g, const float* modl, unsigned char* XN8) {
;     ...
;             for (int e2 = 0; e2 < 64; ++e2) { const float v = __int_as_float(__builtin_amdgcn_readlane(__float_as_int(val), e2)); rank += (v > val || (v == val && e2 < lane)) ? 1 : 0; }
;             const bool sel = rank < TOPK;
;             const float ssum = wave_sum(sel ? sc : 0.f);
;             if (sel) { const int p = atomicAdd((int*)(hist + lane), 1); top_e[t * TOPK + rank] = lane; gate[t * TOPK + rank] = sc / ssum * 2.5f; lpos[t * TOPK + rank] = p; }
	v_readlane_b32 s23, v9, s99
	s_sub_i32 s22, 63, s99
	s_add_i32 s99, s99, 1
	v_addc_co_u32_e32 v6, vcc, 0, v6, vcc
	v_cmp_gt_i64_e32 vcc, s[20:21], v[8:9]
	v_readlane_b32 s21, v9, s99
	s_sub_i32 s20, 63, s99
	s_nop 0
	v_addc_co_u32_e32 v6, vcc, 0, v6, vcc
	v_cmp_gt_i64_e32 vcc, s[22:23], v[8:9]
	v_readlane_b32 s23, v9, s100
	s_sub_i32 s22, 63, s100
	s_add_i32 s100, s100, 1
	v_addc_co_u32_e32 v6, vcc, 0, v6, vcc
	v_cmp_gt_i64_e32 vcc, s[20:21], v[8:9]
	v_readlane_b32 s21, v9, s100
	s_sub_i32 s20, 63, s100
	s_add_i32 s100, s100, 1
	v_addc_co_u32_e32 v6, vcc, 0, v6, vcc
	v_cmp_gt_i64_e32 vcc, s[22:23], v[8:9]
	v_readlane_b32 s23, v9, s100
	s_sub_i32 s22, 63, s100
	s_add_i32 s100, s100, 1
	v_addc_co_u32_e32 v6, vcc, 0, v6, vcc
	v_cmp_gt_i64_e32 vcc, s[20:21], v[8:9]
	v_readlane_b32 s21, v9, s100
	s_sub_i32 s20, 63, s100
	s_add_i32 s100, s100, 1
	v_addc_co_u32_e32 v6, vcc, 0, v6, vcc
	v_cmp_gt_i64_e32 vcc, s[22:23], v[8:9]
	v_readlane_b32 s23, v9, s100
	s_sub_i32 s22, 63, s100
	s_add_i32 s100, s100, 1
	v_addc_co_u32_e32 v6, vcc, 0, v6, vcc
	v_cmp_gt_i64_e32 vcc, s[20:21], v[8:9]
	v_readlane_b32 s21, v9, s100
	s_sub_i32 s20, 63, s100
	s_add_i32 s100, s100, 1
	v_addc_co_u32_e32 v6, vcc, 0, v6, vcc
	v_cmp_gt_i64_e32 vcc, s[22:23], v[8:9]
	v_readlane_b32 s23, v9, s100
	s_sub_i32 s22, 63, s100
	s_add_i32 s100, s100, 1
	v_addc_co_u32_e32 v6, vcc, 0, v6, vcc
	v_cmp_gt_i64_e32 vcc, s[20:21], v[8:9]
	v_readlane_b32 s21, v9, s100
	s_sub_i32 s20, 63, s100
	s_nop 0
	v_addc_co_u32_e32 v6, vcc, 0, v6, vcc
	v_cmp_gt_i64_e32 vcc, s[22:23], v[8:9]
	v_readlane_b32 s23, v9, s101
	s_sub_i32 s22, 63, s101
	s_add_i32 s101, s101, 1
	v_addc_co_u32_e32 v6, vcc, 0, v6, vcc
	v_cmp_gt_i64_e32 vcc, s[20:21], v[8:9]
	v_readlane_b32 s21, v9, s101
	s_sub_i32 s20, 63, s101
	s_add_i32 s101, s101, 1
	v_addc_co_u32_e32 v6, vcc, 0, v6, vcc
	v_cmp_gt_i64_e32 vcc, s[22:23], v[8:9]
	v_readlane_b32 s23, v9, s101
	s_sub_i32 s22, 63, s101
	s_add_i32 s101, s101, 1
	v_addc_co_u32_e32 v6, vcc, 0, v6, vcc
	v_cmp_gt_i64_e32 vcc, s[20:21], v[8:9]
	v_readlane_b32 s21, v9, s101
	s_sub_i32 s20, 63, s101
	s_add_i32 s101, s101, 1
	v_addc_co_u32_e32 v6, vcc, 0, v6, vcc
	v_cmp_gt_i64_e32 vcc, s[22:23], v[8:9]
	v_readlane_b32 s23, v9, s101
	s_sub_i32 s22, 63, s101
	s_add_i32 s101, s101, 1
	v_addc_co_u32_e32 v6, vcc, 0, v6, vcc
	v_cmp_gt_i64_e32 vcc, s[20:21], v[8:9]
	v_readlane_b32 s21, v9, s101
	s_sub_i32 s20, 63, s101
	s_add_i32 s101, s101, 1
	v_addc_co_u32_e32 v6, vcc, 0, v6, vcc
	v_cmp_gt_i64_e32 vcc, s[22:23], v[8:9]
	v_readlane_b32 s23, v9, s101
	s_sub_i32 s22, 63, s101
	s_add_i32 s101, s101, 1
	v_addc_co_u32_e32 v6, vcc, 0, v6, vcc
	v_cmp_gt_i64_e32 vcc, s[20:21], v[8:9]
	v_readlane_b32 s21, v9, s101
	s_sub_i32 s20, 63, s101
	s_nop 0
	v_addc_co_u32_e32 v6, vcc, 0, v6, vcc
	v_cmp_gt_i64_e32 vcc, s[22:23], v[8:9]
	s_nop 1
	v_addc_co_u32_e32 v6, vcc, 0, v6, vcc
	v_cmp_gt_i64_e32 vcc, s[20:21], v[8:9]
	s_nop 1
	v_addc_co_u32_e32 v6, vcc, 0, v6, vcc
	v_cmp_gt_u32_e32 vcc, 6, v6
	s_nop 1
	v_cndmask_b32_e32 v5, 0, v2, vcc
	s_nop 1
	v_add_f32_dpp v5, v5, v5 quad_perm:[1,0,3,2] row_mask:0xf bank_mask:0xf
	s_nop 1
	v_add_f32_dpp v5, v5, v5 quad_perm:[2,3,0,1] row_mask:0xf bank_mask:0xf
	s_nop 1
	v_add_f32_dpp v5, v5, v5 row_half_mirror row_mask:0xf bank_mask:0xf
	s_nop 1
	v_add_f32_dpp v5, v5, v5 row_mirror row_mask:0xf bank_mask:0xf
	v_mov_b32_e32 v7, v5
	s_nop 1
	v_permlane16_swap_b32_e32 v7, v5
	s_waitcnt lgkmcnt(0)
	v_add_f32_e32 v5, v5, v7
	v_mov_b32_e32 v7, v5
	s_nop 1
	v_permlane32_swap_b32_e32 v7, v5
	s_and_saveexec_b64 s[2:3], vcc
	s_cbranch_execz .LBB0_1332
	s_waitcnt lgkmcnt(0)
	v_add_f32_e32 v5, v5, v7
	v_div_scale_f32 v11, s[4:5], v5, v5, v2
	v_add3_u32 v6, s50, 30, v6
	v_rcp_f32_e32 v12, v11
	v_ashrrev_i32_e32 v7, 31, v6
	v_lshlrev_b64 v[6:7], 2, v[6:7]
	v_lshl_add_u64 v[8:9], s[42:43], 0, v[6:7]
	ds_add_rtn_u32 v10, v227, v243
	global_store_dword v[8:9], v230, off
	v_fma_f32 v8, -v11, v12, 1.0
	v_fmac_f32_e32 v12, v8, v12
	v_div_scale_f32 v8, vcc, v2, v5, v2
	v_mul_f32_e32 v9, v8, v12
	v_fma_f32 v13, -v11, v9, v8
	v_fmac_f32_e32 v9, v13, v12
	v_fma_f32 v8, -v11, v9, v8
	v_div_fmas_f32 v8, v8, v12, v9
	v_div_fixup_f32 v2, v8, v5, v2
	v_mul_f32_e32 v2, 0x40200000, v2
	v_lshl_add_u64 v[8:9], s[44:45], 0, v[6:7]
	v_lshl_add_u64 v[6:7], s[46:47], 0, v[6:7]
	global_store_dword v[8:9], v2, off
	s_waitcnt lgkmcnt(0)
	global_store_dword v[6:7], v10, off
; __device__ __forceinline__ void phase_nrr(const Frame& F, const Args& a, int l, const bf16_t* XA, const float* g, const float* modl, unsigned char* XN8) {
;     ...
;         for (int i = 0; i < 8; ++i) { const int t = tb + i;
;             const float lg = Pl[(w * 8 + i) * NE + lane] + Pl[(64 + w * 8 + i) * NE + lane]; const float sc = 1.f / (1.f + __expf(-lg)); const float bb = sc + bias;
;             float m1 = bb; m1 = fmaxf(m1, __shfl_xor(m1, 1)); m1 = fmaxf(m1, __shfl_xor(m1, 2)); m1 = fmaxf(m1, __shfl_xor(m1, 4));
;             const unsigned long long eq = __ballot(bb == m1); const int gbase = lane & ~7; const unsigned grpmask = (unsigned)((eq >> gbase) & 0xffull);
;             const int first = gbase + __builtin_ctz(grpmask);
;             float m2 = (lane == first) ? -INFINITY : bb; m2 = fmaxf(m2, __shfl_xor(m2, 1)); m2 = fmaxf(m2, __shfl_xor(m2, 2)); m2 = fmaxf(m2, __shfl_xor(m2, 4));
;             const float gsum = m1 + m2; const int gq = lane >> 3;
;             int grank = 0;
; #pragma unroll
;             for (int g2 = 0; g2 < 8; ++g2) { const float v = __int_as_float(__builtin_amdgcn_readlane(__float_as_int(gsum), g2 * 8)); grank += (v > gsum || (v == gsum && g2 < gq)) ? 1 : 0; }
;             const bool keep = grank < 4; const float val = keep ? bb : -INFINITY;
;             int rank = 0;
; #pragma unroll 8
;             for (int e2 = 0; e2 < 64; ++e2) { const float v = __int_as_float(__builtin_amdgcn_readlane(__float_as_int(val), e2)); rank += (v > val || (v == val && e2 < lane)) ? 1 : 0; }
.LBB0_1332:
	s_or_b64 exec, exec, s[2:3]
	v_add_u32_e32 v2, s81, v226
	ds_read_b32 v2, v2
	ds_read_b32 v5, v4 offset:17920
	s_waitcnt lgkmcnt(0)
	v_add_f32_e32 v2, v2, v5
	v_mul_f32_e32 v2, 0xbfb8aa3b, v2
	v_exp_f32_e32 v2, v2
	s_nop 0
	v_add_f32_e32 v2, 1.0, v2
	v_div_scale_f32 v5, s[2:3], v2, v2, 1.0
	v_rcp_f32_e32 v6, v5
	v_div_scale_f32 v7, vcc, 1.0, v2, 1.0
	s_mov_b32 s2, 0
	v_fma_f32 v8, -v5, v6, 1.0
	v_fmac_f32_e32 v6, v8, v6
	v_mul_f32_e32 v8, v7, v6
	v_fma_f32 v9, -v5, v8, v7
	v_fmac_f32_e32 v8, v9, v6
	v_fma_f32 v5, -v5, v8, v7
	v_div_fmas_f32 v5, v5, v6, v8
	v_div_fixup_f32 v2, v5, v2, 1.0
	v_add_f32_e32 v5, v3, v2
	s_nop 1
	s_waitcnt lgkmcnt(0)
	v_max_f32_dpp v6, v5, v5 quad_perm:[1,0,3,2] row_mask:0xf bank_mask:0xf
	s_nop 1
	s_waitcnt lgkmcnt(0)
	v_max_f32_dpp v6, v6, v6 quad_perm:[2,3,0,1] row_mask:0xf bank_mask:0xf
	s_nop 1
	s_waitcnt lgkmcnt(0)
	v_max_f32_dpp v8, v6, v6 row_half_mirror row_mask:0xf bank_mask:0xf
	v_cmp_eq_f32_e32 vcc, v5, v8
	s_nop 1
	v_lshrrev_b64 v[6:7], v200, vcc
	v_ffbl_b32_sdwa v6, v6 dst_sel:DWORD dst_unused:UNUSED_PAD src0_sel:BYTE_0
	v_add_u32_e32 v6, v6, v200
	v_cmp_ne_u32_e32 vcc, v230, v6
	s_nop 1
	v_cndmask_b32_e32 v6, v245, v5, vcc
	s_nop 1
	s_waitcnt lgkmcnt(0)
	v_max_f32_dpp v6, v6, v6 quad_perm:[1,0,3,2] row_mask:0xf bank_mask:0xf
	s_nop 1
	s_waitcnt lgkmcnt(0)
	v_max_f32_dpp v6, v6, v6 quad_perm:[2,3,0,1] row_mask:0xf bank_mask:0xf
	s_nop 1
	s_waitcnt lgkmcnt(0)
	v_max_f32_dpp v6, v6, v6 row_half_mirror row_mask:0xf bank_mask:0xf
	v_add_f32_e32 v6, v8, v6
	s_nop 0
	v_readlane_b32 s3, v6, 0
	v_readlane_b32 s4, v6, 8
	v_readlane_b32 s5, v6, 16
	v_cmp_eq_f32_e64 s[20:21], s3, v6
	v_cmp_gt_f32_e32 vcc, s3, v6
	v_cmp_gt_f32_e64 s[22:23], s4, v6
	v_cmp_eq_f32_e64 s[24:25], s4, v6
	v_cmp_gt_f32_e64 s[26:27], s5, v6
	v_cmp_eq_f32_e64 s[28:29], s5, v6
	s_and_b64 s[4:5], s[0:1], s[20:21]
	v_readlane_b32 s34, v6, 24
	s_and_b64 s[20:21], s[6:7], s[24:25]
	s_or_b64 s[4:5], vcc, s[4:5]
	v_readlane_b32 s40, v6, 32
	v_cmp_gt_f32_e64 s[30:31], s34, v6
	v_cmp_eq_f32_e64 s[34:35], s34, v6
	s_and_b64 s[24:25], s[8:9], s[28:29]
	v_cndmask_b32_e64 v7, 0, 1, s[4:5]
	s_or_b64 s[4:5], s[22:23], s[20:21]
	v_cmp_gt_f32_e64 s[36:37], s40, v6
	v_cmp_eq_f32_e64 s[40:41], s40, v6
	s_and_b64 s[28:29], s[10:11], s[34:35]
	v_cndmask_b32_e64 v8, 0, 1, s[4:5]
	s_or_b64 s[4:5], s[26:27], s[24:25]
	v_readlane_b32 s54, v6, 40
	s_and_b64 s[34:35], s[12:13], s[40:41]
	v_cndmask_b32_e64 v9, 0, 1, s[4:5]
	s_or_b64 s[4:5], s[30:31], s[28:29]
	v_cndmask_b32_e64 v10, 0, 1, s[4:5]
	s_or_b64 s[4:5], s[36:37], s[34:35]
	v_cmp_eq_f32_e64 s[20:21], s54, v6
	v_cndmask_b32_e64 v11, 0, 1, s[4:5]
	v_cmp_gt_f32_e32 vcc, s54, v6
	s_and_b64 s[4:5], s[14:15], s[20:21]
	v_readlane_b32 s3, v6, 48
	s_or_b64 s[4:5], vcc, s[4:5]
	v_cndmask_b32_e64 v12, 0, 1, s[4:5]
	v_cmp_eq_f32_e64 s[20:21], s3, v6
	v_cmp_gt_f32_e32 vcc, s3, v6
	s_and_b64 s[4:5], s[16:17], s[20:21]
	v_readlane_b32 s3, v6, 56
	s_or_b64 s[4:5], vcc, s[4:5]
	v_cndmask_b32_e64 v13, 0, 1, s[4:5]
	v_cmp_gt_f32_e32 vcc, s3, v6
	s_nop 1
	v_cndmask_b32_e64 v6, 0, 1, vcc
	v_add_u32_e32 v6, v8, v6
	v_add3_u32 v6, v6, v7, v9
	v_add3_u32 v6, v6, v10, v11
	v_add3_u32 v6, v6, v12, v13
	v_cmp_eq_u32_e32 vcc, 0, v6
	s_ff1_i32_b64 s98, vcc
	v_cmp_eq_u32_e32 vcc, 1, v6
	s_ff1_i32_b64 s99, vcc
	v_cmp_eq_u32_e32 vcc, 2, v6
	s_ff1_i32_b64 s100, vcc
	v_cmp_eq_u32_e32 vcc, 3, v6
	s_ff1_i32_b64 s101, vcc
	v_cmp_gt_u32_e32 vcc, 4, v6
	v_mov_b32_e32 v6, 0
	s_nop 0
	v_cndmask_b32_e32 v5, v245, v5, vcc
	v_ashrrev_i32_e32 v9, 31, v5
	v_sub_u32_e32 v8, 63, v230
	v_and_b32_e32 v9, 0x7fffffff, v9
	v_xor_b32_e32 v9, v5, v9
	s_nop 0
	v_readlane_b32 s23, v9, s98
	s_sub_i32 s22, 63, s98
	s_add_i32 s98, s98, 1
	v_readlane_b32 s21, v9, s98
	s_sub_i32 s20, 63, s98
	s_add_i32 s98, s98, 1
	v_cmp_gt_i64_e32 vcc, s[22:23], v[8:9]
	v_readlane_b32 s23, v9, s98
	s_sub_i32 s22, 63, s98
	s_add_i32 s98, s98, 1
	v_addc_co_u32_e32 v6, vcc, 0, v6, vcc
	v_cmp_gt_i64_e32 vcc, s[20:21], v[8:9]
	v_readlane_b32 s21, v9, s98
	s_sub_i32 s20, 63, s98
	s_add_i32 s98, s98, 1
	v_addc_co_u32_e32 v6, vcc, 0, v6, vcc
	v_cmp_gt_i64_e32 vcc, s[22:23], v[8:9]
	v_readlane_b32 s23, v9, s98
	s_sub_i32 s22, 63, s98
	s_add_i32 s98, s98, 1
	v_addc_co_u32_e32 v6, vcc, 0, v6, vcc
	v_cmp_gt_i64_e32 vcc, s[20:21], v[8:9]
	v_readlane_b32 s21, v9, s98
	s_sub_i32 s20, 63, s98
	s_add_i32 s98, s98, 1
	v_addc_co_u32_e32 v6, vcc, 0, v6, vcc
	v_cmp_gt_i64_e32 vcc, s[22:23], v[8:9]
	v_readlane_b32 s23, v9, s98
	s_sub_i32 s22, 63, s98
	s_add_i32 s98, s98, 1
	v_addc_co_u32_e32 v6, vcc, 0, v6, vcc
	v_cmp_gt_i64_e32 vcc, s[20:21], v[8:9]
	v_readlane_b32 s21, v9, s98
	s_sub_i32 s20, 63, s98
	s_nop 0
	v_addc_co_u32_e32 v6, vcc, 0, v6, vcc
	v_cmp_gt_i64_e32 vcc, s[22:23], v[8:9]
	v_readlane_b32 s23, v9, s99
	s_sub_i32 s22, 63, s99
	s_add_i32 s99, s99, 1
	v_addc_co_u32_e32 v6, vcc, 0, v6, vcc
	v_cmp_gt_i64_e32 vcc, s[20:21], v[8:9]
	v_readlane_b32 s21, v9, s99
	s_sub_i32 s20, 63, s99
	s_add_i32 s99, s99, 1
	v_addc_co_u32_e32 v6, vcc, 0, v6, vcc
	v_cmp_gt_i64_e32 vcc, s[22:23], v[8:9]
	v_readlane_b32 s23, v9, s99
	s_sub_i32 s22, 63, s99
	s_add_i32 s99, s99, 1
	v_addc_co_u32_e32 v6, vcc, 0, v6, vcc
	v_cmp_gt_i64_e32 vcc, s[20:21], v[8:9]
	v_readlane_b32 s21, v9, s99
	s_sub_i32 s20, 63, s99
	s_add_i32 s99, s99, 1
	v_addc_co_u32_e32 v6, vcc, 0, v6, vcc
	v_cmp_gt_i64_e32 vcc, s[22:23], v[8:9]
	v_readlane_b32 s23, v9, s99
	s_sub_i32 s22, 63, s99
	s_add_i32 s99, s99, 1
	v_addc_co_u32_e32 v6, vcc, 0, v6, vcc
	v_cmp_gt_i64_e32 vcc, s[20:21], v[8:9]
	v_readlane_b32 s21, v9, s99
	s_sub_i32 s20, 63, s99
	s_add_i32 s99, s99, 1
	v_addc_co_u32_e32 v6, vcc, 0, v6, vcc
	v_cmp_gt_i64_e32 vcc, s[22:23], v[8:9]
; __device__ __forceinline__ float wave_sum(float v) {
; #pragma unroll
;     for (int o = 1; o < 64; o <<= 1) v += __shfl_xor(v, o);
;     return v;
; __device__ __forceinline__ void phase_nrr(const Frame& F, const Args& a, int l, const bf16_t* XA, const float* g, const float* modl, unsigned char* XN8) {
;     ...
;             for (int e2 = 0; e2 < 64; ++e2) { const float v = __int_as_float(__builtin_amdgcn_readlane(__float_as_int(val), e2)); rank += (v > val || (v == val && e2 < lane)) ? 1 : 0; }
;             const bool sel = rank < TOPK;
;             const float ssum = wave_sum(sel ? sc : 0.f);
;             if (sel) { const int p = atomicAdd((int*)(hist + lane), 1); top_e[t * TOPK + rank] = lane; gate[t * TOPK + rank] = sc / ssum * 2.5f; lpos[t * TOPK + rank] = p; }
	v_readlane_b32 s23, v9, s99
	s_sub_i32 s22, 63, s99
	s_add_i32 s99, s99, 1
	v_addc_co_u32_e32 v6, vcc, 0, v6, vcc
	v_cmp_gt_i64_e32 vcc, s[20:21], v[8:9]
	v_readlane_b32 s21, v9, s99
	s_sub_i32 s20, 63, s99
	s_nop 0
	v_addc_co_u32_e32 v6, vcc, 0, v6, vcc
	v_cmp_gt_i64_e32 vcc, s[22:23], v[8:9]
	v_readlane_b32 s23, v9, s100
	s_sub_i32 s22, 63, s100
	s_add_i32 s100, s100, 1
	v_addc_co_u32_e32 v6, vcc, 0, v6, vcc
	v_cmp_gt_i64_e32 vcc, s[20:21], v[8:9]
	v_readlane_b32 s21, v9, s100
	s_sub_i32 s20, 63, s100
	s_add_i32 s100, s100, 1
	v_addc_co_u32_e32 v6, vcc, 0, v6, vcc
	v_cmp_gt_i64_e32 vcc, s[22:23], v[8:9]
	v_readlane_b32 s23, v9, s100
	s_sub_i32 s22, 63, s100
	s_add_i32 s100, s100, 1
	v_addc_co_u32_e32 v6, vcc, 0, v6, vcc
	v_cmp_gt_i64_e32 vcc, s[20:21], v[8:9]
	v_readlane_b32 s21, v9, s100
	s_sub_i32 s20, 63, s100
	s_add_i32 s100, s100, 1
	v_addc_co_u32_e32 v6, vcc, 0, v6, vcc
	v_cmp_gt_i64_e32 vcc, s[22:23], v[8:9]
	v_readlane_b32 s23, v9, s100
	s_sub_i32 s22, 63, s100
	s_add_i32 s100, s100, 1
	v_addc_co_u32_e32 v6, vcc, 0, v6, vcc
	v_cmp_gt_i64_e32 vcc, s[20:21], v[8:9]
	v_readlane_b32 s21, v9, s100
	s_sub_i32 s20, 63, s100
	s_add_i32 s100, s100, 1
	v_addc_co_u32_e32 v6, vcc, 0, v6, vcc
	v_cmp_gt_i64_e32 vcc, s[22:23], v[8:9]
	v_readlane_b32 s23, v9, s100
	s_sub_i32 s22, 63, s100
	s_add_i32 s100, s100, 1
	v_addc_co_u32_e32 v6, vcc, 0, v6, vcc
	v_cmp_gt_i64_e32 vcc, s[20:21], v[8:9]
	v_readlane_b32 s21, v9, s100
	s_sub_i32 s20, 63, s100
	s_nop 0
	v_addc_co_u32_e32 v6, vcc, 0, v6, vcc
	v_cmp_gt_i64_e32 vcc, s[22:23], v[8:9]
	v_readlane_b32 s23, v9, s101
	s_sub_i32 s22, 63, s101
	s_add_i32 s101, s101, 1
	v_addc_co_u32_e32 v6, vcc, 0, v6, vcc
	v_cmp_gt_i64_e32 vcc, s[20:21], v[8:9]
	v_readlane_b32 s21, v9, s101
	s_sub_i32 s20, 63, s101
	s_add_i32 s101, s101, 1
	v_addc_co_u32_e32 v6, vcc, 0, v6, vcc
	v_cmp_gt_i64_e32 vcc, s[22:23], v[8:9]
	v_readlane_b32 s23, v9, s101
	s_sub_i32 s22, 63, s101
	s_add_i32 s101, s101, 1
	v_addc_co_u32_e32 v6, vcc, 0, v6, vcc
	v_cmp_gt_i64_e32 vcc, s[20:21], v[8:9]
	v_readlane_b32 s21, v9, s101
	s_sub_i32 s20, 63, s101
	s_add_i32 s101, s101, 1
	v_addc_co_u32_e32 v6, vcc, 0, v6, vcc
	v_cmp_gt_i64_e32 vcc, s[22:23], v[8:9]
	v_readlane_b32 s23, v9, s101
	s_sub_i32 s22, 63, s101
	s_add_i32 s101, s101, 1
	v_addc_co_u32_e32 v6, vcc, 0, v6, vcc
	v_cmp_gt_i64_e32 vcc, s[20:21], v[8:9]
	v_readlane_b32 s21, v9, s101
	s_sub_i32 s20, 63, s101
	s_add_i32 s101, s101, 1
	v_addc_co_u32_e32 v6, vcc, 0, v6, vcc
	v_cmp_gt_i64_e32 vcc, s[22:23], v[8:9]
	v_readlane_b32 s23, v9, s101
	s_sub_i32 s22, 63, s101
	s_add_i32 s101, s101, 1
	v_addc_co_u32_e32 v6, vcc, 0, v6, vcc
	v_cmp_gt_i64_e32 vcc, s[20:21], v[8:9]
	v_readlane_b32 s21, v9, s101
	s_sub_i32 s20, 63, s101
	s_nop 0
	v_addc_co_u32_e32 v6, vcc, 0, v6, vcc
	v_cmp_gt_i64_e32 vcc, s[22:23], v[8:9]
	s_nop 1
	v_addc_co_u32_e32 v6, vcc, 0, v6, vcc
	v_cmp_gt_i64_e32 vcc, s[20:21], v[8:9]
	s_nop 1
	v_addc_co_u32_e32 v6, vcc, 0, v6, vcc
	v_cmp_gt_u32_e32 vcc, 6, v6
	s_nop 1
	v_cndmask_b32_e32 v5, 0, v2, vcc
	s_nop 1
	v_add_f32_dpp v5, v5, v5 quad_perm:[1,0,3,2] row_mask:0xf bank_mask:0xf
	s_nop 1
	v_add_f32_dpp v5, v5, v5 quad_perm:[2,3,0,1] row_mask:0xf bank_mask:0xf
	s_nop 1
	v_add_f32_dpp v5, v5, v5 row_half_mirror row_mask:0xf bank_mask:0xf
	s_nop 1
	v_add_f32_dpp v5, v5, v5 row_mirror row_mask:0xf bank_mask:0xf
	v_mov_b32_e32 v7, v5
	s_nop 1
	v_permlane16_swap_b32_e32 v7, v5
	s_waitcnt lgkmcnt(0)
	v_add_f32_e32 v5, v5, v7
	v_mov_b32_e32 v7, v5
	s_nop 1
	v_permlane32_swap_b32_e32 v7, v5
	s_and_saveexec_b64 s[2:3], vcc
	s_cbranch_execz .LBB0_1336
	s_waitcnt lgkmcnt(0)
	v_add_f32_e32 v5, v5, v7
	v_div_scale_f32 v11, s[4:5], v5, v5, v2
	v_add3_u32 v6, s50, 36, v6
	v_rcp_f32_e32 v12, v11
	v_ashrrev_i32_e32 v7, 31, v6
	v_lshlrev_b64 v[6:7], 2, v[6:7]
	v_lshl_add_u64 v[8:9], s[42:43], 0, v[6:7]
	ds_add_rtn_u32 v10, v227, v243
	global_store_dword v[8:9], v230, off
	v_fma_f32 v8, -v11, v12, 1.0
	v_fmac_f32_e32 v12, v8, v12
	v_div_scale_f32 v8, vcc, v2, v5, v2
	v_mul_f32_e32 v9, v8, v12
	v_fma_f32 v13, -v11, v9, v8
	v_fmac_f32_e32 v9, v13, v12
	v_fma_f32 v8, -v11, v9, v8
	v_div_fmas_f32 v8, v8, v12, v9
	v_div_fixup_f32 v2, v8, v5, v2
	v_mul_f32_e32 v2, 0x40200000, v2
	v_lshl_add_u64 v[8:9], s[44:45], 0, v[6:7]
	v_lshl_add_u64 v[6:7], s[46:47], 0, v[6:7]
	global_store_dword v[8:9], v2, off
	s_waitcnt lgkmcnt(0)
	global_store_dword v[6:7], v10, off
; __device__ __forceinline__ void phase_nrr(const Frame& F, const Args& a, int l, const bf16_t* XA, const float* g, const float* modl, unsigned char* XN8) {
;     ...
;         for (int i = 0; i < 8; ++i) { const int t = tb + i;
;             const float lg = Pl[(w * 8 + i) * NE + lane] + Pl[(64 + w * 8 + i) * NE + lane]; const float sc = 1.f / (1.f + __expf(-lg)); const float bb = sc + bias;
;             float m1 = bb; m1 = fmaxf(m1, __shfl_xor(m1, 1)); m1 = fmaxf(m1, __shfl_xor(m1, 2)); m1 = fmaxf(m1, __shfl_xor(m1, 4));
;             const unsigned long long eq = __ballot(bb == m1); const int gbase = lane & ~7; const unsigned grpmask = (unsigned)((eq >> gbase) & 0xffull);
;             const int first = gbase + __builtin_ctz(grpmask);
;             float m2 = (lane == first) ? -INFINITY : bb; m2 = fmaxf(m2, __shfl_xor(m2, 1)); m2 = fmaxf(m2, __shfl_xor(m2, 2)); m2 = fmaxf(m2, __shfl_xor(m2, 4));
;             const float gsum = m1 + m2; const int gq = lane >> 3;
;             int grank = 0;
; #pragma unroll
;             for (int g2 = 0; g2 < 8; ++g2) { const float v = __int_as_float(__builtin_amdgcn_readlane(__float_as_int(gsum), g2 * 8)); grank += (v > gsum || (v == gsum && g2 < gq)) ? 1 : 0; }
;             const bool keep = grank < 4; const float val = keep ? bb : -INFINITY;
;             int rank = 0;
; #pragma unroll 8
;             for (int e2 = 0; e2 < 64; ++e2) { const float v = __int_as_float(__builtin_amdgcn_readlane(__float_as_int(val), e2)); rank += (v > val || (v == val && e2 < lane)) ? 1 : 0; }
.LBB0_1336:
	s_or_b64 exec, exec, s[2:3]
	v_add_u32_e32 v2, s82, v226
	ds_read_b32 v2, v2
	ds_read_b32 v4, v4 offset:18176
	s_waitcnt lgkmcnt(0)
	v_add_f32_e32 v2, v2, v4
	v_mul_f32_e32 v2, 0xbfb8aa3b, v2
	v_exp_f32_e32 v2, v2
	s_nop 0
	v_add_f32_e32 v2, 1.0, v2
	v_div_scale_f32 v4, s[2:3], v2, v2, 1.0
	v_rcp_f32_e32 v5, v4
	v_div_scale_f32 v6, vcc, 1.0, v2, 1.0
	s_mov_b32 s2, 0
	v_fma_f32 v7, -v4, v5, 1.0
	v_fmac_f32_e32 v5, v7, v5
	v_mul_f32_e32 v7, v6, v5
	v_fma_f32 v8, -v4, v7, v6
	v_fmac_f32_e32 v7, v8, v5
	v_fma_f32 v4, -v4, v7, v6
	v_div_fmas_f32 v4, v4, v5, v7
	v_div_fixup_f32 v2, v4, v2, 1.0
	v_add_f32_e32 v3, v3, v2
	s_nop 1
	s_waitcnt lgkmcnt(0)
	v_max_f32_dpp v4, v3, v3 quad_perm:[1,0,3,2] row_mask:0xf bank_mask:0xf
	s_nop 1
	s_waitcnt lgkmcnt(0)
	v_max_f32_dpp v4, v4, v4 quad_perm:[2,3,0,1] row_mask:0xf bank_mask:0xf
	s_nop 1
	s_waitcnt lgkmcnt(0)
	v_max_f32_dpp v6, v4, v4 row_half_mirror row_mask:0xf bank_mask:0xf
	v_cmp_eq_f32_e32 vcc, v3, v6
	s_nop 1
	v_lshrrev_b64 v[4:5], v200, vcc
	v_ffbl_b32_sdwa v4, v4 dst_sel:DWORD dst_unused:UNUSED_PAD src0_sel:BYTE_0
	v_add_u32_e32 v4, v4, v200
	v_cmp_ne_u32_e32 vcc, v230, v4
	s_nop 1
	v_cndmask_b32_e32 v4, v245, v3, vcc
	s_nop 1
	s_waitcnt lgkmcnt(0)
	v_max_f32_dpp v4, v4, v4 quad_perm:[1,0,3,2] row_mask:0xf bank_mask:0xf
	s_nop 1
	s_waitcnt lgkmcnt(0)
	v_max_f32_dpp v4, v4, v4 quad_perm:[2,3,0,1] row_mask:0xf bank_mask:0xf
	s_nop 1
	s_waitcnt lgkmcnt(0)
	v_max_f32_dpp v4, v4, v4 row_half_mirror row_mask:0xf bank_mask:0xf
	v_add_f32_e32 v4, v6, v4
	s_nop 0
	v_readlane_b32 s3, v4, 0
	v_readlane_b32 s4, v4, 8
	v_readlane_b32 s5, v4, 16
	v_cmp_eq_f32_e64 s[20:21], s3, v4
	v_cmp_gt_f32_e32 vcc, s3, v4
	v_cmp_gt_f32_e64 s[22:23], s4, v4
	v_cmp_eq_f32_e64 s[24:25], s4, v4
	v_cmp_gt_f32_e64 s[26:27], s5, v4
	v_cmp_eq_f32_e64 s[28:29], s5, v4
	s_and_b64 s[4:5], s[0:1], s[20:21]
	v_readlane_b32 s34, v4, 24
	s_and_b64 s[20:21], s[6:7], s[24:25]
	s_or_b64 s[4:5], vcc, s[4:5]
	v_readlane_b32 s40, v4, 32
	v_cmp_gt_f32_e64 s[30:31], s34, v4
	v_cmp_eq_f32_e64 s[34:35], s34, v4
	s_and_b64 s[24:25], s[8:9], s[28:29]
	v_cndmask_b32_e64 v5, 0, 1, s[4:5]
	s_or_b64 s[4:5], s[22:23], s[20:21]
	v_cmp_gt_f32_e64 s[36:37], s40, v4
	v_cmp_eq_f32_e64 s[40:41], s40, v4
	s_and_b64 s[28:29], s[10:11], s[34:35]
	v_cndmask_b32_e64 v6, 0, 1, s[4:5]
	s_or_b64 s[4:5], s[26:27], s[24:25]
	v_readlane_b32 s54, v4, 40
	s_and_b64 s[34:35], s[12:13], s[40:41]
	v_cndmask_b32_e64 v7, 0, 1, s[4:5]
	s_or_b64 s[4:5], s[30:31], s[28:29]
	v_cndmask_b32_e64 v8, 0, 1, s[4:5]
	s_or_b64 s[4:5], s[36:37], s[34:35]
	v_cmp_eq_f32_e64 s[20:21], s54, v4
	v_cndmask_b32_e64 v9, 0, 1, s[4:5]
	v_cmp_gt_f32_e32 vcc, s54, v4
	s_and_b64 s[4:5], s[14:15], s[20:21]
	v_readlane_b32 s3, v4, 48
	s_or_b64 s[4:5], vcc, s[4:5]
	v_cndmask_b32_e64 v10, 0, 1, s[4:5]
	v_cmp_eq_f32_e64 s[20:21], s3, v4
	v_cmp_gt_f32_e32 vcc, s3, v4
	s_and_b64 s[4:5], s[16:17], s[20:21]
	v_readlane_b32 s3, v4, 56
	s_or_b64 s[4:5], vcc, s[4:5]
	v_cndmask_b32_e64 v11, 0, 1, s[4:5]
	v_cmp_gt_f32_e32 vcc, s3, v4
	s_nop 1
	v_cndmask_b32_e64 v4, 0, 1, vcc
	v_add_u32_e32 v4, v6, v4
	v_add3_u32 v4, v4, v5, v7
	v_add3_u32 v4, v4, v8, v9
	v_add3_u32 v4, v4, v10, v11
	v_cmp_eq_u32_e32 vcc, 0, v4
	s_ff1_i32_b64 s98, vcc
	v_cmp_eq_u32_e32 vcc, 1, v4
	s_ff1_i32_b64 s99, vcc
	v_cmp_eq_u32_e32 vcc, 2, v4
	s_ff1_i32_b64 s100, vcc
	v_cmp_eq_u32_e32 vcc, 3, v4
	s_ff1_i32_b64 s101, vcc
	v_cmp_gt_u32_e32 vcc, 4, v4
	v_mov_b32_e32 v4, 0
	s_nop 0
	v_cndmask_b32_e32 v3, v245, v3, vcc
	v_ashrrev_i32_e32 v9, 31, v3
	v_sub_u32_e32 v8, 63, v230
	v_and_b32_e32 v9, 0x7fffffff, v9
	v_xor_b32_e32 v9, v3, v9
	s_nop 0
	v_readlane_b32 s23, v9, s98
	s_sub_i32 s22, 63, s98
	s_add_i32 s98, s98, 1
	v_readlane_b32 s21, v9, s98
	s_sub_i32 s20, 63, s98
	s_add_i32 s98, s98, 1
	v_cmp_gt_i64_e32 vcc, s[22:23], v[8:9]
	v_readlane_b32 s23, v9, s98
	s_sub_i32 s22, 63, s98
	s_add_i32 s98, s98, 1
	v_addc_co_u32_e32 v4, vcc, 0, v4, vcc
	v_cmp_gt_i64_e32 vcc, s[20:21], v[8:9]
	v_readlane_b32 s21, v9, s98
	s_sub_i32 s20, 63, s98
	s_add_i32 s98, s98, 1
	v_addc_co_u32_e32 v4, vcc, 0, v4, vcc
	v_cmp_gt_i64_e32 vcc, s[22:23], v[8:9]
	v_readlane_b32 s23, v9, s98
	s_sub_i32 s22, 63, s98
	s_add_i32 s98, s98, 1
	v_addc_co_u32_e32 v4, vcc, 0, v4, vcc
	v_cmp_gt_i64_e32 vcc, s[20:21], v[8:9]
	v_readlane_b32 s21, v9, s98
	s_sub_i32 s20, 63, s98
	s_add_i32 s98, s98, 1
	v_addc_co_u32_e32 v4, vcc, 0, v4, vcc
	v_cmp_gt_i64_e32 vcc, s[22:23], v[8:9]
	v_readlane_b32 s23, v9, s98
	s_sub_i32 s22, 63, s98
	s_add_i32 s98, s98, 1
	v_addc_co_u32_e32 v4, vcc, 0, v4, vcc
	v_cmp_gt_i64_e32 vcc, s[20:21], v[8:9]
	v_readlane_b32 s21, v9, s98
	s_sub_i32 s20, 63, s98
	s_nop 0
	v_addc_co_u32_e32 v4, vcc, 0, v4, vcc
	v_cmp_gt_i64_e32 vcc, s[22:23], v[8:9]
	v_readlane_b32 s23, v9, s99
	s_sub_i32 s22, 63, s99
	s_add_i32 s99, s99, 1
	v_addc_co_u32_e32 v4, vcc, 0, v4, vcc
	v_cmp_gt_i64_e32 vcc, s[20:21], v[8:9]
	v_readlane_b32 s21, v9, s99
	s_sub_i32 s20, 63, s99
	s_add_i32 s99, s99, 1
	v_addc_co_u32_e32 v4, vcc, 0, v4, vcc
; __device__ __forceinline__ float wave_sum(float v) {
; #pragma unroll
;     for (int o = 1; o < 64; o <<= 1) v += __shfl_xor(v, o);
;     return v;
; __device__ __forceinline__ void phase_nrr(const Frame& F, const Args& a, int l, const bf16_t* XA, const float* g, const float* modl, unsigned char* XN8) {
;     ...
;             for (int e2 = 0; e2 < 64; ++e2) { const float v = __int_as_float(__builtin_amdgcn_readlane(__float_as_int(val), e2)); rank += (v > val || (v == val && e2 < lane)) ? 1 : 0; }
;             const bool sel = rank < TOPK;
;             const float ssum = wave_sum(sel ? sc : 0.f);
;             if (sel) { const int p = atomicAdd((int*)(hist + lane), 1); top_e[t * TOPK + rank] = lane; gate[t * TOPK + rank] = sc / ssum * 2.5f; lpos[t * TOPK + rank] = p; }
	v_cmp_gt_i64_e32 vcc, s[22:23], v[8:9]
	v_readlane_b32 s23, v9, s99
	s_sub_i32 s22, 63, s99
	s_add_i32 s99, s99, 1
	v_addc_co_u32_e32 v4, vcc, 0, v4, vcc
	v_cmp_gt_i64_e32 vcc, s[20:21], v[8:9]
	v_readlane_b32 s21, v9, s99
	s_sub_i32 s20, 63, s99
	s_add_i32 s99, s99, 1
	v_addc_co_u32_e32 v4, vcc, 0, v4, vcc
	v_cmp_gt_i64_e32 vcc, s[22:23], v[8:9]
	v_readlane_b32 s23, v9, s99
	s_sub_i32 s22, 63, s99
	s_add_i32 s99, s99, 1
	v_addc_co_u32_e32 v4, vcc, 0, v4, vcc
	v_cmp_gt_i64_e32 vcc, s[20:21], v[8:9]
	v_readlane_b32 s21, v9, s99
	s_sub_i32 s20, 63, s99
	s_add_i32 s99, s99, 1
	v_addc_co_u32_e32 v4, vcc, 0, v4, vcc
	v_cmp_gt_i64_e32 vcc, s[22:23], v[8:9]
	v_readlane_b32 s23, v9, s99
	s_sub_i32 s22, 63, s99
	s_add_i32 s99, s99, 1
	v_addc_co_u32_e32 v4, vcc, 0, v4, vcc
	v_cmp_gt_i64_e32 vcc, s[20:21], v[8:9]
	v_readlane_b32 s21, v9, s99
	s_sub_i32 s20, 63, s99
	s_nop 0
	v_addc_co_u32_e32 v4, vcc, 0, v4, vcc
	v_cmp_gt_i64_e32 vcc, s[22:23], v[8:9]
	v_readlane_b32 s23, v9, s100
	s_sub_i32 s22, 63, s100
	s_add_i32 s100, s100, 1
	v_addc_co_u32_e32 v4, vcc, 0, v4, vcc
	v_cmp_gt_i64_e32 vcc, s[20:21], v[8:9]
	v_readlane_b32 s21, v9, s100
	s_sub_i32 s20, 63, s100
	s_add_i32 s100, s100, 1
	v_addc_co_u32_e32 v4, vcc, 0, v4, vcc
	v_cmp_gt_i64_e32 vcc, s[22:23], v[8:9]
	v_readlane_b32 s23, v9, s100
	s_sub_i32 s22, 63, s100
	s_add_i32 s100, s100, 1
	v_addc_co_u32_e32 v4, vcc, 0, v4, vcc
	v_cmp_gt_i64_e32 vcc, s[20:21], v[8:9]
	v_readlane_b32 s21, v9, s100
	s_sub_i32 s20, 63, s100
	s_add_i32 s100, s100, 1
	v_addc_co_u32_e32 v4, vcc, 0, v4, vcc
	v_cmp_gt_i64_e32 vcc, s[22:23], v[8:9]
	v_readlane_b32 s23, v9, s100
	s_sub_i32 s22, 63, s100
	s_add_i32 s100, s100, 1
	v_addc_co_u32_e32 v4, vcc, 0, v4, vcc
	v_cmp_gt_i64_e32 vcc, s[20:21], v[8:9]
	v_readlane_b32 s21, v9, s100
	s_sub_i32 s20, 63, s100
	s_add_i32 s100, s100, 1
	v_addc_co_u32_e32 v4, vcc, 0, v4, vcc
	v_cmp_gt_i64_e32 vcc, s[22:23], v[8:9]
	v_readlane_b32 s23, v9, s100
	s_sub_i32 s22, 63, s100
	s_add_i32 s100, s100, 1
	v_addc_co_u32_e32 v4, vcc, 0, v4, vcc
	v_cmp_gt_i64_e32 vcc, s[20:21], v[8:9]
	v_readlane_b32 s21, v9, s100
	s_sub_i32 s20, 63, s100
	s_nop 0
	v_addc_co_u32_e32 v4, vcc, 0, v4, vcc
	v_cmp_gt_i64_e32 vcc, s[22:23], v[8:9]
	v_readlane_b32 s23, v9, s101
	s_sub_i32 s22, 63, s101
	s_add_i32 s101, s101, 1
	v_addc_co_u32_e32 v4, vcc, 0, v4, vcc
	v_cmp_gt_i64_e32 vcc, s[20:21], v[8:9]
	v_readlane_b32 s21, v9, s101
	s_sub_i32 s20, 63, s101
	s_add_i32 s101, s101, 1
	v_addc_co_u32_e32 v4, vcc, 0, v4, vcc
	v_cmp_gt_i64_e32 vcc, s[22:23], v[8:9]
	v_readlane_b32 s23, v9, s101
	s_sub_i32 s22, 63, s101
	s_add_i32 s101, s101, 1
	v_addc_co_u32_e32 v4, vcc, 0, v4, vcc
	v_cmp_gt_i64_e32 vcc, s[20:21], v[8:9]
	v_readlane_b32 s21, v9, s101
	s_sub_i32 s20, 63, s101
	s_add_i32 s101, s101, 1
	v_addc_co_u32_e32 v4, vcc, 0, v4, vcc
	v_cmp_gt_i64_e32 vcc, s[22:23], v[8:9]
	v_readlane_b32 s23, v9, s101
	s_sub_i32 s22, 63, s101
	s_add_i32 s101, s101, 1
	v_addc_co_u32_e32 v4, vcc, 0, v4, vcc
	v_cmp_gt_i64_e32 vcc, s[20:21], v[8:9]
	v_readlane_b32 s21, v9, s101
	s_sub_i32 s20, 63, s101
	s_add_i32 s101, s101, 1
	v_addc_co_u32_e32 v4, vcc, 0, v4, vcc
	v_cmp_gt_i64_e32 vcc, s[22:23], v[8:9]
	v_readlane_b32 s23, v9, s101
	s_sub_i32 s22, 63, s101
	s_add_i32 s101, s101, 1
	v_addc_co_u32_e32 v4, vcc, 0, v4, vcc
	v_cmp_gt_i64_e32 vcc, s[20:21], v[8:9]
	v_readlane_b32 s21, v9, s101
	s_sub_i32 s20, 63, s101
	s_nop 0
	v_addc_co_u32_e32 v4, vcc, 0, v4, vcc
	v_cmp_gt_i64_e32 vcc, s[22:23], v[8:9]
	s_nop 1
	v_addc_co_u32_e32 v4, vcc, 0, v4, vcc
	v_cmp_gt_i64_e32 vcc, s[20:21], v[8:9]
	s_nop 1
	v_addc_co_u32_e32 v4, vcc, 0, v4, vcc
	v_cmp_gt_u32_e32 vcc, 6, v4
	s_nop 1
	v_cndmask_b32_e32 v3, 0, v2, vcc
	s_nop 1
	v_add_f32_dpp v3, v3, v3 quad_perm:[1,0,3,2] row_mask:0xf bank_mask:0xf
	s_nop 1
	v_add_f32_dpp v3, v3, v3 quad_perm:[2,3,0,1] row_mask:0xf bank_mask:0xf
	s_nop 1
	v_add_f32_dpp v3, v3, v3 row_half_mirror row_mask:0xf bank_mask:0xf
	s_nop 1
	v_add_f32_dpp v3, v3, v3 row_mirror row_mask:0xf bank_mask:0xf
	v_mov_b32_e32 v5, v3
	s_nop 1
	v_permlane16_swap_b32_e32 v5, v3
	s_waitcnt lgkmcnt(0)
	v_add_f32_e32 v3, v3, v5
	v_mov_b32_e32 v5, v3
	s_nop 1
	v_permlane32_swap_b32_e32 v5, v3
	s_and_saveexec_b64 s[2:3], vcc
	s_cbranch_execz .LBB0_1340
	s_waitcnt lgkmcnt(0)
	v_add_f32_e32 v3, v3, v5
	v_div_scale_f32 v9, s[4:5], v3, v3, v2
	v_add3_u32 v4, s50, 42, v4
	v_rcp_f32_e32 v10, v9
	v_ashrrev_i32_e32 v5, 31, v4
	v_lshlrev_b64 v[4:5], 2, v[4:5]
	v_lshl_add_u64 v[6:7], s[42:43], 0, v[4:5]
	ds_add_rtn_u32 v8, v227, v243
	global_store_dword v[6:7], v230, off
	v_fma_f32 v6, -v9, v10, 1.0
	v_fmac_f32_e32 v10, v6, v10
	v_div_scale_f32 v6, vcc, v2, v3, v2
	v_mul_f32_e32 v7, v6, v10
	v_fma_f32 v11, -v9, v7, v6
	v_fmac_f32_e32 v7, v11, v10
	v_fma_f32 v6, -v9, v7, v6
	v_div_fmas_f32 v6, v6, v10, v7
	v_div_fixup_f32 v2, v6, v3, v2
	v_mul_f32_e32 v6, 0x40200000, v2
	v_lshl_add_u64 v[2:3], s[44:45], 0, v[4:5]
	global_store_dword v[2:3], v6, off
	v_lshl_add_u64 v[2:3], s[46:47], 0, v[4:5]
	s_waitcnt lgkmcnt(0)
	global_store_dword v[2:3], v8, off
